# v14 + P1 GEMM epilogues: packed f32 VALU ops (v_pk_mul/fma_f32) split into single f32 ops (bit-identical)
# baseline (speedup 1.0000x reference)
; __device__ __forceinline__ f32x2 gelu_pk(f32x2 v) {
;     const f32x2 av = __builtin_elementwise_abs(v), d = av * 0.2316418882f + 1.0f;
;     f32x2 t; t.x = __builtin_amdgcn_rcpf(d.x); t.y = __builtin_amdgcn_rcpf(d.y);
;     f32x2 q = t * 0.5307027145f + (-0.7265760135f); q = q * t + 0.7107068705f; q = q * t + (-0.142248368f); q = q * t + 0.127414796f; q = q * t;
;     const f32x2 s = (v * v) * (-0.72134752044f);
;     f32x2 e; e.x = __builtin_amdgcn_exp2f(s.x); e.y = __builtin_amdgcn_exp2f(s.y);
;     const f32x2 m = v * (q * e), r = v - m;
;     f32x2 o; o.x = v.x < 0.f ? m.x : r.x; o.y = v.y < 0.f ? m.y : r.y; return o;
;     __device__ __forceinline__ void operator()(const f32x4 (&acc)[2][2][4][2], const Unit& u, int wr, int wc, int fr, int fq) const {
;         const int row0 = u.pm * BM + wr * 64 + fr; const int col0 = u.pn * BM + wc * 32 + 8 * fq;
;         const bool act = u.pn < gelu_tiles;
;         f32x4 cv[2][2];
; #pragma unroll
;         for (int bj = 0; bj < 2; ++bj)
; #pragma unroll
;             for (int n = 0; n < 2; ++n) cv[bj][n] = *(const f32x4*)(cs + col0 + bj * HALF + 4 * n);
;         float rsv[2][4];
; #pragma unroll
;         for (int ai = 0; ai < 2; ++ai)
; #pragma unroll
;             for (int m = 0; m < 4; ++m) rsv[ai][m] = rs[row0 + ai * HALF + m * 16];
; #pragma unroll
;         for (int ai = 0; ai < 2; ++ai)
; #pragma unroll
;             for (int m = 0; m < 4; ++m) { const int row = row0 + ai * HALF + m * 16; const float rsc = rsv[ai][m]; bf16_t* rowp = O + (size_t)row * ldc + col0;
; #pragma unroll
;                 for (int bj = 0; bj < 2; ++bj) { const i32x4 a0 = __builtin_bit_cast(i32x4, acc[ai][bj][m][0]), a1 = __builtin_bit_cast(i32x4, acc[ai][bj][m][1]);
;                     f32x4 v0 = (f32x4){(float)a0[0], (float)a0[1], (float)a0[2], (float)a0[3]} * rsc * cv[bj][0], v1 = (f32x4){(float)a1[0], (float)a1[1], (float)a1[2], (float)a1[3]} * rsc * cv[bj][1];
;                     if (act) { f32x2 a = gelu_pk((f32x2){v0[0], v0[1]}), b = gelu_pk((f32x2){v0[2], v0[3]}), c = gelu_pk((f32x2){v1[0], v1[1]}), d = gelu_pk((f32x2){v1[2], v1[3]});
;                         v0 = (f32x4){a.x, a.y, b.x, b.y}; v1 = (f32x4){c.x, c.y, d.x, d.y}; }
.LBB0_279:
	v_lshl_add_u32 v172, s4, 8, v200
	v_lshl_or_b32 v170, s2, 8, v202
	v_or_b32_e32 v190, 16, v172
	v_or_b32_e32 v186, 32, v172
	v_or_b32_e32 v182, 48, v172
	v_ashrrev_i32_e32 v171, 31, v170
	v_ashrrev_i32_e32 v173, 31, v172
	v_ashrrev_i32_e32 v191, 31, v190
	v_ashrrev_i32_e32 v187, 31, v186
	v_ashrrev_i32_e32 v183, 31, v182
	v_lshl_add_u64 v[30:31], v[170:171], 2, s[12:13]
	v_lshl_add_u64 v[168:169], v[172:173], 2, s[64:65]
	v_lshl_add_u64 v[174:175], v[190:191], 2, s[64:65]
	v_lshl_add_u64 v[176:177], v[186:187], 2, s[64:65]
	v_lshl_add_u64 v[178:179], v[182:183], 2, s[64:65]
	global_load_dwordx4 v[34:37], v[30:31], off offset:16
	global_load_dwordx4 v[38:41], v[30:31], off
	global_load_dwordx4 v[22:25], v[30:31], off offset:528
	s_nop 0
	global_load_dwordx4 v[30:33], v[30:31], off offset:512
	v_cvt_f32_i32_e32 v145, v145
	global_load_dword v192, v[168:169], off
	global_load_dword v188, v[174:175], off
	global_load_dword v184, v[176:177], off
	global_load_dword v180, v[178:179], off
	s_nop 0
	global_load_dword v178, v[168:169], off offset:512
	global_load_dword v176, v[168:169], off offset:576
	global_load_dword v174, v[168:169], off offset:640
	s_nop 0
	global_load_dword v168, v[168:169], off offset:704
	v_cvt_f32_i32_e32 v144, v144
	v_cvt_f32_i32_e32 v143, v143
	v_cvt_f32_i32_e32 v142, v142
	v_cvt_f32_i32_e32 v141, v141
	v_cvt_f32_i32_e32 v140, v140
	v_cvt_f32_i32_e32 v139, v139
	v_cvt_f32_i32_e32 v138, v138
	s_cmp_lt_i32 s2, 8
	s_cselect_b64 s[42:43], -1, 0
	s_cmp_gt_i32 s2, 7
	s_waitcnt vmcnt(0)
	v_mul_f32_e32 v142, v192, v142
	v_mul_f32_e32 v143, v192, v143
	v_mul_f32_e32 v144, v192, v144
	v_mul_f32_e32 v145, v192, v145
	v_mul_f32_e32 v138, v192, v138
	v_mul_f32_e32 v139, v192, v139
	v_mul_f32_e32 v194, v192, v140
	v_mul_f32_e32 v195, v192, v141
	v_mul_f32_e32 v140, v40, v144
	v_mul_f32_e32 v141, v41, v145
	v_mul_f32_e32 v144, v38, v142
	v_mul_f32_e32 v145, v39, v143
	v_mul_f32_e32 v142, v36, v194
	v_mul_f32_e32 v143, v37, v195
	v_mul_f32_e32 v194, v34, v138
	v_mul_f32_e32 v195, v35, v139
	s_cbranch_scc1 .LBB0_281
	v_and_b32_e32 v139, 0x7fffffff, v145
	v_and_b32_e32 v138, 0x7fffffff, v144
	v_fma_f32 v138, v138, s18, 1.0
	v_fma_f32 v139, v139, s18, 1.0
	v_mov_b64_e32 v[206:207], s[22:23]
	v_rcp_f32_e32 v138, v138
	v_rcp_f32_e32 v139, v139
	v_mul_f32_e32 v210, v144, v144
	v_mul_f32_e32 v211, v145, v145
	v_cmp_gt_f32_e32 vcc, 0, v144
	v_mul_f32_e32 v210, s30, v210
	v_mul_f32_e32 v211, s30, v211
	v_fma_f32 v208, v138, s20, v206
	v_fma_f32 v209, v139, s20, v206
	v_exp_f32_e32 v210, v210
	v_fma_f32 v208, v138, v208, s24
	v_fma_f32 v209, v139, v209, s24
	v_exp_f32_e32 v211, v211
	v_fma_f32 v208, v138, v208, s26
	v_fma_f32 v209, v139, v209, s26
	s_nop 0
	v_fma_f32 v208, v138, v208, s28
	v_fma_f32 v209, v139, v209, s28
	s_nop 0
	v_mul_f32_e32 v138, v138, v208
	v_mul_f32_e32 v139, v139, v209
	v_mul_f32_e32 v208, v140, v140
	v_mul_f32_e32 v209, v141, v141
	v_mul_f32_e32 v138, v210, v138
	v_mul_f32_e32 v139, v211, v139
	v_mul_f32_e32 v208, s30, v208
	v_mul_f32_e32 v209, s30, v209
	v_mul_f32_e32 v210, v144, v138
	v_mul_f32_e32 v211, v145, v139
	v_fma_f32 v138, -v144, v138, v144
	v_fma_f32 v139, -v145, v139, v145
	v_exp_f32_e32 v208, v208
	v_cndmask_b32_e32 v144, v138, v210, vcc
	v_cmp_gt_f32_e32 vcc, 0, v145
	v_and_b32_e32 v138, 0x7fffffff, v140
	v_exp_f32_e32 v209, v209
	v_cndmask_b32_e32 v145, v139, v211, vcc
	v_and_b32_e32 v139, 0x7fffffff, v141
	v_fma_f32 v138, v138, s18, 1.0
	v_fma_f32 v139, v139, s18, 1.0
	v_cmp_gt_f32_e32 vcc, 0, v140
	v_rcp_f32_e32 v138, v138
	v_rcp_f32_e32 v139, v139
	s_nop 0
	v_fma_f32 v210, v138, s20, v206
	v_fma_f32 v211, v139, s20, v206
	s_nop 0
	v_fma_f32 v210, v138, v210, s24
	v_fma_f32 v211, v139, v211, s24
	s_nop 0
	v_fma_f32 v210, v138, v210, s26
	v_fma_f32 v211, v139, v211, s26
	s_nop 0
	v_fma_f32 v210, v138, v210, s28
	v_fma_f32 v211, v139, v211, s28
	s_nop 0
	v_mul_f32_e32 v138, v138, v210
	v_mul_f32_e32 v139, v139, v211
	v_mul_f32_e32 v210, v194, v194
	v_mul_f32_e32 v211, v195, v195
	v_mul_f32_e32 v138, v208, v138
	v_mul_f32_e32 v139, v209, v139
	v_mul_f32_e32 v210, s30, v210
	v_mul_f32_e32 v211, s30, v211
	v_mul_f32_e32 v208, v140, v138
	v_mul_f32_e32 v209, v141, v139
	v_fma_f32 v138, -v140, v138, v140
	v_fma_f32 v139, -v141, v139, v141
	v_exp_f32_e32 v210, v210
	v_cndmask_b32_e32 v140, v138, v208, vcc
	v_cmp_gt_f32_e32 vcc, 0, v141
	v_and_b32_e32 v138, 0x7fffffff, v194
	v_exp_f32_e32 v211, v211
	v_cndmask_b32_e32 v141, v139, v209, vcc
	v_and_b32_e32 v139, 0x7fffffff, v195
	v_fma_f32 v138, v138, s18, 1.0
	v_fma_f32 v139, v139, s18, 1.0
	v_cmp_gt_f32_e32 vcc, 0, v194
	v_rcp_f32_e32 v138, v138
	v_rcp_f32_e32 v139, v139
	s_nop 0
	v_fma_f32 v208, v138, s20, v206
	v_fma_f32 v209, v139, s20, v206
	s_nop 0
	v_fma_f32 v208, v138, v208, s24
	v_fma_f32 v209, v139, v209, s24
	s_nop 0
	v_fma_f32 v208, v138, v208, s26
	v_fma_f32 v209, v139, v209, s26
	s_nop 0
	v_fma_f32 v208, v138, v208, s28
	v_fma_f32 v209, v139, v209, s28
	s_nop 0
	v_mul_f32_e32 v138, v138, v208
	v_mul_f32_e32 v139, v139, v209
	v_mul_f32_e32 v208, v142, v142
	v_mul_f32_e32 v209, v143, v143
	v_mul_f32_e32 v138, v210, v138
	v_mul_f32_e32 v139, v211, v139
	s_nop 0
	v_mul_f32_e32 v210, v194, v138
	v_mul_f32_e32 v211, v195, v139
	v_fma_f32 v138, -v194, v138, v194
	v_fma_f32 v139, -v195, v139, v195
	s_nop 0
	v_cndmask_b32_e32 v194, v138, v210, vcc
	v_cmp_gt_f32_e32 vcc, 0, v195
	v_and_b32_e32 v138, 0x7fffffff, v142
	s_nop 0
	v_cndmask_b32_e32 v195, v139, v211, vcc
	v_and_b32_e32 v139, 0x7fffffff, v143
	v_fma_f32 v138, v138, s18, 1.0
	v_fma_f32 v139, v139, s18, 1.0
	v_cmp_gt_f32_e32 vcc, 0, v142
	v_rcp_f32_e32 v138, v138
	v_rcp_f32_e32 v139, v139
	s_nop 0
	v_fma_f32 v207, v139, s20, v206
	v_fma_f32 v206, v138, s20, v206
	s_nop 0
	v_fma_f32 v206, v138, v206, s24
	v_fma_f32 v207, v139, v207, s24
	s_nop 0
	v_fma_f32 v206, v138, v206, s26
	v_fma_f32 v207, v139, v207, s26
	s_nop 0
	v_fma_f32 v206, v138, v206, s28
	v_fma_f32 v207, v139, v207, s28
	s_nop 0
	v_mul_f32_e32 v138, v138, v206
	v_mul_f32_e32 v139, v139, v207
	v_mul_f32_e32 v206, s30, v208
	v_mul_f32_e32 v207, s30, v209
	s_nop 0
	v_exp_f32_e32 v206, v206
	v_exp_f32_e32 v207, v207
	s_nop 0
	v_mul_f32_e32 v138, v206, v138
	v_mul_f32_e32 v139, v207, v139
	s_nop 0
	v_mul_f32_e32 v206, v142, v138
	v_mul_f32_e32 v207, v143, v139
	v_fma_f32 v138, -v142, v138, v142
	v_fma_f32 v139, -v143, v139, v143
	s_nop 0
	v_cndmask_b32_e32 v142, v138, v206, vcc
	v_cmp_gt_f32_e32 vcc, 0, v143
	s_nop 1
	v_cndmask_b32_e32 v143, v139, v207, vcc
; __device__ __forceinline__ unsigned cvt_pk_bf16(float lo, float hi) { unsigned r; asm volatile("v_cvt_pk_bf16_f32 %0, %1, %2" : "=v"(r) : "v"(lo), "v"(hi)); return r; }
; __device__ __forceinline__ f32x2 gelu_pk(f32x2 v) {
;     const f32x2 av = __builtin_elementwise_abs(v), d = av * 0.2316418882f + 1.0f;
;     f32x2 t; t.x = __builtin_amdgcn_rcpf(d.x); t.y = __builtin_amdgcn_rcpf(d.y);
;     f32x2 q = t * 0.5307027145f + (-0.7265760135f); q = q * t + 0.7107068705f; q = q * t + (-0.142248368f); q = q * t + 0.127414796f; q = q * t;
;     const f32x2 s = (v * v) * (-0.72134752044f);
;     f32x2 e; e.x = __builtin_amdgcn_exp2f(s.x); e.y = __builtin_amdgcn_exp2f(s.y);
;     const f32x2 m = v * (q * e), r = v - m;
;     f32x2 o; o.x = v.x < 0.f ? m.x : r.x; o.y = v.y < 0.f ? m.y : r.y; return o;
;     __device__ __forceinline__ void operator()(const f32x4 (&acc)[2][2][4][2], const Unit& u, int wr, int wc, int fr, int fq) const {
;     ...
;             for (int m = 0; m < 4; ++m) { const int row = row0 + ai * HALF + m * 16; const float rsc = rsv[ai][m]; bf16_t* rowp = O + (size_t)row * ldc + col0;
; #pragma unroll
;                 for (int bj = 0; bj < 2; ++bj) { const i32x4 a0 = __builtin_bit_cast(i32x4, acc[ai][bj][m][0]), a1 = __builtin_bit_cast(i32x4, acc[ai][bj][m][1]);
;                     f32x4 v0 = (f32x4){(float)a0[0], (float)a0[1], (float)a0[2], (float)a0[3]} * rsc * cv[bj][0], v1 = (f32x4){(float)a1[0], (float)a1[1], (float)a1[2], (float)a1[3]} * rsc * cv[bj][1];
;                     if (act) { f32x2 a = gelu_pk((f32x2){v0[0], v0[1]}), b = gelu_pk((f32x2){v0[2], v0[3]}), c = gelu_pk((f32x2){v1[0], v1[1]}), d = gelu_pk((f32x2){v1[2], v1[3]});
;                         v0 = (f32x4){a.x, a.y, b.x, b.y}; v1 = (f32x4){c.x, c.y, d.x, d.y}; }
;                     u32x4 w; w.x = cvt_pk_bf16(v0[0], v0[1]); w.y = cvt_pk_bf16(v0[2], v0[3]); w.z = cvt_pk_bf16(v1[0], v1[1]); w.w = cvt_pk_bf16(v1[2], v1[3]);
;                     if (nt) __builtin_nontemporal_store(w, (u32x4*)(rowp + bj * HALF)); else *(u32x4*)(rowp + bj * HALF) = w; } }
.LBB0_281:
	v_cvt_f32_i32_e32 v137, v137
	v_cvt_f32_i32_e32 v136, v136
	v_cvt_pk_bf16_f32 v206, v144, v145
	v_cvt_pk_bf16_f32 v207, v140, v141
	v_cvt_pk_bf16_f32 v208, v194, v195
	v_cvt_pk_bf16_f32 v209, v142, v143
	v_cvt_f32_i32_e32 v143, v133
	v_cvt_f32_i32_e32 v142, v132
	v_cvt_f32_i32_e32 v135, v135
	v_cvt_f32_i32_e32 v134, v134
	v_cvt_f32_i32_e32 v131, v131
	v_cvt_f32_i32_e32 v130, v130
	v_mov_b32_e32 v140, v192
	v_mov_b32_e32 v141, v192
	v_mul_f32_e32 v136, v140, v136
	v_mul_f32_e32 v137, v141, v137
	v_mov_b32_e32 v193, v192
	v_mov_b64_e32 v[138:139], s[66:67]
	v_mul_f32_e32 v132, v32, v136
	v_mul_f32_e32 v133, v33, v137
	v_mul_f32_e32 v136, v140, v142
	v_mul_f32_e32 v137, v141, v143
	v_mad_i64_i32 v[138:139], s[4:5], v172, s86, v[138:139]
	v_mul_f32_e32 v134, v192, v134
	v_mul_f32_e32 v135, v193, v135
	v_mul_f32_e32 v140, v192, v130
	v_mul_f32_e32 v141, v193, v131
	v_mul_f32_e32 v130, v24, v136
	v_mul_f32_e32 v131, v25, v137
	v_cndmask_b32_e64 v136, 0, 1, s[42:43]
	v_lshl_add_u64 v[138:139], v[170:171], 1, v[138:139]
	v_mul_f32_e32 v134, v30, v134
	v_mul_f32_e32 v135, v31, v135
	v_cmp_ne_u32_e64 s[4:5], 1, v136
	s_andn2_b64 vcc, exec, s[42:43]
	v_mul_f32_e32 v136, v22, v140
	v_mul_f32_e32 v137, v23, v141
	global_store_dwordx4 v[138:139], v[206:209], off
	s_cbranch_vccnz .LBB0_283
	v_and_b32_e32 v141, 0x7fffffff, v135
	v_and_b32_e32 v140, 0x7fffffff, v134
	v_fma_f32 v140, v140, s18, 1.0
	v_fma_f32 v141, v141, s18, 1.0
	v_mov_b64_e32 v[142:143], s[22:23]
	v_rcp_f32_e32 v140, v140
	v_rcp_f32_e32 v141, v141
	v_mul_f32_e32 v192, v134, v134
	v_mul_f32_e32 v193, v135, v135
	v_cmp_gt_f32_e32 vcc, 0, v134
	v_mul_f32_e32 v192, s30, v192
	v_mul_f32_e32 v193, s30, v193
	v_fma_f32 v144, v140, s20, v142
	v_fma_f32 v145, v141, s20, v142
	v_exp_f32_e32 v192, v192
	v_fma_f32 v144, v140, v144, s24
	v_fma_f32 v145, v141, v145, s24
	v_exp_f32_e32 v193, v193
	v_fma_f32 v144, v140, v144, s26
	v_fma_f32 v145, v141, v145, s26
	s_nop 0
	v_fma_f32 v144, v140, v144, s28
	v_fma_f32 v145, v141, v145, s28
	s_nop 0
	v_mul_f32_e32 v140, v140, v144
	v_mul_f32_e32 v141, v141, v145
	v_mul_f32_e32 v144, v132, v132
	v_mul_f32_e32 v145, v133, v133
	v_mul_f32_e32 v140, v192, v140
	v_mul_f32_e32 v141, v193, v141
	v_mul_f32_e32 v144, s30, v144
	v_mul_f32_e32 v145, s30, v145
	v_mul_f32_e32 v192, v134, v140
	v_mul_f32_e32 v193, v135, v141
	v_fma_f32 v140, -v134, v140, v134
	v_fma_f32 v141, -v135, v141, v135
	v_exp_f32_e32 v144, v144
	v_cndmask_b32_e32 v134, v140, v192, vcc
	v_cmp_gt_f32_e32 vcc, 0, v135
	v_and_b32_e32 v140, 0x7fffffff, v132
	v_exp_f32_e32 v145, v145
	v_cndmask_b32_e32 v135, v141, v193, vcc
	v_and_b32_e32 v141, 0x7fffffff, v133
	v_fma_f32 v140, v140, s18, 1.0
	v_fma_f32 v141, v141, s18, 1.0
	v_cmp_gt_f32_e32 vcc, 0, v132
	v_rcp_f32_e32 v140, v140
	v_rcp_f32_e32 v141, v141
	s_nop 0
	v_fma_f32 v192, v140, s20, v142
	v_fma_f32 v193, v141, s20, v142
	s_nop 0
	v_fma_f32 v192, v140, v192, s24
	v_fma_f32 v193, v141, v193, s24
	s_nop 0
	v_fma_f32 v192, v140, v192, s26
	v_fma_f32 v193, v141, v193, s26
	s_nop 0
	v_fma_f32 v192, v140, v192, s28
	v_fma_f32 v193, v141, v193, s28
	s_nop 0
	v_mul_f32_e32 v140, v140, v192
	v_mul_f32_e32 v141, v141, v193
	v_mul_f32_e32 v192, v136, v136
	v_mul_f32_e32 v193, v137, v137
	v_mul_f32_e32 v140, v144, v140
	v_mul_f32_e32 v141, v145, v141
	v_mul_f32_e32 v192, s30, v192
	v_mul_f32_e32 v193, s30, v193
	v_mul_f32_e32 v144, v132, v140
	v_mul_f32_e32 v145, v133, v141
	v_fma_f32 v140, -v132, v140, v132
	v_fma_f32 v141, -v133, v141, v133
	v_exp_f32_e32 v192, v192
	v_cndmask_b32_e32 v132, v140, v144, vcc
	v_cmp_gt_f32_e32 vcc, 0, v133
	v_and_b32_e32 v140, 0x7fffffff, v136
	v_exp_f32_e32 v193, v193
	v_cndmask_b32_e32 v133, v141, v145, vcc
	v_and_b32_e32 v141, 0x7fffffff, v137
	v_fma_f32 v140, v140, s18, 1.0
	v_fma_f32 v141, v141, s18, 1.0
	v_cmp_gt_f32_e32 vcc, 0, v136
	v_rcp_f32_e32 v140, v140
	v_rcp_f32_e32 v141, v141
	s_nop 0
	v_fma_f32 v144, v140, s20, v142
	v_fma_f32 v145, v141, s20, v142
	s_nop 0
	v_fma_f32 v144, v140, v144, s24
	v_fma_f32 v145, v141, v145, s24
	s_nop 0
	v_fma_f32 v144, v140, v144, s26
	v_fma_f32 v145, v141, v145, s26
	s_nop 0
	v_fma_f32 v144, v140, v144, s28
	v_fma_f32 v145, v141, v145, s28
	s_nop 0
	v_mul_f32_e32 v140, v140, v144
	v_mul_f32_e32 v141, v141, v145
	v_mul_f32_e32 v144, v130, v130
	v_mul_f32_e32 v145, v131, v131
	v_mul_f32_e32 v140, v192, v140
	v_mul_f32_e32 v141, v193, v141
	s_nop 0
	v_mul_f32_e32 v192, v136, v140
	v_mul_f32_e32 v193, v137, v141
	v_fma_f32 v140, -v136, v140, v136
	v_fma_f32 v141, -v137, v141, v137
	s_nop 0
	v_cndmask_b32_e32 v136, v140, v192, vcc
	v_cmp_gt_f32_e32 vcc, 0, v137
	v_and_b32_e32 v140, 0x7fffffff, v130
	s_nop 0
	v_cndmask_b32_e32 v137, v141, v193, vcc
	v_and_b32_e32 v141, 0x7fffffff, v131
	v_fma_f32 v140, v140, s18, 1.0
	v_fma_f32 v141, v141, s18, 1.0
	v_cmp_gt_f32_e32 vcc, 0, v130
	v_rcp_f32_e32 v140, v140
	v_rcp_f32_e32 v141, v141
	s_nop 0
	v_fma_f32 v143, v141, s20, v142
	v_fma_f32 v142, v140, s20, v142
	s_nop 0
	v_fma_f32 v142, v140, v142, s24
	v_fma_f32 v143, v141, v143, s24
	s_nop 0
	v_fma_f32 v142, v140, v142, s26
	v_fma_f32 v143, v141, v143, s26
	s_nop 0
	v_fma_f32 v142, v140, v142, s28
	v_fma_f32 v143, v141, v143, s28
	s_nop 0
	v_mul_f32_e32 v140, v140, v142
	v_mul_f32_e32 v141, v141, v143
	v_mul_f32_e32 v142, s30, v144
	v_mul_f32_e32 v143, s30, v145
	s_nop 0
	v_exp_f32_e32 v142, v142
	v_exp_f32_e32 v143, v143
	s_nop 0
	v_mul_f32_e32 v140, v142, v140
	v_mul_f32_e32 v141, v143, v141
	s_nop 0
	v_mul_f32_e32 v142, v130, v140
	v_mul_f32_e32 v143, v131, v141
	v_fma_f32 v140, -v130, v140, v130
	v_fma_f32 v141, -v131, v141, v131
	s_nop 0
	v_cndmask_b32_e32 v130, v140, v142, vcc
	v_cmp_gt_f32_e32 vcc, 0, v131
	s_nop 1
	v_cndmask_b32_e32 v131, v141, v143, vcc
; __device__ __forceinline__ unsigned cvt_pk_bf16(float lo, float hi) { unsigned r; asm volatile("v_cvt_pk_bf16_f32 %0, %1, %2" : "=v"(r) : "v"(lo), "v"(hi)); return r; }
; __device__ __forceinline__ f32x2 gelu_pk(f32x2 v) {
;     const f32x2 av = __builtin_elementwise_abs(v), d = av * 0.2316418882f + 1.0f;
;     f32x2 t; t.x = __builtin_amdgcn_rcpf(d.x); t.y = __builtin_amdgcn_rcpf(d.y);
;     f32x2 q = t * 0.5307027145f + (-0.7265760135f); q = q * t + 0.7107068705f; q = q * t + (-0.142248368f); q = q * t + 0.127414796f; q = q * t;
;     const f32x2 s = (v * v) * (-0.72134752044f);
;     f32x2 e; e.x = __builtin_amdgcn_exp2f(s.x); e.y = __builtin_amdgcn_exp2f(s.y);
;     const f32x2 m = v * (q * e), r = v - m;
;     f32x2 o; o.x = v.x < 0.f ? m.x : r.x; o.y = v.y < 0.f ? m.y : r.y; return o;
;     __device__ __forceinline__ void operator()(const f32x4 (&acc)[2][2][4][2], const Unit& u, int wr, int wc, int fr, int fq) const {
;     ...
;             for (int m = 0; m < 4; ++m) { const int row = row0 + ai * HALF + m * 16; const float rsc = rsv[ai][m]; bf16_t* rowp = O + (size_t)row * ldc + col0;
; #pragma unroll
;                 for (int bj = 0; bj < 2; ++bj) { const i32x4 a0 = __builtin_bit_cast(i32x4, acc[ai][bj][m][0]), a1 = __builtin_bit_cast(i32x4, acc[ai][bj][m][1]);
;                     f32x4 v0 = (f32x4){(float)a0[0], (float)a0[1], (float)a0[2], (float)a0[3]} * rsc * cv[bj][0], v1 = (f32x4){(float)a1[0], (float)a1[1], (float)a1[2], (float)a1[3]} * rsc * cv[bj][1];
;                     if (act) { f32x2 a = gelu_pk((f32x2){v0[0], v0[1]}), b = gelu_pk((f32x2){v0[2], v0[3]}), c = gelu_pk((f32x2){v1[0], v1[1]}), d = gelu_pk((f32x2){v1[2], v1[3]});
;                         v0 = (f32x4){a.x, a.y, b.x, b.y}; v1 = (f32x4){c.x, c.y, d.x, d.y}; }
;                     u32x4 w; w.x = cvt_pk_bf16(v0[0], v0[1]); w.y = cvt_pk_bf16(v0[2], v0[3]); w.z = cvt_pk_bf16(v1[0], v1[1]); w.w = cvt_pk_bf16(v1[2], v1[3]);
;                     if (nt) __builtin_nontemporal_store(w, (u32x4*)(rowp + bj * HALF)); else *(u32x4*)(rowp + bj * HALF) = w; } }
.LBB0_283:
	v_cvt_f32_i32_e32 v129, v129
	v_cvt_f32_i32_e32 v128, v128
	v_cvt_pk_bf16_f32 v134, v134, v135
	v_cvt_pk_bf16_f32 v135, v132, v133
	v_cvt_pk_bf16_f32 v136, v136, v137
	v_cvt_f32_i32_e32 v127, v127
	v_cvt_f32_i32_e32 v126, v126
	v_cvt_pk_bf16_f32 v137, v130, v131
	v_cvt_f32_i32_e32 v131, v125
	v_cvt_f32_i32_e32 v123, v123
	v_cvt_f32_i32_e32 v122, v122
	v_cvt_f32_i32_e32 v130, v124
	v_mul_f32_e32 v128, v188, v128
	v_mul_f32_e32 v129, v188, v129
	v_mul_f32_e32 v126, v188, v126
	v_mul_f32_e32 v127, v188, v127
	v_mul_f32_e32 v124, v40, v128
	v_mul_f32_e32 v125, v41, v129
	v_mul_f32_e32 v122, v188, v122
	v_mul_f32_e32 v123, v188, v123
	v_mul_f32_e32 v128, v188, v130
	v_mul_f32_e32 v129, v188, v131
	v_mul_f32_e32 v126, v38, v126
	v_mul_f32_e32 v127, v39, v127
	v_mul_f32_e32 v128, v36, v128
	v_mul_f32_e32 v129, v37, v129
	s_and_b64 vcc, exec, s[4:5]
	v_mul_f32_e32 v130, v34, v122
	v_mul_f32_e32 v131, v35, v123
	global_store_dwordx4 v[138:139], v[134:137], off offset:256
	s_cbranch_vccnz .LBB0_285
	v_and_b32_e32 v123, 0x7fffffff, v127
	v_and_b32_e32 v122, 0x7fffffff, v126
	v_fma_f32 v122, v122, s18, 1.0
	v_fma_f32 v123, v123, s18, 1.0
	v_mov_b64_e32 v[132:133], s[22:23]
	v_rcp_f32_e32 v122, v122
	v_rcp_f32_e32 v123, v123
	v_mul_f32_e32 v136, v126, v126
	v_mul_f32_e32 v137, v127, v127
	v_cmp_gt_f32_e32 vcc, 0, v126
	v_mul_f32_e32 v136, s30, v136
	v_mul_f32_e32 v137, s30, v137
	v_fma_f32 v134, v122, s20, v132
	v_fma_f32 v135, v123, s20, v132
	v_exp_f32_e32 v136, v136
	v_fma_f32 v134, v122, v134, s24
	v_fma_f32 v135, v123, v135, s24
	v_exp_f32_e32 v137, v137
	v_fma_f32 v134, v122, v134, s26
	v_fma_f32 v135, v123, v135, s26
	s_nop 0
	v_fma_f32 v134, v122, v134, s28
	v_fma_f32 v135, v123, v135, s28
	s_nop 0
	v_mul_f32_e32 v122, v122, v134
	v_mul_f32_e32 v123, v123, v135
	v_mul_f32_e32 v134, v124, v124
	v_mul_f32_e32 v135, v125, v125
	v_mul_f32_e32 v122, v136, v122
	v_mul_f32_e32 v123, v137, v123
	v_mul_f32_e32 v134, s30, v134
	v_mul_f32_e32 v135, s30, v135
	v_mul_f32_e32 v136, v126, v122
	v_mul_f32_e32 v137, v127, v123
	v_fma_f32 v122, -v126, v122, v126
	v_fma_f32 v123, -v127, v123, v127
	v_exp_f32_e32 v134, v134
	v_cndmask_b32_e32 v126, v122, v136, vcc
	v_cmp_gt_f32_e32 vcc, 0, v127
	v_and_b32_e32 v122, 0x7fffffff, v124
	v_exp_f32_e32 v135, v135
	v_cndmask_b32_e32 v127, v123, v137, vcc
	v_and_b32_e32 v123, 0x7fffffff, v125
	v_fma_f32 v122, v122, s18, 1.0
	v_fma_f32 v123, v123, s18, 1.0
	v_cmp_gt_f32_e32 vcc, 0, v124
	v_rcp_f32_e32 v122, v122
	v_rcp_f32_e32 v123, v123
	s_nop 0
	v_fma_f32 v136, v122, s20, v132
	v_fma_f32 v137, v123, s20, v132
	s_nop 0
	v_fma_f32 v136, v122, v136, s24
	v_fma_f32 v137, v123, v137, s24
	s_nop 0
	v_fma_f32 v136, v122, v136, s26
	v_fma_f32 v137, v123, v137, s26
	s_nop 0
	v_fma_f32 v136, v122, v136, s28
	v_fma_f32 v137, v123, v137, s28
	s_nop 0
	v_mul_f32_e32 v122, v122, v136
	v_mul_f32_e32 v123, v123, v137
	v_mul_f32_e32 v136, v130, v130
	v_mul_f32_e32 v137, v131, v131
	v_mul_f32_e32 v122, v134, v122
	v_mul_f32_e32 v123, v135, v123
	v_mul_f32_e32 v136, s30, v136
	v_mul_f32_e32 v137, s30, v137
	v_mul_f32_e32 v134, v124, v122
	v_mul_f32_e32 v135, v125, v123
	v_fma_f32 v122, -v124, v122, v124
	v_fma_f32 v123, -v125, v123, v125
	v_exp_f32_e32 v136, v136
	v_cndmask_b32_e32 v124, v122, v134, vcc
	v_cmp_gt_f32_e32 vcc, 0, v125
	v_and_b32_e32 v122, 0x7fffffff, v130
	v_exp_f32_e32 v137, v137
	v_cndmask_b32_e32 v125, v123, v135, vcc
	v_and_b32_e32 v123, 0x7fffffff, v131
	v_fma_f32 v122, v122, s18, 1.0
	v_fma_f32 v123, v123, s18, 1.0
	v_cmp_gt_f32_e32 vcc, 0, v130
	v_rcp_f32_e32 v122, v122
	v_rcp_f32_e32 v123, v123
	s_nop 0
	v_fma_f32 v134, v122, s20, v132
	v_fma_f32 v135, v123, s20, v132
	s_nop 0
	v_fma_f32 v134, v122, v134, s24
	v_fma_f32 v135, v123, v135, s24
	s_nop 0
	v_fma_f32 v134, v122, v134, s26
	v_fma_f32 v135, v123, v135, s26
	s_nop 0
	v_fma_f32 v134, v122, v134, s28
	v_fma_f32 v135, v123, v135, s28
	s_nop 0
	v_mul_f32_e32 v122, v122, v134
	v_mul_f32_e32 v123, v123, v135
	v_mul_f32_e32 v134, v128, v128
	v_mul_f32_e32 v135, v129, v129
	v_mul_f32_e32 v122, v136, v122
	v_mul_f32_e32 v123, v137, v123
	s_nop 0
	v_mul_f32_e32 v136, v130, v122
	v_mul_f32_e32 v137, v131, v123
	v_fma_f32 v122, -v130, v122, v130
	v_fma_f32 v123, -v131, v123, v131
	s_nop 0
	v_cndmask_b32_e32 v130, v122, v136, vcc
	v_cmp_gt_f32_e32 vcc, 0, v131
	v_and_b32_e32 v122, 0x7fffffff, v128
	s_nop 0
	v_cndmask_b32_e32 v131, v123, v137, vcc
	v_and_b32_e32 v123, 0x7fffffff, v129
	v_fma_f32 v122, v122, s18, 1.0
	v_fma_f32 v123, v123, s18, 1.0
	v_cmp_gt_f32_e32 vcc, 0, v128
	v_rcp_f32_e32 v122, v122
	v_rcp_f32_e32 v123, v123
	s_nop 0
	v_fma_f32 v133, v123, s20, v132
	v_fma_f32 v132, v122, s20, v132
	s_nop 0
	v_fma_f32 v132, v122, v132, s24
	v_fma_f32 v133, v123, v133, s24
	s_nop 0
	v_fma_f32 v132, v122, v132, s26
	v_fma_f32 v133, v123, v133, s26
	s_nop 0
	v_fma_f32 v132, v122, v132, s28
	v_fma_f32 v133, v123, v133, s28
	s_nop 0
	v_mul_f32_e32 v122, v122, v132
	v_mul_f32_e32 v123, v123, v133
	v_mul_f32_e32 v132, s30, v134
	v_mul_f32_e32 v133, s30, v135
	s_nop 0
	v_exp_f32_e32 v132, v132
	v_exp_f32_e32 v133, v133
	s_nop 0
	v_mul_f32_e32 v122, v132, v122
	v_mul_f32_e32 v123, v133, v123
	s_nop 0
	v_mul_f32_e32 v132, v128, v122
	v_mul_f32_e32 v133, v129, v123
	v_fma_f32 v122, -v128, v122, v128
	v_fma_f32 v123, -v129, v123, v129
	s_nop 0
	v_cndmask_b32_e32 v128, v122, v132, vcc
	v_cmp_gt_f32_e32 vcc, 0, v129
	s_nop 1
	v_cndmask_b32_e32 v129, v123, v133, vcc
; __device__ __forceinline__ unsigned cvt_pk_bf16(float lo, float hi) { unsigned r; asm volatile("v_cvt_pk_bf16_f32 %0, %1, %2" : "=v"(r) : "v"(lo), "v"(hi)); return r; }
; __device__ __forceinline__ f32x2 gelu_pk(f32x2 v) {
;     const f32x2 av = __builtin_elementwise_abs(v), d = av * 0.2316418882f + 1.0f;
;     f32x2 t; t.x = __builtin_amdgcn_rcpf(d.x); t.y = __builtin_amdgcn_rcpf(d.y);
;     f32x2 q = t * 0.5307027145f + (-0.7265760135f); q = q * t + 0.7107068705f; q = q * t + (-0.142248368f); q = q * t + 0.127414796f; q = q * t;
;     const f32x2 s = (v * v) * (-0.72134752044f);
;     f32x2 e; e.x = __builtin_amdgcn_exp2f(s.x); e.y = __builtin_amdgcn_exp2f(s.y);
;     const f32x2 m = v * (q * e), r = v - m;
;     f32x2 o; o.x = v.x < 0.f ? m.x : r.x; o.y = v.y < 0.f ? m.y : r.y; return o;
;     __device__ __forceinline__ void operator()(const f32x4 (&acc)[2][2][4][2], const Unit& u, int wr, int wc, int fr, int fq) const {
;     ...
;             for (int m = 0; m < 4; ++m) { const int row = row0 + ai * HALF + m * 16; const float rsc = rsv[ai][m]; bf16_t* rowp = O + (size_t)row * ldc + col0;
; #pragma unroll
;                 for (int bj = 0; bj < 2; ++bj) { const i32x4 a0 = __builtin_bit_cast(i32x4, acc[ai][bj][m][0]), a1 = __builtin_bit_cast(i32x4, acc[ai][bj][m][1]);
;                     f32x4 v0 = (f32x4){(float)a0[0], (float)a0[1], (float)a0[2], (float)a0[3]} * rsc * cv[bj][0], v1 = (f32x4){(float)a1[0], (float)a1[1], (float)a1[2], (float)a1[3]} * rsc * cv[bj][1];
;                     if (act) { f32x2 a = gelu_pk((f32x2){v0[0], v0[1]}), b = gelu_pk((f32x2){v0[2], v0[3]}), c = gelu_pk((f32x2){v1[0], v1[1]}), d = gelu_pk((f32x2){v1[2], v1[3]});
;                         v0 = (f32x4){a.x, a.y, b.x, b.y}; v1 = (f32x4){c.x, c.y, d.x, d.y}; }
;                     u32x4 w; w.x = cvt_pk_bf16(v0[0], v0[1]); w.y = cvt_pk_bf16(v0[2], v0[3]); w.z = cvt_pk_bf16(v1[0], v1[1]); w.w = cvt_pk_bf16(v1[2], v1[3]);
;                     if (nt) __builtin_nontemporal_store(w, (u32x4*)(rowp + bj * HALF)); else *(u32x4*)(rowp + bj * HALF) = w; } }
.LBB0_285:
	v_cvt_f32_i32_e32 v121, v121
	v_cvt_f32_i32_e32 v120, v120
	v_cvt_pk_bf16_f32 v132, v126, v127
	v_cvt_f32_i32_e32 v119, v119
	v_cvt_f32_i32_e32 v118, v118
	v_cvt_f32_i32_e32 v115, v115
	v_cvt_f32_i32_e32 v127, v117
	v_cvt_f32_i32_e32 v126, v116
	v_cvt_f32_i32_e32 v114, v114
	v_cvt_pk_bf16_f32 v133, v124, v125
	v_mov_b32_e32 v124, v188
	v_mov_b32_e32 v125, v188
	v_mov_b32_e32 v189, v188
	v_mov_b64_e32 v[122:123], s[66:67]
	v_mul_f32_e32 v120, v124, v120
	v_mul_f32_e32 v121, v125, v121
	v_mad_i64_i32 v[122:123], s[42:43], v190, s86, v[122:123]
	v_mul_f32_e32 v118, v188, v118
	v_mul_f32_e32 v119, v189, v119
	v_mul_f32_e32 v116, v32, v120
	v_mul_f32_e32 v117, v33, v121
	v_mul_f32_e32 v120, v124, v126
	v_mul_f32_e32 v121, v125, v127
	v_mul_f32_e32 v124, v188, v114
	v_mul_f32_e32 v125, v189, v115
	v_lshl_add_u64 v[122:123], v[170:171], 1, v[122:123]
	v_mul_f32_e32 v118, v30, v118
	v_mul_f32_e32 v119, v31, v119
	v_mul_f32_e32 v114, v24, v120
	v_mul_f32_e32 v115, v25, v121
	s_and_b64 vcc, exec, s[4:5]
	v_mul_f32_e32 v120, v22, v124
	v_mul_f32_e32 v121, v23, v125
	v_cvt_pk_bf16_f32 v134, v130, v131
	v_cvt_pk_bf16_f32 v135, v128, v129
	global_store_dwordx4 v[122:123], v[132:135], off
	s_cbranch_vccnz .LBB0_287
	v_and_b32_e32 v125, 0x7fffffff, v119
	v_and_b32_e32 v124, 0x7fffffff, v118
	v_fma_f32 v124, v124, s18, 1.0
	v_fma_f32 v125, v125, s18, 1.0
	v_mov_b64_e32 v[126:127], s[22:23]
	v_rcp_f32_e32 v124, v124
	v_rcp_f32_e32 v125, v125
	v_mul_f32_e32 v130, v118, v118
	v_mul_f32_e32 v131, v119, v119
	v_cmp_gt_f32_e32 vcc, 0, v118
	v_mul_f32_e32 v130, s30, v130
	v_mul_f32_e32 v131, s30, v131
	v_fma_f32 v128, v124, s20, v126
	v_fma_f32 v129, v125, s20, v126
	v_exp_f32_e32 v130, v130
	v_fma_f32 v128, v124, v128, s24
	v_fma_f32 v129, v125, v129, s24
	v_exp_f32_e32 v131, v131
	v_fma_f32 v128, v124, v128, s26
	v_fma_f32 v129, v125, v129, s26
	s_nop 0
	v_fma_f32 v128, v124, v128, s28
	v_fma_f32 v129, v125, v129, s28
	s_nop 0
	v_mul_f32_e32 v124, v124, v128
	v_mul_f32_e32 v125, v125, v129
	v_mul_f32_e32 v128, v116, v116
	v_mul_f32_e32 v129, v117, v117
	v_mul_f32_e32 v124, v130, v124
	v_mul_f32_e32 v125, v131, v125
	v_mul_f32_e32 v128, s30, v128
	v_mul_f32_e32 v129, s30, v129
	v_mul_f32_e32 v130, v118, v124
	v_mul_f32_e32 v131, v119, v125
	v_fma_f32 v124, -v118, v124, v118
	v_fma_f32 v125, -v119, v125, v119
	v_exp_f32_e32 v128, v128
	v_cndmask_b32_e32 v118, v124, v130, vcc
	v_cmp_gt_f32_e32 vcc, 0, v119
	v_and_b32_e32 v124, 0x7fffffff, v116
	v_exp_f32_e32 v129, v129
	v_cndmask_b32_e32 v119, v125, v131, vcc
	v_and_b32_e32 v125, 0x7fffffff, v117
	v_fma_f32 v124, v124, s18, 1.0
	v_fma_f32 v125, v125, s18, 1.0
	v_cmp_gt_f32_e32 vcc, 0, v116
	v_rcp_f32_e32 v124, v124
	v_rcp_f32_e32 v125, v125
	s_nop 0
	v_fma_f32 v130, v124, s20, v126
	v_fma_f32 v131, v125, s20, v126
	s_nop 0
	v_fma_f32 v130, v124, v130, s24
	v_fma_f32 v131, v125, v131, s24
	s_nop 0
	v_fma_f32 v130, v124, v130, s26
	v_fma_f32 v131, v125, v131, s26
	s_nop 0
	v_fma_f32 v130, v124, v130, s28
	v_fma_f32 v131, v125, v131, s28
	s_nop 0
	v_mul_f32_e32 v124, v124, v130
	v_mul_f32_e32 v125, v125, v131
	v_mul_f32_e32 v130, v120, v120
	v_mul_f32_e32 v131, v121, v121
	v_mul_f32_e32 v124, v128, v124
	v_mul_f32_e32 v125, v129, v125
	v_mul_f32_e32 v130, s30, v130
	v_mul_f32_e32 v131, s30, v131
	v_mul_f32_e32 v128, v116, v124
	v_mul_f32_e32 v129, v117, v125
	v_fma_f32 v124, -v116, v124, v116
	v_fma_f32 v125, -v117, v125, v117
	v_exp_f32_e32 v130, v130
	v_cndmask_b32_e32 v116, v124, v128, vcc
	v_cmp_gt_f32_e32 vcc, 0, v117
	v_and_b32_e32 v124, 0x7fffffff, v120
	v_exp_f32_e32 v131, v131
	v_cndmask_b32_e32 v117, v125, v129, vcc
	v_and_b32_e32 v125, 0x7fffffff, v121
	v_fma_f32 v124, v124, s18, 1.0
	v_fma_f32 v125, v125, s18, 1.0
	v_cmp_gt_f32_e32 vcc, 0, v120
	v_rcp_f32_e32 v124, v124
	v_rcp_f32_e32 v125, v125
	s_nop 0
	v_fma_f32 v128, v124, s20, v126
	v_fma_f32 v129, v125, s20, v126
	s_nop 0
	v_fma_f32 v128, v124, v128, s24
	v_fma_f32 v129, v125, v129, s24
	s_nop 0
	v_fma_f32 v128, v124, v128, s26
	v_fma_f32 v129, v125, v129, s26
	s_nop 0
	v_fma_f32 v128, v124, v128, s28
	v_fma_f32 v129, v125, v129, s28
	s_nop 0
	v_mul_f32_e32 v124, v124, v128
	v_mul_f32_e32 v125, v125, v129
	v_mul_f32_e32 v128, v114, v114
	v_mul_f32_e32 v129, v115, v115
	v_mul_f32_e32 v124, v130, v124
	v_mul_f32_e32 v125, v131, v125
	s_nop 0
	v_mul_f32_e32 v130, v120, v124
	v_mul_f32_e32 v131, v121, v125
	v_fma_f32 v124, -v120, v124, v120
	v_fma_f32 v125, -v121, v125, v121
	s_nop 0
	v_cndmask_b32_e32 v120, v124, v130, vcc
	v_cmp_gt_f32_e32 vcc, 0, v121
	v_and_b32_e32 v124, 0x7fffffff, v114
	s_nop 0
	v_cndmask_b32_e32 v121, v125, v131, vcc
	v_and_b32_e32 v125, 0x7fffffff, v115
	v_fma_f32 v124, v124, s18, 1.0
	v_fma_f32 v125, v125, s18, 1.0
	v_cmp_gt_f32_e32 vcc, 0, v114
	v_rcp_f32_e32 v124, v124
	v_rcp_f32_e32 v125, v125
	s_nop 0
	v_fma_f32 v127, v125, s20, v126
	v_fma_f32 v126, v124, s20, v126
	s_nop 0
	v_fma_f32 v126, v124, v126, s24
	v_fma_f32 v127, v125, v127, s24
	s_nop 0
	v_fma_f32 v126, v124, v126, s26
	v_fma_f32 v127, v125, v127, s26
	s_nop 0
	v_fma_f32 v126, v124, v126, s28
	v_fma_f32 v127, v125, v127, s28
	s_nop 0
	v_mul_f32_e32 v124, v124, v126
	v_mul_f32_e32 v125, v125, v127
	v_mul_f32_e32 v126, s30, v128
	v_mul_f32_e32 v127, s30, v129
	s_nop 0
	v_exp_f32_e32 v126, v126
	v_exp_f32_e32 v127, v127
	s_nop 0
	v_mul_f32_e32 v124, v126, v124
	v_mul_f32_e32 v125, v127, v125
	s_nop 0
	v_mul_f32_e32 v126, v114, v124
	v_mul_f32_e32 v127, v115, v125
	v_fma_f32 v124, -v114, v124, v114
	v_fma_f32 v125, -v115, v125, v115
	s_nop 0
	v_cndmask_b32_e32 v114, v124, v126, vcc
	v_cmp_gt_f32_e32 vcc, 0, v115
	s_nop 1
	v_cndmask_b32_e32 v115, v125, v127, vcc
; __device__ __forceinline__ unsigned cvt_pk_bf16(float lo, float hi) { unsigned r; asm volatile("v_cvt_pk_bf16_f32 %0, %1, %2" : "=v"(r) : "v"(lo), "v"(hi)); return r; }
; __device__ __forceinline__ f32x2 gelu_pk(f32x2 v) {
;     const f32x2 av = __builtin_elementwise_abs(v), d = av * 0.2316418882f + 1.0f;
;     f32x2 t; t.x = __builtin_amdgcn_rcpf(d.x); t.y = __builtin_amdgcn_rcpf(d.y);
;     f32x2 q = t * 0.5307027145f + (-0.7265760135f); q = q * t + 0.7107068705f; q = q * t + (-0.142248368f); q = q * t + 0.127414796f; q = q * t;
;     const f32x2 s = (v * v) * (-0.72134752044f);
;     f32x2 e; e.x = __builtin_amdgcn_exp2f(s.x); e.y = __builtin_amdgcn_exp2f(s.y);
;     const f32x2 m = v * (q * e), r = v - m;
;     f32x2 o; o.x = v.x < 0.f ? m.x : r.x; o.y = v.y < 0.f ? m.y : r.y; return o;
;     __device__ __forceinline__ void operator()(const f32x4 (&acc)[2][2][4][2], const Unit& u, int wr, int wc, int fr, int fq) const {
;     ...
;             for (int m = 0; m < 4; ++m) { const int row = row0 + ai * HALF + m * 16; const float rsc = rsv[ai][m]; bf16_t* rowp = O + (size_t)row * ldc + col0;
; #pragma unroll
;                 for (int bj = 0; bj < 2; ++bj) { const i32x4 a0 = __builtin_bit_cast(i32x4, acc[ai][bj][m][0]), a1 = __builtin_bit_cast(i32x4, acc[ai][bj][m][1]);
;                     f32x4 v0 = (f32x4){(float)a0[0], (float)a0[1], (float)a0[2], (float)a0[3]} * rsc * cv[bj][0], v1 = (f32x4){(float)a1[0], (float)a1[1], (float)a1[2], (float)a1[3]} * rsc * cv[bj][1];
;                     if (act) { f32x2 a = gelu_pk((f32x2){v0[0], v0[1]}), b = gelu_pk((f32x2){v0[2], v0[3]}), c = gelu_pk((f32x2){v1[0], v1[1]}), d = gelu_pk((f32x2){v1[2], v1[3]});
;                         v0 = (f32x4){a.x, a.y, b.x, b.y}; v1 = (f32x4){c.x, c.y, d.x, d.y}; }
;                     u32x4 w; w.x = cvt_pk_bf16(v0[0], v0[1]); w.y = cvt_pk_bf16(v0[2], v0[3]); w.z = cvt_pk_bf16(v1[0], v1[1]); w.w = cvt_pk_bf16(v1[2], v1[3]);
;                     if (nt) __builtin_nontemporal_store(w, (u32x4*)(rowp + bj * HALF)); else *(u32x4*)(rowp + bj * HALF) = w; } }
.LBB0_287:
	v_cvt_f32_i32_e32 v113, v113
	v_cvt_f32_i32_e32 v112, v112
	v_cvt_pk_bf16_f32 v118, v118, v119
	v_cvt_pk_bf16_f32 v119, v116, v117
	v_cvt_pk_bf16_f32 v120, v120, v121
	v_cvt_f32_i32_e32 v111, v111
	v_cvt_f32_i32_e32 v110, v110
	v_cvt_pk_bf16_f32 v121, v114, v115
	v_cvt_f32_i32_e32 v115, v109
	v_cvt_f32_i32_e32 v107, v107
	v_cvt_f32_i32_e32 v106, v106
	v_cvt_f32_i32_e32 v114, v108
	v_mul_f32_e32 v112, v184, v112
	v_mul_f32_e32 v113, v184, v113
	v_mul_f32_e32 v110, v184, v110
	v_mul_f32_e32 v111, v184, v111
	v_mul_f32_e32 v108, v40, v112
	v_mul_f32_e32 v109, v41, v113
	v_mul_f32_e32 v106, v184, v106
	v_mul_f32_e32 v107, v184, v107
	v_mul_f32_e32 v112, v184, v114
	v_mul_f32_e32 v113, v184, v115
	v_mul_f32_e32 v110, v38, v110
	v_mul_f32_e32 v111, v39, v111
	v_mul_f32_e32 v112, v36, v112
	v_mul_f32_e32 v113, v37, v113
	s_and_b64 vcc, exec, s[4:5]
	v_mul_f32_e32 v114, v34, v106
	v_mul_f32_e32 v115, v35, v107
	global_store_dwordx4 v[122:123], v[118:121], off offset:256
	s_cbranch_vccnz .LBB0_289
	v_and_b32_e32 v107, 0x7fffffff, v111
	v_and_b32_e32 v106, 0x7fffffff, v110
	v_fma_f32 v106, v106, s18, 1.0
	v_fma_f32 v107, v107, s18, 1.0
	v_mov_b64_e32 v[116:117], s[22:23]
	v_rcp_f32_e32 v106, v106
	v_rcp_f32_e32 v107, v107
	v_mul_f32_e32 v120, v110, v110
	v_mul_f32_e32 v121, v111, v111
	v_cmp_gt_f32_e32 vcc, 0, v110
	v_mul_f32_e32 v120, s30, v120
	v_mul_f32_e32 v121, s30, v121
	v_fma_f32 v118, v106, s20, v116
	v_fma_f32 v119, v107, s20, v116
	v_exp_f32_e32 v120, v120
	v_fma_f32 v118, v106, v118, s24
	v_fma_f32 v119, v107, v119, s24
	v_exp_f32_e32 v121, v121
	v_fma_f32 v118, v106, v118, s26
	v_fma_f32 v119, v107, v119, s26
	s_nop 0
	v_fma_f32 v118, v106, v118, s28
	v_fma_f32 v119, v107, v119, s28
	s_nop 0
	v_mul_f32_e32 v106, v106, v118
	v_mul_f32_e32 v107, v107, v119
	v_mul_f32_e32 v118, v108, v108
	v_mul_f32_e32 v119, v109, v109
	v_mul_f32_e32 v106, v120, v106
	v_mul_f32_e32 v107, v121, v107
	v_mul_f32_e32 v118, s30, v118
	v_mul_f32_e32 v119, s30, v119
	v_mul_f32_e32 v120, v110, v106
	v_mul_f32_e32 v121, v111, v107
	v_fma_f32 v106, -v110, v106, v110
	v_fma_f32 v107, -v111, v107, v111
	v_exp_f32_e32 v118, v118
	v_cndmask_b32_e32 v110, v106, v120, vcc
	v_cmp_gt_f32_e32 vcc, 0, v111
	v_and_b32_e32 v106, 0x7fffffff, v108
	v_exp_f32_e32 v119, v119
	v_cndmask_b32_e32 v111, v107, v121, vcc
	v_and_b32_e32 v107, 0x7fffffff, v109
	v_fma_f32 v106, v106, s18, 1.0
	v_fma_f32 v107, v107, s18, 1.0
	v_cmp_gt_f32_e32 vcc, 0, v108
	v_rcp_f32_e32 v106, v106
	v_rcp_f32_e32 v107, v107
	s_nop 0
	v_fma_f32 v120, v106, s20, v116
	v_fma_f32 v121, v107, s20, v116
	s_nop 0
	v_fma_f32 v120, v106, v120, s24
	v_fma_f32 v121, v107, v121, s24
	s_nop 0
	v_fma_f32 v120, v106, v120, s26
	v_fma_f32 v121, v107, v121, s26
	s_nop 0
	v_fma_f32 v120, v106, v120, s28
	v_fma_f32 v121, v107, v121, s28
	s_nop 0
	v_mul_f32_e32 v106, v106, v120
	v_mul_f32_e32 v107, v107, v121
	v_mul_f32_e32 v120, v114, v114
	v_mul_f32_e32 v121, v115, v115
	v_mul_f32_e32 v106, v118, v106
	v_mul_f32_e32 v107, v119, v107
	v_mul_f32_e32 v120, s30, v120
	v_mul_f32_e32 v121, s30, v121
	v_mul_f32_e32 v118, v108, v106
	v_mul_f32_e32 v119, v109, v107
	v_fma_f32 v106, -v108, v106, v108
	v_fma_f32 v107, -v109, v107, v109
	v_exp_f32_e32 v120, v120
	v_cndmask_b32_e32 v108, v106, v118, vcc
	v_cmp_gt_f32_e32 vcc, 0, v109
	v_and_b32_e32 v106, 0x7fffffff, v114
	v_exp_f32_e32 v121, v121
	v_cndmask_b32_e32 v109, v107, v119, vcc
	v_and_b32_e32 v107, 0x7fffffff, v115
	v_fma_f32 v106, v106, s18, 1.0
	v_fma_f32 v107, v107, s18, 1.0
	v_cmp_gt_f32_e32 vcc, 0, v114
	v_rcp_f32_e32 v106, v106
	v_rcp_f32_e32 v107, v107
	s_nop 0
	v_fma_f32 v118, v106, s20, v116
	v_fma_f32 v119, v107, s20, v116
	s_nop 0
	v_fma_f32 v118, v106, v118, s24
	v_fma_f32 v119, v107, v119, s24
	s_nop 0
	v_fma_f32 v118, v106, v118, s26
	v_fma_f32 v119, v107, v119, s26
	s_nop 0
	v_fma_f32 v118, v106, v118, s28
	v_fma_f32 v119, v107, v119, s28
	s_nop 0
	v_mul_f32_e32 v106, v106, v118
	v_mul_f32_e32 v107, v107, v119
	v_mul_f32_e32 v118, v112, v112
	v_mul_f32_e32 v119, v113, v113
	v_mul_f32_e32 v106, v120, v106
	v_mul_f32_e32 v107, v121, v107
	s_nop 0
	v_mul_f32_e32 v120, v114, v106
	v_mul_f32_e32 v121, v115, v107
	v_fma_f32 v106, -v114, v106, v114
	v_fma_f32 v107, -v115, v107, v115
	s_nop 0
	v_cndmask_b32_e32 v114, v106, v120, vcc
	v_cmp_gt_f32_e32 vcc, 0, v115
	v_and_b32_e32 v106, 0x7fffffff, v112
	s_nop 0
	v_cndmask_b32_e32 v115, v107, v121, vcc
	v_and_b32_e32 v107, 0x7fffffff, v113
	v_fma_f32 v106, v106, s18, 1.0
	v_fma_f32 v107, v107, s18, 1.0
	v_cmp_gt_f32_e32 vcc, 0, v112
	v_rcp_f32_e32 v106, v106
	v_rcp_f32_e32 v107, v107
	s_nop 0
	v_fma_f32 v117, v107, s20, v116
	v_fma_f32 v116, v106, s20, v116
	s_nop 0
	v_fma_f32 v116, v106, v116, s24
	v_fma_f32 v117, v107, v117, s24
	s_nop 0
	v_fma_f32 v116, v106, v116, s26
	v_fma_f32 v117, v107, v117, s26
	s_nop 0
	v_fma_f32 v116, v106, v116, s28
	v_fma_f32 v117, v107, v117, s28
	s_nop 0
	v_mul_f32_e32 v106, v106, v116
	v_mul_f32_e32 v107, v107, v117
	v_mul_f32_e32 v116, s30, v118
	v_mul_f32_e32 v117, s30, v119
	s_nop 0
	v_exp_f32_e32 v116, v116
	v_exp_f32_e32 v117, v117
	s_nop 0
	v_mul_f32_e32 v106, v116, v106
	v_mul_f32_e32 v107, v117, v107
	s_nop 0
	v_mul_f32_e32 v116, v112, v106
	v_mul_f32_e32 v117, v113, v107
	v_fma_f32 v106, -v112, v106, v112
	v_fma_f32 v107, -v113, v107, v113
	s_nop 0
	v_cndmask_b32_e32 v112, v106, v116, vcc
	v_cmp_gt_f32_e32 vcc, 0, v113
	s_nop 1
	v_cndmask_b32_e32 v113, v107, v117, vcc
; __device__ __forceinline__ unsigned cvt_pk_bf16(float lo, float hi) { unsigned r; asm volatile("v_cvt_pk_bf16_f32 %0, %1, %2" : "=v"(r) : "v"(lo), "v"(hi)); return r; }
; __device__ __forceinline__ f32x2 gelu_pk(f32x2 v) {
;     const f32x2 av = __builtin_elementwise_abs(v), d = av * 0.2316418882f + 1.0f;
;     f32x2 t; t.x = __builtin_amdgcn_rcpf(d.x); t.y = __builtin_amdgcn_rcpf(d.y);
;     f32x2 q = t * 0.5307027145f + (-0.7265760135f); q = q * t + 0.7107068705f; q = q * t + (-0.142248368f); q = q * t + 0.127414796f; q = q * t;
;     const f32x2 s = (v * v) * (-0.72134752044f);
;     f32x2 e; e.x = __builtin_amdgcn_exp2f(s.x); e.y = __builtin_amdgcn_exp2f(s.y);
;     const f32x2 m = v * (q * e), r = v - m;
;     f32x2 o; o.x = v.x < 0.f ? m.x : r.x; o.y = v.y < 0.f ? m.y : r.y; return o;
;     __device__ __forceinline__ void operator()(const f32x4 (&acc)[2][2][4][2], const Unit& u, int wr, int wc, int fr, int fq) const {
;     ...
;             for (int m = 0; m < 4; ++m) { const int row = row0 + ai * HALF + m * 16; const float rsc = rsv[ai][m]; bf16_t* rowp = O + (size_t)row * ldc + col0;
; #pragma unroll
;                 for (int bj = 0; bj < 2; ++bj) { const i32x4 a0 = __builtin_bit_cast(i32x4, acc[ai][bj][m][0]), a1 = __builtin_bit_cast(i32x4, acc[ai][bj][m][1]);
;                     f32x4 v0 = (f32x4){(float)a0[0], (float)a0[1], (float)a0[2], (float)a0[3]} * rsc * cv[bj][0], v1 = (f32x4){(float)a1[0], (float)a1[1], (float)a1[2], (float)a1[3]} * rsc * cv[bj][1];
;                     if (act) { f32x2 a = gelu_pk((f32x2){v0[0], v0[1]}), b = gelu_pk((f32x2){v0[2], v0[3]}), c = gelu_pk((f32x2){v1[0], v1[1]}), d = gelu_pk((f32x2){v1[2], v1[3]});
;                         v0 = (f32x4){a.x, a.y, b.x, b.y}; v1 = (f32x4){c.x, c.y, d.x, d.y}; }
;                     u32x4 w; w.x = cvt_pk_bf16(v0[0], v0[1]); w.y = cvt_pk_bf16(v0[2], v0[3]); w.z = cvt_pk_bf16(v1[0], v1[1]); w.w = cvt_pk_bf16(v1[2], v1[3]);
;                     if (nt) __builtin_nontemporal_store(w, (u32x4*)(rowp + bj * HALF)); else *(u32x4*)(rowp + bj * HALF) = w; } }
.LBB0_289:
	v_cvt_f32_i32_e32 v105, v105
	v_cvt_f32_i32_e32 v104, v104
	v_cvt_pk_bf16_f32 v116, v110, v111
	v_cvt_f32_i32_e32 v103, v103
	v_cvt_f32_i32_e32 v102, v102
	v_cvt_f32_i32_e32 v99, v99
	v_cvt_f32_i32_e32 v111, v101
	v_cvt_f32_i32_e32 v110, v100
	v_cvt_f32_i32_e32 v98, v98
	v_cvt_pk_bf16_f32 v117, v108, v109
	v_mov_b32_e32 v108, v184
	v_mov_b32_e32 v109, v184
	v_mov_b32_e32 v185, v184
	v_mov_b64_e32 v[106:107], s[66:67]
	v_mul_f32_e32 v104, v108, v104
	v_mul_f32_e32 v105, v109, v105
	v_mad_i64_i32 v[106:107], s[42:43], v186, s86, v[106:107]
	v_mul_f32_e32 v102, v184, v102
	v_mul_f32_e32 v103, v185, v103
	v_mul_f32_e32 v100, v32, v104
	v_mul_f32_e32 v101, v33, v105
	v_mul_f32_e32 v104, v108, v110
	v_mul_f32_e32 v105, v109, v111
	v_mul_f32_e32 v108, v184, v98
	v_mul_f32_e32 v109, v185, v99
	v_lshl_add_u64 v[106:107], v[170:171], 1, v[106:107]
	v_mul_f32_e32 v102, v30, v102
	v_mul_f32_e32 v103, v31, v103
	v_mul_f32_e32 v98, v24, v104
	v_mul_f32_e32 v99, v25, v105
	s_and_b64 vcc, exec, s[4:5]
	v_mul_f32_e32 v104, v22, v108
	v_mul_f32_e32 v105, v23, v109
	v_cvt_pk_bf16_f32 v118, v114, v115
	v_cvt_pk_bf16_f32 v119, v112, v113
	global_store_dwordx4 v[106:107], v[116:119], off
	s_cbranch_vccnz .LBB0_291
	v_and_b32_e32 v109, 0x7fffffff, v103
	v_and_b32_e32 v108, 0x7fffffff, v102
	v_fma_f32 v108, v108, s18, 1.0
	v_fma_f32 v109, v109, s18, 1.0
	v_mov_b64_e32 v[110:111], s[22:23]
	v_rcp_f32_e32 v108, v108
	v_rcp_f32_e32 v109, v109
	v_mul_f32_e32 v114, v102, v102
	v_mul_f32_e32 v115, v103, v103
	v_cmp_gt_f32_e32 vcc, 0, v102
	v_mul_f32_e32 v114, s30, v114
	v_mul_f32_e32 v115, s30, v115
	v_fma_f32 v112, v108, s20, v110
	v_fma_f32 v113, v109, s20, v110
	v_exp_f32_e32 v114, v114
	v_fma_f32 v112, v108, v112, s24
	v_fma_f32 v113, v109, v113, s24
	v_exp_f32_e32 v115, v115
	v_fma_f32 v112, v108, v112, s26
	v_fma_f32 v113, v109, v113, s26
	s_nop 0
	v_fma_f32 v112, v108, v112, s28
	v_fma_f32 v113, v109, v113, s28
	s_nop 0
	v_mul_f32_e32 v108, v108, v112
	v_mul_f32_e32 v109, v109, v113
	v_mul_f32_e32 v112, v100, v100
	v_mul_f32_e32 v113, v101, v101
	v_mul_f32_e32 v108, v114, v108
	v_mul_f32_e32 v109, v115, v109
	v_mul_f32_e32 v112, s30, v112
	v_mul_f32_e32 v113, s30, v113
	v_mul_f32_e32 v114, v102, v108
	v_mul_f32_e32 v115, v103, v109
	v_fma_f32 v108, -v102, v108, v102
	v_fma_f32 v109, -v103, v109, v103
	v_exp_f32_e32 v112, v112
	v_cndmask_b32_e32 v102, v108, v114, vcc
	v_cmp_gt_f32_e32 vcc, 0, v103
	v_and_b32_e32 v108, 0x7fffffff, v100
	v_exp_f32_e32 v113, v113
	v_cndmask_b32_e32 v103, v109, v115, vcc
	v_and_b32_e32 v109, 0x7fffffff, v101
	v_fma_f32 v108, v108, s18, 1.0
	v_fma_f32 v109, v109, s18, 1.0
	v_cmp_gt_f32_e32 vcc, 0, v100
	v_rcp_f32_e32 v108, v108
	v_rcp_f32_e32 v109, v109
	s_nop 0
	v_fma_f32 v114, v108, s20, v110
	v_fma_f32 v115, v109, s20, v110
	s_nop 0
	v_fma_f32 v114, v108, v114, s24
	v_fma_f32 v115, v109, v115, s24
	s_nop 0
	v_fma_f32 v114, v108, v114, s26
	v_fma_f32 v115, v109, v115, s26
	s_nop 0
	v_fma_f32 v114, v108, v114, s28
	v_fma_f32 v115, v109, v115, s28
	s_nop 0
	v_mul_f32_e32 v108, v108, v114
	v_mul_f32_e32 v109, v109, v115
	v_mul_f32_e32 v114, v104, v104
	v_mul_f32_e32 v115, v105, v105
	v_mul_f32_e32 v108, v112, v108
	v_mul_f32_e32 v109, v113, v109
	v_mul_f32_e32 v114, s30, v114
	v_mul_f32_e32 v115, s30, v115
	v_mul_f32_e32 v112, v100, v108
	v_mul_f32_e32 v113, v101, v109
	v_fma_f32 v108, -v100, v108, v100
	v_fma_f32 v109, -v101, v109, v101
	v_exp_f32_e32 v114, v114
	v_cndmask_b32_e32 v100, v108, v112, vcc
	v_cmp_gt_f32_e32 vcc, 0, v101
	v_and_b32_e32 v108, 0x7fffffff, v104
	v_exp_f32_e32 v115, v115
	v_cndmask_b32_e32 v101, v109, v113, vcc
	v_and_b32_e32 v109, 0x7fffffff, v105
	v_fma_f32 v108, v108, s18, 1.0
	v_fma_f32 v109, v109, s18, 1.0
	v_cmp_gt_f32_e32 vcc, 0, v104
	v_rcp_f32_e32 v108, v108
	v_rcp_f32_e32 v109, v109
	s_nop 0
	v_fma_f32 v112, v108, s20, v110
	v_fma_f32 v113, v109, s20, v110
	s_nop 0
	v_fma_f32 v112, v108, v112, s24
	v_fma_f32 v113, v109, v113, s24
	s_nop 0
	v_fma_f32 v112, v108, v112, s26
	v_fma_f32 v113, v109, v113, s26
	s_nop 0
	v_fma_f32 v112, v108, v112, s28
	v_fma_f32 v113, v109, v113, s28
	s_nop 0
	v_mul_f32_e32 v108, v108, v112
	v_mul_f32_e32 v109, v109, v113
	v_mul_f32_e32 v112, v98, v98
	v_mul_f32_e32 v113, v99, v99
	v_mul_f32_e32 v108, v114, v108
	v_mul_f32_e32 v109, v115, v109
	s_nop 0
	v_mul_f32_e32 v114, v104, v108
	v_mul_f32_e32 v115, v105, v109
	v_fma_f32 v108, -v104, v108, v104
	v_fma_f32 v109, -v105, v109, v105
	s_nop 0
	v_cndmask_b32_e32 v104, v108, v114, vcc
	v_cmp_gt_f32_e32 vcc, 0, v105
	v_and_b32_e32 v108, 0x7fffffff, v98
	s_nop 0
	v_cndmask_b32_e32 v105, v109, v115, vcc
	v_and_b32_e32 v109, 0x7fffffff, v99
	v_fma_f32 v108, v108, s18, 1.0
	v_fma_f32 v109, v109, s18, 1.0
	v_cmp_gt_f32_e32 vcc, 0, v98
	v_rcp_f32_e32 v108, v108
	v_rcp_f32_e32 v109, v109
	s_nop 0
	v_fma_f32 v111, v109, s20, v110
	v_fma_f32 v110, v108, s20, v110
	s_nop 0
	v_fma_f32 v110, v108, v110, s24
	v_fma_f32 v111, v109, v111, s24
	s_nop 0
	v_fma_f32 v110, v108, v110, s26
	v_fma_f32 v111, v109, v111, s26
	s_nop 0
	v_fma_f32 v110, v108, v110, s28
	v_fma_f32 v111, v109, v111, s28
	s_nop 0
	v_mul_f32_e32 v108, v108, v110
	v_mul_f32_e32 v109, v109, v111
	v_mul_f32_e32 v110, s30, v112
	v_mul_f32_e32 v111, s30, v113
	s_nop 0
	v_exp_f32_e32 v110, v110
	v_exp_f32_e32 v111, v111
	s_nop 0
	v_mul_f32_e32 v108, v110, v108
	v_mul_f32_e32 v109, v111, v109
	s_nop 0
	v_mul_f32_e32 v110, v98, v108
	v_mul_f32_e32 v111, v99, v109
	v_fma_f32 v108, -v98, v108, v98
	v_fma_f32 v109, -v99, v109, v99
	s_nop 0
	v_cndmask_b32_e32 v98, v108, v110, vcc
	v_cmp_gt_f32_e32 vcc, 0, v99
	s_nop 1
	v_cndmask_b32_e32 v99, v109, v111, vcc
; __device__ __forceinline__ unsigned cvt_pk_bf16(float lo, float hi) { unsigned r; asm volatile("v_cvt_pk_bf16_f32 %0, %1, %2" : "=v"(r) : "v"(lo), "v"(hi)); return r; }
; __device__ __forceinline__ f32x2 gelu_pk(f32x2 v) {
;     const f32x2 av = __builtin_elementwise_abs(v), d = av * 0.2316418882f + 1.0f;
;     f32x2 t; t.x = __builtin_amdgcn_rcpf(d.x); t.y = __builtin_amdgcn_rcpf(d.y);
;     f32x2 q = t * 0.5307027145f + (-0.7265760135f); q = q * t + 0.7107068705f; q = q * t + (-0.142248368f); q = q * t + 0.127414796f; q = q * t;
;     const f32x2 s = (v * v) * (-0.72134752044f);
;     f32x2 e; e.x = __builtin_amdgcn_exp2f(s.x); e.y = __builtin_amdgcn_exp2f(s.y);
;     const f32x2 m = v * (q * e), r = v - m;
;     f32x2 o; o.x = v.x < 0.f ? m.x : r.x; o.y = v.y < 0.f ? m.y : r.y; return o;
;     __device__ __forceinline__ void operator()(const f32x4 (&acc)[2][2][4][2], const Unit& u, int wr, int wc, int fr, int fq) const {
;     ...
;             for (int m = 0; m < 4; ++m) { const int row = row0 + ai * HALF + m * 16; const float rsc = rsv[ai][m]; bf16_t* rowp = O + (size_t)row * ldc + col0;
; #pragma unroll
;                 for (int bj = 0; bj < 2; ++bj) { const i32x4 a0 = __builtin_bit_cast(i32x4, acc[ai][bj][m][0]), a1 = __builtin_bit_cast(i32x4, acc[ai][bj][m][1]);
;                     f32x4 v0 = (f32x4){(float)a0[0], (float)a0[1], (float)a0[2], (float)a0[3]} * rsc * cv[bj][0], v1 = (f32x4){(float)a1[0], (float)a1[1], (float)a1[2], (float)a1[3]} * rsc * cv[bj][1];
;                     if (act) { f32x2 a = gelu_pk((f32x2){v0[0], v0[1]}), b = gelu_pk((f32x2){v0[2], v0[3]}), c = gelu_pk((f32x2){v1[0], v1[1]}), d = gelu_pk((f32x2){v1[2], v1[3]});
;                         v0 = (f32x4){a.x, a.y, b.x, b.y}; v1 = (f32x4){c.x, c.y, d.x, d.y}; }
;                     u32x4 w; w.x = cvt_pk_bf16(v0[0], v0[1]); w.y = cvt_pk_bf16(v0[2], v0[3]); w.z = cvt_pk_bf16(v1[0], v1[1]); w.w = cvt_pk_bf16(v1[2], v1[3]);
;                     if (nt) __builtin_nontemporal_store(w, (u32x4*)(rowp + bj * HALF)); else *(u32x4*)(rowp + bj * HALF) = w; } }
.LBB0_291:
	v_cvt_f32_i32_e32 v97, v97
	v_cvt_f32_i32_e32 v96, v96
	v_cvt_pk_bf16_f32 v102, v102, v103
	v_cvt_pk_bf16_f32 v103, v100, v101
	v_cvt_pk_bf16_f32 v104, v104, v105
	v_cvt_f32_i32_e32 v95, v95
	v_cvt_f32_i32_e32 v94, v94
	v_cvt_pk_bf16_f32 v105, v98, v99
	v_cvt_f32_i32_e32 v99, v93
	v_cvt_f32_i32_e32 v91, v91
	v_cvt_f32_i32_e32 v90, v90
	v_cvt_f32_i32_e32 v98, v92
	v_mul_f32_e32 v96, v180, v96
	v_mul_f32_e32 v97, v180, v97
	v_mul_f32_e32 v94, v180, v94
	v_mul_f32_e32 v95, v180, v95
	v_mul_f32_e32 v92, v40, v96
	v_mul_f32_e32 v93, v41, v97
	v_mul_f32_e32 v90, v180, v90
	v_mul_f32_e32 v91, v180, v91
	v_mul_f32_e32 v96, v180, v98
	v_mul_f32_e32 v97, v180, v99
	v_mul_f32_e32 v94, v38, v94
	v_mul_f32_e32 v95, v39, v95
	v_mul_f32_e32 v96, v36, v96
	v_mul_f32_e32 v97, v37, v97
	s_and_b64 vcc, exec, s[4:5]
	v_mul_f32_e32 v98, v34, v90
	v_mul_f32_e32 v99, v35, v91
	global_store_dwordx4 v[106:107], v[102:105], off offset:256
	s_cbranch_vccnz .LBB0_293
	v_and_b32_e32 v91, 0x7fffffff, v95
	v_and_b32_e32 v90, 0x7fffffff, v94
	v_fma_f32 v90, v90, s18, 1.0
	v_fma_f32 v91, v91, s18, 1.0
	v_mov_b64_e32 v[100:101], s[22:23]
	v_rcp_f32_e32 v90, v90
	v_rcp_f32_e32 v91, v91
	v_mul_f32_e32 v104, v94, v94
	v_mul_f32_e32 v105, v95, v95
	v_cmp_gt_f32_e32 vcc, 0, v94
	v_mul_f32_e32 v104, s30, v104
	v_mul_f32_e32 v105, s30, v105
	v_fma_f32 v102, v90, s20, v100
	v_fma_f32 v103, v91, s20, v100
	v_exp_f32_e32 v104, v104
	v_fma_f32 v102, v90, v102, s24
	v_fma_f32 v103, v91, v103, s24
	v_exp_f32_e32 v105, v105
	v_fma_f32 v102, v90, v102, s26
	v_fma_f32 v103, v91, v103, s26
	s_nop 0
	v_fma_f32 v102, v90, v102, s28
	v_fma_f32 v103, v91, v103, s28
	s_nop 0
	v_mul_f32_e32 v90, v90, v102
	v_mul_f32_e32 v91, v91, v103
	v_mul_f32_e32 v102, v92, v92
	v_mul_f32_e32 v103, v93, v93
	v_mul_f32_e32 v90, v104, v90
	v_mul_f32_e32 v91, v105, v91
	v_mul_f32_e32 v102, s30, v102
	v_mul_f32_e32 v103, s30, v103
	v_mul_f32_e32 v104, v94, v90
	v_mul_f32_e32 v105, v95, v91
	v_fma_f32 v90, -v94, v90, v94
	v_fma_f32 v91, -v95, v91, v95
	v_exp_f32_e32 v102, v102
	v_cndmask_b32_e32 v94, v90, v104, vcc
	v_cmp_gt_f32_e32 vcc, 0, v95
	v_and_b32_e32 v90, 0x7fffffff, v92
	v_exp_f32_e32 v103, v103
	v_cndmask_b32_e32 v95, v91, v105, vcc
	v_and_b32_e32 v91, 0x7fffffff, v93
	v_fma_f32 v90, v90, s18, 1.0
	v_fma_f32 v91, v91, s18, 1.0
	v_cmp_gt_f32_e32 vcc, 0, v92
	v_rcp_f32_e32 v90, v90
	v_rcp_f32_e32 v91, v91
	s_nop 0
	v_fma_f32 v104, v90, s20, v100
	v_fma_f32 v105, v91, s20, v100
	s_nop 0
	v_fma_f32 v104, v90, v104, s24
	v_fma_f32 v105, v91, v105, s24
	s_nop 0
	v_fma_f32 v104, v90, v104, s26
	v_fma_f32 v105, v91, v105, s26
	s_nop 0
	v_fma_f32 v104, v90, v104, s28
	v_fma_f32 v105, v91, v105, s28
	s_nop 0
	v_mul_f32_e32 v90, v90, v104
	v_mul_f32_e32 v91, v91, v105
	v_mul_f32_e32 v104, v98, v98
	v_mul_f32_e32 v105, v99, v99
	v_mul_f32_e32 v90, v102, v90
	v_mul_f32_e32 v91, v103, v91
	v_mul_f32_e32 v104, s30, v104
	v_mul_f32_e32 v105, s30, v105
	v_mul_f32_e32 v102, v92, v90
	v_mul_f32_e32 v103, v93, v91
	v_fma_f32 v90, -v92, v90, v92
	v_fma_f32 v91, -v93, v91, v93
	v_exp_f32_e32 v104, v104
	v_cndmask_b32_e32 v92, v90, v102, vcc
	v_cmp_gt_f32_e32 vcc, 0, v93
	v_and_b32_e32 v90, 0x7fffffff, v98
	v_exp_f32_e32 v105, v105
	v_cndmask_b32_e32 v93, v91, v103, vcc
	v_and_b32_e32 v91, 0x7fffffff, v99
	v_fma_f32 v90, v90, s18, 1.0
	v_fma_f32 v91, v91, s18, 1.0
	v_cmp_gt_f32_e32 vcc, 0, v98
	v_rcp_f32_e32 v90, v90
	v_rcp_f32_e32 v91, v91
	s_nop 0
	v_fma_f32 v102, v90, s20, v100
	v_fma_f32 v103, v91, s20, v100
	s_nop 0
	v_fma_f32 v102, v90, v102, s24
	v_fma_f32 v103, v91, v103, s24
	s_nop 0
	v_fma_f32 v102, v90, v102, s26
	v_fma_f32 v103, v91, v103, s26
	s_nop 0
	v_fma_f32 v102, v90, v102, s28
	v_fma_f32 v103, v91, v103, s28
	s_nop 0
	v_mul_f32_e32 v90, v90, v102
	v_mul_f32_e32 v91, v91, v103
	v_mul_f32_e32 v102, v96, v96
	v_mul_f32_e32 v103, v97, v97
	v_mul_f32_e32 v90, v104, v90
	v_mul_f32_e32 v91, v105, v91
	s_nop 0
	v_mul_f32_e32 v104, v98, v90
	v_mul_f32_e32 v105, v99, v91
	v_fma_f32 v90, -v98, v90, v98
	v_fma_f32 v91, -v99, v91, v99
	s_nop 0
	v_cndmask_b32_e32 v98, v90, v104, vcc
	v_cmp_gt_f32_e32 vcc, 0, v99
	v_and_b32_e32 v90, 0x7fffffff, v96
	s_nop 0
	v_cndmask_b32_e32 v99, v91, v105, vcc
	v_and_b32_e32 v91, 0x7fffffff, v97
	v_fma_f32 v90, v90, s18, 1.0
	v_fma_f32 v91, v91, s18, 1.0
	v_cmp_gt_f32_e32 vcc, 0, v96
	v_rcp_f32_e32 v90, v90
	v_rcp_f32_e32 v91, v91
	s_nop 0
	v_fma_f32 v101, v91, s20, v100
	v_fma_f32 v100, v90, s20, v100
	s_nop 0
	v_fma_f32 v100, v90, v100, s24
	v_fma_f32 v101, v91, v101, s24
	s_nop 0
	v_fma_f32 v100, v90, v100, s26
	v_fma_f32 v101, v91, v101, s26
	s_nop 0
	v_fma_f32 v100, v90, v100, s28
	v_fma_f32 v101, v91, v101, s28
	s_nop 0
	v_mul_f32_e32 v90, v90, v100
	v_mul_f32_e32 v91, v91, v101
	v_mul_f32_e32 v100, s30, v102
	v_mul_f32_e32 v101, s30, v103
	s_nop 0
	v_exp_f32_e32 v100, v100
	v_exp_f32_e32 v101, v101
	s_nop 0
	v_mul_f32_e32 v90, v100, v90
	v_mul_f32_e32 v91, v101, v91
	s_nop 0
	v_mul_f32_e32 v100, v96, v90
	v_mul_f32_e32 v101, v97, v91
	v_fma_f32 v90, -v96, v90, v96
	v_fma_f32 v91, -v97, v91, v97
	s_nop 0
	v_cndmask_b32_e32 v96, v90, v100, vcc
	v_cmp_gt_f32_e32 vcc, 0, v97
	s_nop 1
	v_cndmask_b32_e32 v97, v91, v101, vcc
; __device__ __forceinline__ unsigned cvt_pk_bf16(float lo, float hi) { unsigned r; asm volatile("v_cvt_pk_bf16_f32 %0, %1, %2" : "=v"(r) : "v"(lo), "v"(hi)); return r; }
; __device__ __forceinline__ f32x2 gelu_pk(f32x2 v) {
;     const f32x2 av = __builtin_elementwise_abs(v), d = av * 0.2316418882f + 1.0f;
;     f32x2 t; t.x = __builtin_amdgcn_rcpf(d.x); t.y = __builtin_amdgcn_rcpf(d.y);
;     f32x2 q = t * 0.5307027145f + (-0.7265760135f); q = q * t + 0.7107068705f; q = q * t + (-0.142248368f); q = q * t + 0.127414796f; q = q * t;
;     const f32x2 s = (v * v) * (-0.72134752044f);
;     f32x2 e; e.x = __builtin_amdgcn_exp2f(s.x); e.y = __builtin_amdgcn_exp2f(s.y);
;     const f32x2 m = v * (q * e), r = v - m;
;     f32x2 o; o.x = v.x < 0.f ? m.x : r.x; o.y = v.y < 0.f ? m.y : r.y; return o;
;     __device__ __forceinline__ void operator()(const f32x4 (&acc)[2][2][4][2], const Unit& u, int wr, int wc, int fr, int fq) const {
;     ...
;             for (int m = 0; m < 4; ++m) { const int row = row0 + ai * HALF + m * 16; const float rsc = rsv[ai][m]; bf16_t* rowp = O + (size_t)row * ldc + col0;
; #pragma unroll
;                 for (int bj = 0; bj < 2; ++bj) { const i32x4 a0 = __builtin_bit_cast(i32x4, acc[ai][bj][m][0]), a1 = __builtin_bit_cast(i32x4, acc[ai][bj][m][1]);
;                     f32x4 v0 = (f32x4){(float)a0[0], (float)a0[1], (float)a0[2], (float)a0[3]} * rsc * cv[bj][0], v1 = (f32x4){(float)a1[0], (float)a1[1], (float)a1[2], (float)a1[3]} * rsc * cv[bj][1];
;                     if (act) { f32x2 a = gelu_pk((f32x2){v0[0], v0[1]}), b = gelu_pk((f32x2){v0[2], v0[3]}), c = gelu_pk((f32x2){v1[0], v1[1]}), d = gelu_pk((f32x2){v1[2], v1[3]});
;                         v0 = (f32x4){a.x, a.y, b.x, b.y}; v1 = (f32x4){c.x, c.y, d.x, d.y}; }
;                     u32x4 w; w.x = cvt_pk_bf16(v0[0], v0[1]); w.y = cvt_pk_bf16(v0[2], v0[3]); w.z = cvt_pk_bf16(v1[0], v1[1]); w.w = cvt_pk_bf16(v1[2], v1[3]);
;                     if (nt) __builtin_nontemporal_store(w, (u32x4*)(rowp + bj * HALF)); else *(u32x4*)(rowp + bj * HALF) = w; } }
.LBB0_293:
	v_cvt_f32_i32_e32 v89, v89
	v_cvt_f32_i32_e32 v88, v88
	v_cvt_pk_bf16_f32 v100, v94, v95
	v_cvt_f32_i32_e32 v87, v87
	v_cvt_f32_i32_e32 v86, v86
	v_cvt_f32_i32_e32 v83, v83
	v_cvt_f32_i32_e32 v95, v85
	v_cvt_f32_i32_e32 v94, v84
	v_cvt_f32_i32_e32 v82, v82
	v_cvt_pk_bf16_f32 v101, v92, v93
	v_mov_b32_e32 v92, v180
	v_mov_b32_e32 v93, v180
	v_mov_b32_e32 v181, v180
	v_mov_b64_e32 v[90:91], s[66:67]
	v_mul_f32_e32 v88, v92, v88
	v_mul_f32_e32 v89, v93, v89
	v_mad_i64_i32 v[90:91], s[42:43], v182, s86, v[90:91]
	v_mul_f32_e32 v86, v180, v86
	v_mul_f32_e32 v87, v181, v87
	v_mul_f32_e32 v84, v32, v88
	v_mul_f32_e32 v85, v33, v89
	v_mul_f32_e32 v88, v92, v94
	v_mul_f32_e32 v89, v93, v95
	v_mul_f32_e32 v92, v180, v82
	v_mul_f32_e32 v93, v181, v83
	v_lshl_add_u64 v[90:91], v[170:171], 1, v[90:91]
	v_mul_f32_e32 v86, v30, v86
	v_mul_f32_e32 v87, v31, v87
	v_mul_f32_e32 v82, v24, v88
	v_mul_f32_e32 v83, v25, v89
	s_and_b64 vcc, exec, s[4:5]
	v_mul_f32_e32 v88, v22, v92
	v_mul_f32_e32 v89, v23, v93
	v_cvt_pk_bf16_f32 v102, v98, v99
	v_cvt_pk_bf16_f32 v103, v96, v97
	global_store_dwordx4 v[90:91], v[100:103], off
	s_cbranch_vccnz .LBB0_295
	v_and_b32_e32 v93, 0x7fffffff, v87
	v_and_b32_e32 v92, 0x7fffffff, v86
	v_fma_f32 v92, v92, s18, 1.0
	v_fma_f32 v93, v93, s18, 1.0
	v_mov_b64_e32 v[94:95], s[22:23]
	v_rcp_f32_e32 v92, v92
	v_rcp_f32_e32 v93, v93
	v_mul_f32_e32 v98, v86, v86
	v_mul_f32_e32 v99, v87, v87
	v_cmp_gt_f32_e32 vcc, 0, v86
	v_mul_f32_e32 v98, s30, v98
	v_mul_f32_e32 v99, s30, v99
	v_fma_f32 v96, v92, s20, v94
	v_fma_f32 v97, v93, s20, v94
	v_exp_f32_e32 v98, v98
	v_fma_f32 v96, v92, v96, s24
	v_fma_f32 v97, v93, v97, s24
	v_exp_f32_e32 v99, v99
	v_fma_f32 v96, v92, v96, s26
	v_fma_f32 v97, v93, v97, s26
	s_nop 0
	v_fma_f32 v96, v92, v96, s28
	v_fma_f32 v97, v93, v97, s28
	s_nop 0
	v_mul_f32_e32 v92, v92, v96
	v_mul_f32_e32 v93, v93, v97
	v_mul_f32_e32 v96, v84, v84
	v_mul_f32_e32 v97, v85, v85
	v_mul_f32_e32 v92, v98, v92
	v_mul_f32_e32 v93, v99, v93
	v_mul_f32_e32 v96, s30, v96
	v_mul_f32_e32 v97, s30, v97
	v_mul_f32_e32 v98, v86, v92
	v_mul_f32_e32 v99, v87, v93
	v_fma_f32 v92, -v86, v92, v86
	v_fma_f32 v93, -v87, v93, v87
	v_exp_f32_e32 v96, v96
	v_cndmask_b32_e32 v86, v92, v98, vcc
	v_cmp_gt_f32_e32 vcc, 0, v87
	v_and_b32_e32 v92, 0x7fffffff, v84
	v_exp_f32_e32 v97, v97
	v_cndmask_b32_e32 v87, v93, v99, vcc
	v_and_b32_e32 v93, 0x7fffffff, v85
	v_fma_f32 v92, v92, s18, 1.0
	v_fma_f32 v93, v93, s18, 1.0
	v_cmp_gt_f32_e32 vcc, 0, v84
	v_rcp_f32_e32 v92, v92
	v_rcp_f32_e32 v93, v93
	s_nop 0
	v_fma_f32 v98, v92, s20, v94
	v_fma_f32 v99, v93, s20, v94
	s_nop 0
	v_fma_f32 v98, v92, v98, s24
	v_fma_f32 v99, v93, v99, s24
	s_nop 0
	v_fma_f32 v98, v92, v98, s26
	v_fma_f32 v99, v93, v99, s26
	s_nop 0
	v_fma_f32 v98, v92, v98, s28
	v_fma_f32 v99, v93, v99, s28
	s_nop 0
	v_mul_f32_e32 v92, v92, v98
	v_mul_f32_e32 v93, v93, v99
	v_mul_f32_e32 v98, v88, v88
	v_mul_f32_e32 v99, v89, v89
	v_mul_f32_e32 v92, v96, v92
	v_mul_f32_e32 v93, v97, v93
	v_mul_f32_e32 v98, s30, v98
	v_mul_f32_e32 v99, s30, v99
	v_mul_f32_e32 v96, v84, v92
	v_mul_f32_e32 v97, v85, v93
	v_fma_f32 v92, -v84, v92, v84
	v_fma_f32 v93, -v85, v93, v85
	v_exp_f32_e32 v98, v98
	v_cndmask_b32_e32 v84, v92, v96, vcc
	v_cmp_gt_f32_e32 vcc, 0, v85
	v_and_b32_e32 v92, 0x7fffffff, v88
	v_exp_f32_e32 v99, v99
	v_cndmask_b32_e32 v85, v93, v97, vcc
	v_and_b32_e32 v93, 0x7fffffff, v89
	v_fma_f32 v92, v92, s18, 1.0
	v_fma_f32 v93, v93, s18, 1.0
	v_cmp_gt_f32_e32 vcc, 0, v88
	v_rcp_f32_e32 v92, v92
	v_rcp_f32_e32 v93, v93
	s_nop 0
	v_fma_f32 v96, v92, s20, v94
	v_fma_f32 v97, v93, s20, v94
	s_nop 0
	v_fma_f32 v96, v92, v96, s24
	v_fma_f32 v97, v93, v97, s24
	s_nop 0
	v_fma_f32 v96, v92, v96, s26
	v_fma_f32 v97, v93, v97, s26
	s_nop 0
	v_fma_f32 v96, v92, v96, s28
	v_fma_f32 v97, v93, v97, s28
	s_nop 0
	v_mul_f32_e32 v92, v92, v96
	v_mul_f32_e32 v93, v93, v97
	v_mul_f32_e32 v96, v82, v82
	v_mul_f32_e32 v97, v83, v83
	v_mul_f32_e32 v92, v98, v92
	v_mul_f32_e32 v93, v99, v93
	s_nop 0
	v_mul_f32_e32 v98, v88, v92
	v_mul_f32_e32 v99, v89, v93
	v_fma_f32 v92, -v88, v92, v88
	v_fma_f32 v93, -v89, v93, v89
	s_nop 0
	v_cndmask_b32_e32 v88, v92, v98, vcc
	v_cmp_gt_f32_e32 vcc, 0, v89
	v_and_b32_e32 v92, 0x7fffffff, v82
	s_nop 0
	v_cndmask_b32_e32 v89, v93, v99, vcc
	v_and_b32_e32 v93, 0x7fffffff, v83
	v_fma_f32 v92, v92, s18, 1.0
	v_fma_f32 v93, v93, s18, 1.0
	v_cmp_gt_f32_e32 vcc, 0, v82
	v_rcp_f32_e32 v92, v92
	v_rcp_f32_e32 v93, v93
	s_nop 0
	v_fma_f32 v95, v93, s20, v94
	v_fma_f32 v94, v92, s20, v94
	s_nop 0
	v_fma_f32 v94, v92, v94, s24
	v_fma_f32 v95, v93, v95, s24
	s_nop 0
	v_fma_f32 v94, v92, v94, s26
	v_fma_f32 v95, v93, v95, s26
	s_nop 0
	v_fma_f32 v94, v92, v94, s28
	v_fma_f32 v95, v93, v95, s28
	s_nop 0
	v_mul_f32_e32 v92, v92, v94
	v_mul_f32_e32 v93, v93, v95
	v_mul_f32_e32 v94, s30, v96
	v_mul_f32_e32 v95, s30, v97
	s_nop 0
	v_exp_f32_e32 v94, v94
	v_exp_f32_e32 v95, v95
	s_nop 0
	v_mul_f32_e32 v92, v94, v92
	v_mul_f32_e32 v93, v95, v93
	s_nop 0
	v_mul_f32_e32 v94, v82, v92
	v_mul_f32_e32 v95, v83, v93
	v_fma_f32 v92, -v82, v92, v82
	v_fma_f32 v93, -v83, v93, v83
	s_nop 0
	v_cndmask_b32_e32 v82, v92, v94, vcc
	v_cmp_gt_f32_e32 vcc, 0, v83
	s_nop 1
	v_cndmask_b32_e32 v83, v93, v95, vcc
; __device__ __forceinline__ unsigned cvt_pk_bf16(float lo, float hi) { unsigned r; asm volatile("v_cvt_pk_bf16_f32 %0, %1, %2" : "=v"(r) : "v"(lo), "v"(hi)); return r; }
; __device__ __forceinline__ f32x2 gelu_pk(f32x2 v) {
;     const f32x2 av = __builtin_elementwise_abs(v), d = av * 0.2316418882f + 1.0f;
;     f32x2 t; t.x = __builtin_amdgcn_rcpf(d.x); t.y = __builtin_amdgcn_rcpf(d.y);
;     f32x2 q = t * 0.5307027145f + (-0.7265760135f); q = q * t + 0.7107068705f; q = q * t + (-0.142248368f); q = q * t + 0.127414796f; q = q * t;
;     const f32x2 s = (v * v) * (-0.72134752044f);
;     f32x2 e; e.x = __builtin_amdgcn_exp2f(s.x); e.y = __builtin_amdgcn_exp2f(s.y);
;     const f32x2 m = v * (q * e), r = v - m;
;     f32x2 o; o.x = v.x < 0.f ? m.x : r.x; o.y = v.y < 0.f ? m.y : r.y; return o;
;     __device__ __forceinline__ void operator()(const f32x4 (&acc)[2][2][4][2], const Unit& u, int wr, int wc, int fr, int fq) const {
;     ...
;             for (int m = 0; m < 4; ++m) { const int row = row0 + ai * HALF + m * 16; const float rsc = rsv[ai][m]; bf16_t* rowp = O + (size_t)row * ldc + col0;
; #pragma unroll
;                 for (int bj = 0; bj < 2; ++bj) { const i32x4 a0 = __builtin_bit_cast(i32x4, acc[ai][bj][m][0]), a1 = __builtin_bit_cast(i32x4, acc[ai][bj][m][1]);
;                     f32x4 v0 = (f32x4){(float)a0[0], (float)a0[1], (float)a0[2], (float)a0[3]} * rsc * cv[bj][0], v1 = (f32x4){(float)a1[0], (float)a1[1], (float)a1[2], (float)a1[3]} * rsc * cv[bj][1];
;                     if (act) { f32x2 a = gelu_pk((f32x2){v0[0], v0[1]}), b = gelu_pk((f32x2){v0[2], v0[3]}), c = gelu_pk((f32x2){v1[0], v1[1]}), d = gelu_pk((f32x2){v1[2], v1[3]});
;                         v0 = (f32x4){a.x, a.y, b.x, b.y}; v1 = (f32x4){c.x, c.y, d.x, d.y}; }
;                     u32x4 w; w.x = cvt_pk_bf16(v0[0], v0[1]); w.y = cvt_pk_bf16(v0[2], v0[3]); w.z = cvt_pk_bf16(v1[0], v1[1]); w.w = cvt_pk_bf16(v1[2], v1[3]);
;                     if (nt) __builtin_nontemporal_store(w, (u32x4*)(rowp + bj * HALF)); else *(u32x4*)(rowp + bj * HALF) = w; } }
.LBB0_295:
	v_cvt_f32_i32_e32 v81, v81
	v_cvt_f32_i32_e32 v80, v80
	v_cvt_pk_bf16_f32 v86, v86, v87
	v_cvt_pk_bf16_f32 v87, v84, v85
	v_cvt_pk_bf16_f32 v88, v88, v89
	v_cvt_f32_i32_e32 v79, v79
	v_cvt_f32_i32_e32 v78, v78
	v_cvt_pk_bf16_f32 v89, v82, v83
	v_cvt_f32_i32_e32 v83, v77
	v_cvt_f32_i32_e32 v75, v75
	v_cvt_f32_i32_e32 v74, v74
	v_cvt_f32_i32_e32 v82, v76
	v_mul_f32_e32 v80, v178, v80
	v_mul_f32_e32 v81, v178, v81
	v_mul_f32_e32 v78, v178, v78
	v_mul_f32_e32 v79, v178, v79
	v_mul_f32_e32 v76, v40, v80
	v_mul_f32_e32 v77, v41, v81
	v_mul_f32_e32 v74, v178, v74
	v_mul_f32_e32 v75, v178, v75
	v_mul_f32_e32 v80, v178, v82
	v_mul_f32_e32 v81, v178, v83
	v_mul_f32_e32 v78, v38, v78
	v_mul_f32_e32 v79, v39, v79
	v_mul_f32_e32 v80, v36, v80
	v_mul_f32_e32 v81, v37, v81
	s_and_b64 vcc, exec, s[4:5]
	v_mul_f32_e32 v82, v34, v74
	v_mul_f32_e32 v83, v35, v75
	global_store_dwordx4 v[90:91], v[86:89], off offset:256
	s_cbranch_vccnz .LBB0_297
	v_and_b32_e32 v75, 0x7fffffff, v79
	v_and_b32_e32 v74, 0x7fffffff, v78
	v_fma_f32 v74, v74, s18, 1.0
	v_fma_f32 v75, v75, s18, 1.0
	v_mov_b64_e32 v[84:85], s[22:23]
	v_rcp_f32_e32 v74, v74
	v_rcp_f32_e32 v75, v75
	v_mul_f32_e32 v88, v78, v78
	v_mul_f32_e32 v89, v79, v79
	v_cmp_gt_f32_e32 vcc, 0, v78
	v_mul_f32_e32 v88, s30, v88
	v_mul_f32_e32 v89, s30, v89
	v_fma_f32 v86, v74, s20, v84
	v_fma_f32 v87, v75, s20, v84
	v_exp_f32_e32 v88, v88
	v_fma_f32 v86, v74, v86, s24
	v_fma_f32 v87, v75, v87, s24
	v_exp_f32_e32 v89, v89
	v_fma_f32 v86, v74, v86, s26
	v_fma_f32 v87, v75, v87, s26
	s_nop 0
	v_fma_f32 v86, v74, v86, s28
	v_fma_f32 v87, v75, v87, s28
	s_nop 0
	v_mul_f32_e32 v74, v74, v86
	v_mul_f32_e32 v75, v75, v87
	v_mul_f32_e32 v86, v76, v76
	v_mul_f32_e32 v87, v77, v77
	v_mul_f32_e32 v74, v88, v74
	v_mul_f32_e32 v75, v89, v75
	v_mul_f32_e32 v86, s30, v86
	v_mul_f32_e32 v87, s30, v87
	v_mul_f32_e32 v88, v78, v74
	v_mul_f32_e32 v89, v79, v75
	v_fma_f32 v74, -v78, v74, v78
	v_fma_f32 v75, -v79, v75, v79
	v_exp_f32_e32 v86, v86
	v_cndmask_b32_e32 v78, v74, v88, vcc
	v_cmp_gt_f32_e32 vcc, 0, v79
	v_and_b32_e32 v74, 0x7fffffff, v76
	v_exp_f32_e32 v87, v87
	v_cndmask_b32_e32 v79, v75, v89, vcc
	v_and_b32_e32 v75, 0x7fffffff, v77
	v_fma_f32 v74, v74, s18, 1.0
	v_fma_f32 v75, v75, s18, 1.0
	v_cmp_gt_f32_e32 vcc, 0, v76
	v_rcp_f32_e32 v74, v74
	v_rcp_f32_e32 v75, v75
	s_nop 0
	v_fma_f32 v88, v74, s20, v84
	v_fma_f32 v89, v75, s20, v84
	s_nop 0
	v_fma_f32 v88, v74, v88, s24
	v_fma_f32 v89, v75, v89, s24
	s_nop 0
	v_fma_f32 v88, v74, v88, s26
	v_fma_f32 v89, v75, v89, s26
	s_nop 0
	v_fma_f32 v88, v74, v88, s28
	v_fma_f32 v89, v75, v89, s28
	s_nop 0
	v_mul_f32_e32 v74, v74, v88
	v_mul_f32_e32 v75, v75, v89
	v_mul_f32_e32 v88, v82, v82
	v_mul_f32_e32 v89, v83, v83
	v_mul_f32_e32 v74, v86, v74
	v_mul_f32_e32 v75, v87, v75
	v_mul_f32_e32 v88, s30, v88
	v_mul_f32_e32 v89, s30, v89
	v_mul_f32_e32 v86, v76, v74
	v_mul_f32_e32 v87, v77, v75
	v_fma_f32 v74, -v76, v74, v76
	v_fma_f32 v75, -v77, v75, v77
	v_exp_f32_e32 v88, v88
	v_cndmask_b32_e32 v76, v74, v86, vcc
	v_cmp_gt_f32_e32 vcc, 0, v77
	v_and_b32_e32 v74, 0x7fffffff, v82
	v_exp_f32_e32 v89, v89
	v_cndmask_b32_e32 v77, v75, v87, vcc
	v_and_b32_e32 v75, 0x7fffffff, v83
	v_fma_f32 v74, v74, s18, 1.0
	v_fma_f32 v75, v75, s18, 1.0
	v_cmp_gt_f32_e32 vcc, 0, v82
	v_rcp_f32_e32 v74, v74
	v_rcp_f32_e32 v75, v75
	s_nop 0
	v_fma_f32 v86, v74, s20, v84
	v_fma_f32 v87, v75, s20, v84
	s_nop 0
	v_fma_f32 v86, v74, v86, s24
	v_fma_f32 v87, v75, v87, s24
	s_nop 0
	v_fma_f32 v86, v74, v86, s26
	v_fma_f32 v87, v75, v87, s26
	s_nop 0
	v_fma_f32 v86, v74, v86, s28
	v_fma_f32 v87, v75, v87, s28
	s_nop 0
	v_mul_f32_e32 v74, v74, v86
	v_mul_f32_e32 v75, v75, v87
	v_mul_f32_e32 v86, v80, v80
	v_mul_f32_e32 v87, v81, v81
	v_mul_f32_e32 v74, v88, v74
	v_mul_f32_e32 v75, v89, v75
	s_nop 0
	v_mul_f32_e32 v88, v82, v74
	v_mul_f32_e32 v89, v83, v75
	v_fma_f32 v74, -v82, v74, v82
	v_fma_f32 v75, -v83, v75, v83
	s_nop 0
	v_cndmask_b32_e32 v82, v74, v88, vcc
	v_cmp_gt_f32_e32 vcc, 0, v83
	v_and_b32_e32 v74, 0x7fffffff, v80
	s_nop 0
	v_cndmask_b32_e32 v83, v75, v89, vcc
	v_and_b32_e32 v75, 0x7fffffff, v81
	v_fma_f32 v74, v74, s18, 1.0
	v_fma_f32 v75, v75, s18, 1.0
	v_cmp_gt_f32_e32 vcc, 0, v80
	v_rcp_f32_e32 v74, v74
	v_rcp_f32_e32 v75, v75
	s_nop 0
	v_fma_f32 v85, v75, s20, v84
	v_fma_f32 v84, v74, s20, v84
	s_nop 0
	v_fma_f32 v84, v74, v84, s24
	v_fma_f32 v85, v75, v85, s24
	s_nop 0
	v_fma_f32 v84, v74, v84, s26
	v_fma_f32 v85, v75, v85, s26
	s_nop 0
	v_fma_f32 v84, v74, v84, s28
	v_fma_f32 v85, v75, v85, s28
	s_nop 0
	v_mul_f32_e32 v74, v74, v84
	v_mul_f32_e32 v75, v75, v85
	v_mul_f32_e32 v84, s30, v86
	v_mul_f32_e32 v85, s30, v87
	s_nop 0
	v_exp_f32_e32 v84, v84
	v_exp_f32_e32 v85, v85
	s_nop 0
	v_mul_f32_e32 v74, v84, v74
	v_mul_f32_e32 v75, v85, v75
	s_nop 0
	v_mul_f32_e32 v84, v80, v74
	v_mul_f32_e32 v85, v81, v75
	v_fma_f32 v74, -v80, v74, v80
	v_fma_f32 v75, -v81, v75, v81
	s_nop 0
	v_cndmask_b32_e32 v80, v74, v84, vcc
	v_cmp_gt_f32_e32 vcc, 0, v81
	s_nop 1
	v_cndmask_b32_e32 v81, v75, v85, vcc
; __device__ __forceinline__ unsigned cvt_pk_bf16(float lo, float hi) { unsigned r; asm volatile("v_cvt_pk_bf16_f32 %0, %1, %2" : "=v"(r) : "v"(lo), "v"(hi)); return r; }
; __device__ __forceinline__ f32x2 gelu_pk(f32x2 v) {
;     const f32x2 av = __builtin_elementwise_abs(v), d = av * 0.2316418882f + 1.0f;
;     f32x2 t; t.x = __builtin_amdgcn_rcpf(d.x); t.y = __builtin_amdgcn_rcpf(d.y);
;     f32x2 q = t * 0.5307027145f + (-0.7265760135f); q = q * t + 0.7107068705f; q = q * t + (-0.142248368f); q = q * t + 0.127414796f; q = q * t;
;     const f32x2 s = (v * v) * (-0.72134752044f);
;     f32x2 e; e.x = __builtin_amdgcn_exp2f(s.x); e.y = __builtin_amdgcn_exp2f(s.y);
;     const f32x2 m = v * (q * e), r = v - m;
;     f32x2 o; o.x = v.x < 0.f ? m.x : r.x; o.y = v.y < 0.f ? m.y : r.y; return o;
;     __device__ __forceinline__ void operator()(const f32x4 (&acc)[2][2][4][2], const Unit& u, int wr, int wc, int fr, int fq) const {
;     ...
;             for (int m = 0; m < 4; ++m) { const int row = row0 + ai * HALF + m * 16; const float rsc = rsv[ai][m]; bf16_t* rowp = O + (size_t)row * ldc + col0;
; #pragma unroll
;                 for (int bj = 0; bj < 2; ++bj) { const i32x4 a0 = __builtin_bit_cast(i32x4, acc[ai][bj][m][0]), a1 = __builtin_bit_cast(i32x4, acc[ai][bj][m][1]);
;                     f32x4 v0 = (f32x4){(float)a0[0], (float)a0[1], (float)a0[2], (float)a0[3]} * rsc * cv[bj][0], v1 = (f32x4){(float)a1[0], (float)a1[1], (float)a1[2], (float)a1[3]} * rsc * cv[bj][1];
;                     if (act) { f32x2 a = gelu_pk((f32x2){v0[0], v0[1]}), b = gelu_pk((f32x2){v0[2], v0[3]}), c = gelu_pk((f32x2){v1[0], v1[1]}), d = gelu_pk((f32x2){v1[2], v1[3]});
;                         v0 = (f32x4){a.x, a.y, b.x, b.y}; v1 = (f32x4){c.x, c.y, d.x, d.y}; }
;                     u32x4 w; w.x = cvt_pk_bf16(v0[0], v0[1]); w.y = cvt_pk_bf16(v0[2], v0[3]); w.z = cvt_pk_bf16(v1[0], v1[1]); w.w = cvt_pk_bf16(v1[2], v1[3]);
;                     if (nt) __builtin_nontemporal_store(w, (u32x4*)(rowp + bj * HALF)); else *(u32x4*)(rowp + bj * HALF) = w; } }
.LBB0_297:
	v_add_u32_e32 v84, 0x80, v172
	v_mov_b64_e32 v[74:75], s[66:67]
	v_cvt_f32_i32_e32 v73, v73
	v_cvt_f32_i32_e32 v72, v72
	v_mad_i64_i32 v[74:75], s[42:43], v84, s86, v[74:75]
	v_cvt_pk_bf16_f32 v84, v78, v79
	v_cvt_f32_i32_e32 v71, v71
	v_cvt_f32_i32_e32 v70, v70
	v_cvt_f32_i32_e32 v67, v67
	v_cvt_f32_i32_e32 v79, v69
	v_cvt_f32_i32_e32 v78, v68
	v_cvt_f32_i32_e32 v66, v66
	v_cvt_pk_bf16_f32 v85, v76, v77
	v_mov_b32_e32 v76, v178
	v_mov_b32_e32 v77, v178
	v_mov_b32_e32 v179, v178
	v_mul_f32_e32 v72, v76, v72
	v_mul_f32_e32 v73, v77, v73
	v_mul_f32_e32 v70, v178, v70
	v_mul_f32_e32 v71, v179, v71
	v_mul_f32_e32 v68, v32, v72
	v_mul_f32_e32 v69, v33, v73
	v_mul_f32_e32 v72, v76, v78
	v_mul_f32_e32 v73, v77, v79
	v_mul_f32_e32 v76, v178, v66
	v_mul_f32_e32 v77, v179, v67
	v_lshl_add_u64 v[74:75], v[170:171], 1, v[74:75]
	v_mul_f32_e32 v70, v30, v70
	v_mul_f32_e32 v71, v31, v71
	v_mul_f32_e32 v66, v24, v72
	v_mul_f32_e32 v67, v25, v73
	s_and_b64 vcc, exec, s[4:5]
	v_mul_f32_e32 v72, v22, v76
	v_mul_f32_e32 v73, v23, v77
	v_cvt_pk_bf16_f32 v86, v82, v83
	v_cvt_pk_bf16_f32 v87, v80, v81
	global_store_dwordx4 v[74:75], v[84:87], off
	s_cbranch_vccnz .LBB0_299
	v_and_b32_e32 v77, 0x7fffffff, v71
	v_and_b32_e32 v76, 0x7fffffff, v70
	v_fma_f32 v76, v76, s18, 1.0
	v_fma_f32 v77, v77, s18, 1.0
	v_mov_b64_e32 v[78:79], s[22:23]
	v_rcp_f32_e32 v76, v76
	v_rcp_f32_e32 v77, v77
	v_mul_f32_e32 v82, v70, v70
	v_mul_f32_e32 v83, v71, v71
	v_cmp_gt_f32_e32 vcc, 0, v70
	v_mul_f32_e32 v82, s30, v82
	v_mul_f32_e32 v83, s30, v83
	v_fma_f32 v80, v76, s20, v78
	v_fma_f32 v81, v77, s20, v78
	v_exp_f32_e32 v82, v82
	v_fma_f32 v80, v76, v80, s24
	v_fma_f32 v81, v77, v81, s24
	v_exp_f32_e32 v83, v83
	v_fma_f32 v80, v76, v80, s26
	v_fma_f32 v81, v77, v81, s26
	s_nop 0
	v_fma_f32 v80, v76, v80, s28
	v_fma_f32 v81, v77, v81, s28
	s_nop 0
	v_mul_f32_e32 v76, v76, v80
	v_mul_f32_e32 v77, v77, v81
	v_mul_f32_e32 v80, v68, v68
	v_mul_f32_e32 v81, v69, v69
	v_mul_f32_e32 v76, v82, v76
	v_mul_f32_e32 v77, v83, v77
	v_mul_f32_e32 v80, s30, v80
	v_mul_f32_e32 v81, s30, v81
	v_mul_f32_e32 v82, v70, v76
	v_mul_f32_e32 v83, v71, v77
	v_fma_f32 v76, -v70, v76, v70
	v_fma_f32 v77, -v71, v77, v71
	v_exp_f32_e32 v80, v80
	v_cndmask_b32_e32 v70, v76, v82, vcc
	v_cmp_gt_f32_e32 vcc, 0, v71
	v_and_b32_e32 v76, 0x7fffffff, v68
	v_exp_f32_e32 v81, v81
	v_cndmask_b32_e32 v71, v77, v83, vcc
	v_and_b32_e32 v77, 0x7fffffff, v69
	v_fma_f32 v76, v76, s18, 1.0
	v_fma_f32 v77, v77, s18, 1.0
	v_cmp_gt_f32_e32 vcc, 0, v68
	v_rcp_f32_e32 v76, v76
	v_rcp_f32_e32 v77, v77
	s_nop 0
	v_fma_f32 v82, v76, s20, v78
	v_fma_f32 v83, v77, s20, v78
	s_nop 0
	v_fma_f32 v82, v76, v82, s24
	v_fma_f32 v83, v77, v83, s24
	s_nop 0
	v_fma_f32 v82, v76, v82, s26
	v_fma_f32 v83, v77, v83, s26
	s_nop 0
	v_fma_f32 v82, v76, v82, s28
	v_fma_f32 v83, v77, v83, s28
	s_nop 0
	v_mul_f32_e32 v76, v76, v82
	v_mul_f32_e32 v77, v77, v83
	v_mul_f32_e32 v82, v72, v72
	v_mul_f32_e32 v83, v73, v73
	v_mul_f32_e32 v76, v80, v76
	v_mul_f32_e32 v77, v81, v77
	v_mul_f32_e32 v82, s30, v82
	v_mul_f32_e32 v83, s30, v83
	v_mul_f32_e32 v80, v68, v76
	v_mul_f32_e32 v81, v69, v77
	v_fma_f32 v76, -v68, v76, v68
	v_fma_f32 v77, -v69, v77, v69
	v_exp_f32_e32 v82, v82
	v_cndmask_b32_e32 v68, v76, v80, vcc
	v_cmp_gt_f32_e32 vcc, 0, v69
	v_and_b32_e32 v76, 0x7fffffff, v72
	v_exp_f32_e32 v83, v83
	v_cndmask_b32_e32 v69, v77, v81, vcc
	v_and_b32_e32 v77, 0x7fffffff, v73
	v_fma_f32 v76, v76, s18, 1.0
	v_fma_f32 v77, v77, s18, 1.0
	v_cmp_gt_f32_e32 vcc, 0, v72
	v_rcp_f32_e32 v76, v76
	v_rcp_f32_e32 v77, v77
	s_nop 0
	v_fma_f32 v80, v76, s20, v78
	v_fma_f32 v81, v77, s20, v78
	s_nop 0
	v_fma_f32 v80, v76, v80, s24
	v_fma_f32 v81, v77, v81, s24
	s_nop 0
	v_fma_f32 v80, v76, v80, s26
	v_fma_f32 v81, v77, v81, s26
	s_nop 0
	v_fma_f32 v80, v76, v80, s28
	v_fma_f32 v81, v77, v81, s28
	s_nop 0
	v_mul_f32_e32 v76, v76, v80
	v_mul_f32_e32 v77, v77, v81
	v_mul_f32_e32 v80, v66, v66
	v_mul_f32_e32 v81, v67, v67
	v_mul_f32_e32 v76, v82, v76
	v_mul_f32_e32 v77, v83, v77
	s_nop 0
	v_mul_f32_e32 v82, v72, v76
	v_mul_f32_e32 v83, v73, v77
	v_fma_f32 v76, -v72, v76, v72
	v_fma_f32 v77, -v73, v77, v73
	s_nop 0
	v_cndmask_b32_e32 v72, v76, v82, vcc
	v_cmp_gt_f32_e32 vcc, 0, v73
	v_and_b32_e32 v76, 0x7fffffff, v66
	s_nop 0
	v_cndmask_b32_e32 v73, v77, v83, vcc
	v_and_b32_e32 v77, 0x7fffffff, v67
	v_fma_f32 v76, v76, s18, 1.0
	v_fma_f32 v77, v77, s18, 1.0
	v_cmp_gt_f32_e32 vcc, 0, v66
	v_rcp_f32_e32 v76, v76
	v_rcp_f32_e32 v77, v77
	s_nop 0
	v_fma_f32 v79, v77, s20, v78
	v_fma_f32 v78, v76, s20, v78
	s_nop 0
	v_fma_f32 v78, v76, v78, s24
	v_fma_f32 v79, v77, v79, s24
	s_nop 0
	v_fma_f32 v78, v76, v78, s26
	v_fma_f32 v79, v77, v79, s26
	s_nop 0
	v_fma_f32 v78, v76, v78, s28
	v_fma_f32 v79, v77, v79, s28
	s_nop 0
	v_mul_f32_e32 v76, v76, v78
	v_mul_f32_e32 v77, v77, v79
	v_mul_f32_e32 v78, s30, v80
	v_mul_f32_e32 v79, s30, v81
	s_nop 0
	v_exp_f32_e32 v78, v78
	v_exp_f32_e32 v79, v79
	s_nop 0
	v_mul_f32_e32 v76, v78, v76
	v_mul_f32_e32 v77, v79, v77
	s_nop 0
	v_mul_f32_e32 v78, v66, v76
	v_mul_f32_e32 v79, v67, v77
	v_fma_f32 v76, -v66, v76, v66
	v_fma_f32 v77, -v67, v77, v67
	s_nop 0
	v_cndmask_b32_e32 v66, v76, v78, vcc
	v_cmp_gt_f32_e32 vcc, 0, v67
	s_nop 1
	v_cndmask_b32_e32 v67, v77, v79, vcc
; __device__ __forceinline__ unsigned cvt_pk_bf16(float lo, float hi) { unsigned r; asm volatile("v_cvt_pk_bf16_f32 %0, %1, %2" : "=v"(r) : "v"(lo), "v"(hi)); return r; }
; __device__ __forceinline__ f32x2 gelu_pk(f32x2 v) {
;     const f32x2 av = __builtin_elementwise_abs(v), d = av * 0.2316418882f + 1.0f;
;     f32x2 t; t.x = __builtin_amdgcn_rcpf(d.x); t.y = __builtin_amdgcn_rcpf(d.y);
;     f32x2 q = t * 0.5307027145f + (-0.7265760135f); q = q * t + 0.7107068705f; q = q * t + (-0.142248368f); q = q * t + 0.127414796f; q = q * t;
;     const f32x2 s = (v * v) * (-0.72134752044f);
;     f32x2 e; e.x = __builtin_amdgcn_exp2f(s.x); e.y = __builtin_amdgcn_exp2f(s.y);
;     const f32x2 m = v * (q * e), r = v - m;
;     f32x2 o; o.x = v.x < 0.f ? m.x : r.x; o.y = v.y < 0.f ? m.y : r.y; return o;
;     __device__ __forceinline__ void operator()(const f32x4 (&acc)[2][2][4][2], const Unit& u, int wr, int wc, int fr, int fq) const {
;     ...
;             for (int m = 0; m < 4; ++m) { const int row = row0 + ai * HALF + m * 16; const float rsc = rsv[ai][m]; bf16_t* rowp = O + (size_t)row * ldc + col0;
; #pragma unroll
;                 for (int bj = 0; bj < 2; ++bj) { const i32x4 a0 = __builtin_bit_cast(i32x4, acc[ai][bj][m][0]), a1 = __builtin_bit_cast(i32x4, acc[ai][bj][m][1]);
;                     f32x4 v0 = (f32x4){(float)a0[0], (float)a0[1], (float)a0[2], (float)a0[3]} * rsc * cv[bj][0], v1 = (f32x4){(float)a1[0], (float)a1[1], (float)a1[2], (float)a1[3]} * rsc * cv[bj][1];
;                     if (act) { f32x2 a = gelu_pk((f32x2){v0[0], v0[1]}), b = gelu_pk((f32x2){v0[2], v0[3]}), c = gelu_pk((f32x2){v1[0], v1[1]}), d = gelu_pk((f32x2){v1[2], v1[3]});
;                         v0 = (f32x4){a.x, a.y, b.x, b.y}; v1 = (f32x4){c.x, c.y, d.x, d.y}; }
;                     u32x4 w; w.x = cvt_pk_bf16(v0[0], v0[1]); w.y = cvt_pk_bf16(v0[2], v0[3]); w.z = cvt_pk_bf16(v1[0], v1[1]); w.w = cvt_pk_bf16(v1[2], v1[3]);
;                     if (nt) __builtin_nontemporal_store(w, (u32x4*)(rowp + bj * HALF)); else *(u32x4*)(rowp + bj * HALF) = w; } }
.LBB0_299:
	v_cvt_f32_i32_e32 v65, v65
	v_cvt_f32_i32_e32 v64, v64
	v_cvt_pk_bf16_f32 v70, v70, v71
	v_cvt_pk_bf16_f32 v71, v68, v69
	v_cvt_pk_bf16_f32 v72, v72, v73
	v_cvt_f32_i32_e32 v63, v63
	v_cvt_f32_i32_e32 v62, v62
	v_cvt_pk_bf16_f32 v73, v66, v67
	v_cvt_f32_i32_e32 v67, v61
	v_cvt_f32_i32_e32 v59, v59
	v_cvt_f32_i32_e32 v58, v58
	v_cvt_f32_i32_e32 v66, v60
	v_mul_f32_e32 v64, v176, v64
	v_mul_f32_e32 v65, v176, v65
	v_mul_f32_e32 v62, v176, v62
	v_mul_f32_e32 v63, v176, v63
	v_mul_f32_e32 v60, v40, v64
	v_mul_f32_e32 v61, v41, v65
	v_mul_f32_e32 v58, v176, v58
	v_mul_f32_e32 v59, v176, v59
	v_mul_f32_e32 v64, v176, v66
	v_mul_f32_e32 v65, v176, v67
	v_mul_f32_e32 v62, v38, v62
	v_mul_f32_e32 v63, v39, v63
	v_mul_f32_e32 v64, v36, v64
	v_mul_f32_e32 v65, v37, v65
	s_and_b64 vcc, exec, s[4:5]
	v_mul_f32_e32 v66, v34, v58
	v_mul_f32_e32 v67, v35, v59
	global_store_dwordx4 v[74:75], v[70:73], off offset:256
	s_cbranch_vccnz .LBB0_301
	v_and_b32_e32 v59, 0x7fffffff, v63
	v_and_b32_e32 v58, 0x7fffffff, v62
	v_fma_f32 v58, v58, s18, 1.0
	v_fma_f32 v59, v59, s18, 1.0
	v_mov_b64_e32 v[68:69], s[22:23]
	v_rcp_f32_e32 v58, v58
	v_rcp_f32_e32 v59, v59
	v_mul_f32_e32 v72, v62, v62
	v_mul_f32_e32 v73, v63, v63
	v_cmp_gt_f32_e32 vcc, 0, v62
	v_mul_f32_e32 v72, s30, v72
	v_mul_f32_e32 v73, s30, v73
	v_fma_f32 v70, v58, s20, v68
	v_fma_f32 v71, v59, s20, v68
	v_exp_f32_e32 v72, v72
	v_fma_f32 v70, v58, v70, s24
	v_fma_f32 v71, v59, v71, s24
	v_exp_f32_e32 v73, v73
	v_fma_f32 v70, v58, v70, s26
	v_fma_f32 v71, v59, v71, s26
	s_nop 0
	v_fma_f32 v70, v58, v70, s28
	v_fma_f32 v71, v59, v71, s28
	s_nop 0
	v_mul_f32_e32 v58, v58, v70
	v_mul_f32_e32 v59, v59, v71
	v_mul_f32_e32 v70, v60, v60
	v_mul_f32_e32 v71, v61, v61
	v_mul_f32_e32 v58, v72, v58
	v_mul_f32_e32 v59, v73, v59
	v_mul_f32_e32 v70, s30, v70
	v_mul_f32_e32 v71, s30, v71
	v_mul_f32_e32 v72, v62, v58
	v_mul_f32_e32 v73, v63, v59
	v_fma_f32 v58, -v62, v58, v62
	v_fma_f32 v59, -v63, v59, v63
	v_exp_f32_e32 v70, v70
	v_cndmask_b32_e32 v62, v58, v72, vcc
	v_cmp_gt_f32_e32 vcc, 0, v63
	v_and_b32_e32 v58, 0x7fffffff, v60
	v_exp_f32_e32 v71, v71
	v_cndmask_b32_e32 v63, v59, v73, vcc
	v_and_b32_e32 v59, 0x7fffffff, v61
	v_fma_f32 v58, v58, s18, 1.0
	v_fma_f32 v59, v59, s18, 1.0
	v_cmp_gt_f32_e32 vcc, 0, v60
	v_rcp_f32_e32 v58, v58
	v_rcp_f32_e32 v59, v59
	s_nop 0
	v_fma_f32 v72, v58, s20, v68
	v_fma_f32 v73, v59, s20, v68
	s_nop 0
	v_fma_f32 v72, v58, v72, s24
	v_fma_f32 v73, v59, v73, s24
	s_nop 0
	v_fma_f32 v72, v58, v72, s26
	v_fma_f32 v73, v59, v73, s26
	s_nop 0
	v_fma_f32 v72, v58, v72, s28
	v_fma_f32 v73, v59, v73, s28
	s_nop 0
	v_mul_f32_e32 v58, v58, v72
	v_mul_f32_e32 v59, v59, v73
	v_mul_f32_e32 v72, v66, v66
	v_mul_f32_e32 v73, v67, v67
	v_mul_f32_e32 v58, v70, v58
	v_mul_f32_e32 v59, v71, v59
	v_mul_f32_e32 v72, s30, v72
	v_mul_f32_e32 v73, s30, v73
	v_mul_f32_e32 v70, v60, v58
	v_mul_f32_e32 v71, v61, v59
	v_fma_f32 v58, -v60, v58, v60
	v_fma_f32 v59, -v61, v59, v61
	v_exp_f32_e32 v72, v72
	v_cndmask_b32_e32 v60, v58, v70, vcc
	v_cmp_gt_f32_e32 vcc, 0, v61
	v_and_b32_e32 v58, 0x7fffffff, v66
	v_exp_f32_e32 v73, v73
	v_cndmask_b32_e32 v61, v59, v71, vcc
	v_and_b32_e32 v59, 0x7fffffff, v67
	v_fma_f32 v58, v58, s18, 1.0
	v_fma_f32 v59, v59, s18, 1.0
	v_cmp_gt_f32_e32 vcc, 0, v66
	v_rcp_f32_e32 v58, v58
	v_rcp_f32_e32 v59, v59
	s_nop 0
	v_fma_f32 v70, v58, s20, v68
	v_fma_f32 v71, v59, s20, v68
	s_nop 0
	v_fma_f32 v70, v58, v70, s24
	v_fma_f32 v71, v59, v71, s24
	s_nop 0
	v_fma_f32 v70, v58, v70, s26
	v_fma_f32 v71, v59, v71, s26
	s_nop 0
	v_fma_f32 v70, v58, v70, s28
	v_fma_f32 v71, v59, v71, s28
	s_nop 0
	v_mul_f32_e32 v58, v58, v70
	v_mul_f32_e32 v59, v59, v71
	v_mul_f32_e32 v70, v64, v64
	v_mul_f32_e32 v71, v65, v65
	v_mul_f32_e32 v58, v72, v58
	v_mul_f32_e32 v59, v73, v59
	s_nop 0
	v_mul_f32_e32 v72, v66, v58
	v_mul_f32_e32 v73, v67, v59
	v_fma_f32 v58, -v66, v58, v66
	v_fma_f32 v59, -v67, v59, v67
	s_nop 0
	v_cndmask_b32_e32 v66, v58, v72, vcc
	v_cmp_gt_f32_e32 vcc, 0, v67
	v_and_b32_e32 v58, 0x7fffffff, v64
	s_nop 0
	v_cndmask_b32_e32 v67, v59, v73, vcc
	v_and_b32_e32 v59, 0x7fffffff, v65
	v_fma_f32 v58, v58, s18, 1.0
	v_fma_f32 v59, v59, s18, 1.0
	v_cmp_gt_f32_e32 vcc, 0, v64
	v_rcp_f32_e32 v58, v58
	v_rcp_f32_e32 v59, v59
	s_nop 0
	v_fma_f32 v69, v59, s20, v68
	v_fma_f32 v68, v58, s20, v68
	s_nop 0
	v_fma_f32 v68, v58, v68, s24
	v_fma_f32 v69, v59, v69, s24
	s_nop 0
	v_fma_f32 v68, v58, v68, s26
	v_fma_f32 v69, v59, v69, s26
	s_nop 0
	v_fma_f32 v68, v58, v68, s28
	v_fma_f32 v69, v59, v69, s28
	s_nop 0
	v_mul_f32_e32 v58, v58, v68
	v_mul_f32_e32 v59, v59, v69
	v_mul_f32_e32 v68, s30, v70
	v_mul_f32_e32 v69, s30, v71
	s_nop 0
	v_exp_f32_e32 v68, v68
	v_exp_f32_e32 v69, v69
	s_nop 0
	v_mul_f32_e32 v58, v68, v58
	v_mul_f32_e32 v59, v69, v59
	s_nop 0
	v_mul_f32_e32 v68, v64, v58
	v_mul_f32_e32 v69, v65, v59
	v_fma_f32 v58, -v64, v58, v64
	v_fma_f32 v59, -v65, v59, v65
	s_nop 0
	v_cndmask_b32_e32 v64, v58, v68, vcc
	v_cmp_gt_f32_e32 vcc, 0, v65
	s_nop 1
	v_cndmask_b32_e32 v65, v59, v69, vcc
; __device__ __forceinline__ unsigned cvt_pk_bf16(float lo, float hi) { unsigned r; asm volatile("v_cvt_pk_bf16_f32 %0, %1, %2" : "=v"(r) : "v"(lo), "v"(hi)); return r; }
; __device__ __forceinline__ f32x2 gelu_pk(f32x2 v) {
;     const f32x2 av = __builtin_elementwise_abs(v), d = av * 0.2316418882f + 1.0f;
;     f32x2 t; t.x = __builtin_amdgcn_rcpf(d.x); t.y = __builtin_amdgcn_rcpf(d.y);
;     f32x2 q = t * 0.5307027145f + (-0.7265760135f); q = q * t + 0.7107068705f; q = q * t + (-0.142248368f); q = q * t + 0.127414796f; q = q * t;
;     const f32x2 s = (v * v) * (-0.72134752044f);
;     f32x2 e; e.x = __builtin_amdgcn_exp2f(s.x); e.y = __builtin_amdgcn_exp2f(s.y);
;     const f32x2 m = v * (q * e), r = v - m;
;     f32x2 o; o.x = v.x < 0.f ? m.x : r.x; o.y = v.y < 0.f ? m.y : r.y; return o;
;     __device__ __forceinline__ void operator()(const f32x4 (&acc)[2][2][4][2], const Unit& u, int wr, int wc, int fr, int fq) const {
;     ...
;             for (int m = 0; m < 4; ++m) { const int row = row0 + ai * HALF + m * 16; const float rsc = rsv[ai][m]; bf16_t* rowp = O + (size_t)row * ldc + col0;
; #pragma unroll
;                 for (int bj = 0; bj < 2; ++bj) { const i32x4 a0 = __builtin_bit_cast(i32x4, acc[ai][bj][m][0]), a1 = __builtin_bit_cast(i32x4, acc[ai][bj][m][1]);
;                     f32x4 v0 = (f32x4){(float)a0[0], (float)a0[1], (float)a0[2], (float)a0[3]} * rsc * cv[bj][0], v1 = (f32x4){(float)a1[0], (float)a1[1], (float)a1[2], (float)a1[3]} * rsc * cv[bj][1];
;                     if (act) { f32x2 a = gelu_pk((f32x2){v0[0], v0[1]}), b = gelu_pk((f32x2){v0[2], v0[3]}), c = gelu_pk((f32x2){v1[0], v1[1]}), d = gelu_pk((f32x2){v1[2], v1[3]});
;                         v0 = (f32x4){a.x, a.y, b.x, b.y}; v1 = (f32x4){c.x, c.y, d.x, d.y}; }
;                     u32x4 w; w.x = cvt_pk_bf16(v0[0], v0[1]); w.y = cvt_pk_bf16(v0[2], v0[3]); w.z = cvt_pk_bf16(v1[0], v1[1]); w.w = cvt_pk_bf16(v1[2], v1[3]);
;                     if (nt) __builtin_nontemporal_store(w, (u32x4*)(rowp + bj * HALF)); else *(u32x4*)(rowp + bj * HALF) = w; } }
.LBB0_301:
	v_add_u32_e32 v68, 0x90, v172
	v_mov_b64_e32 v[58:59], s[66:67]
	v_cvt_f32_i32_e32 v57, v57
	v_cvt_f32_i32_e32 v56, v56
	v_mad_i64_i32 v[58:59], s[42:43], v68, s86, v[58:59]
	v_cvt_pk_bf16_f32 v68, v62, v63
	v_cvt_f32_i32_e32 v55, v55
	v_cvt_f32_i32_e32 v54, v54
	v_cvt_f32_i32_e32 v51, v51
	v_cvt_f32_i32_e32 v63, v53
	v_cvt_f32_i32_e32 v62, v52
	v_cvt_f32_i32_e32 v50, v50
	v_cvt_pk_bf16_f32 v69, v60, v61
	v_mov_b32_e32 v60, v176
	v_mov_b32_e32 v61, v176
	v_mov_b32_e32 v177, v176
	v_mul_f32_e32 v56, v60, v56
	v_mul_f32_e32 v57, v61, v57
	v_mul_f32_e32 v54, v176, v54
	v_mul_f32_e32 v55, v177, v55
	v_mul_f32_e32 v52, v32, v56
	v_mul_f32_e32 v53, v33, v57
	v_mul_f32_e32 v56, v60, v62
	v_mul_f32_e32 v57, v61, v63
	v_mul_f32_e32 v60, v176, v50
	v_mul_f32_e32 v61, v177, v51
	v_lshl_add_u64 v[58:59], v[170:171], 1, v[58:59]
	v_mul_f32_e32 v54, v30, v54
	v_mul_f32_e32 v55, v31, v55
	v_mul_f32_e32 v50, v24, v56
	v_mul_f32_e32 v51, v25, v57
	s_and_b64 vcc, exec, s[4:5]
	v_mul_f32_e32 v56, v22, v60
	v_mul_f32_e32 v57, v23, v61
	v_cvt_pk_bf16_f32 v70, v66, v67
	v_cvt_pk_bf16_f32 v71, v64, v65
	global_store_dwordx4 v[58:59], v[68:71], off
	s_cbranch_vccnz .LBB0_303
	v_and_b32_e32 v61, 0x7fffffff, v55
	v_and_b32_e32 v60, 0x7fffffff, v54
	v_fma_f32 v60, v60, s18, 1.0
	v_fma_f32 v61, v61, s18, 1.0
	v_mov_b64_e32 v[62:63], s[22:23]
	v_rcp_f32_e32 v60, v60
	v_rcp_f32_e32 v61, v61
	v_mul_f32_e32 v66, v54, v54
	v_mul_f32_e32 v67, v55, v55
	v_cmp_gt_f32_e32 vcc, 0, v54
	v_mul_f32_e32 v66, s30, v66
	v_mul_f32_e32 v67, s30, v67
	v_fma_f32 v64, v60, s20, v62
	v_fma_f32 v65, v61, s20, v62
	v_exp_f32_e32 v66, v66
	v_fma_f32 v64, v60, v64, s24
	v_fma_f32 v65, v61, v65, s24
	v_exp_f32_e32 v67, v67
	v_fma_f32 v64, v60, v64, s26
	v_fma_f32 v65, v61, v65, s26
	s_nop 0
	v_fma_f32 v64, v60, v64, s28
	v_fma_f32 v65, v61, v65, s28
	s_nop 0
	v_mul_f32_e32 v60, v60, v64
	v_mul_f32_e32 v61, v61, v65
	v_mul_f32_e32 v64, v52, v52
	v_mul_f32_e32 v65, v53, v53
	v_mul_f32_e32 v60, v66, v60
	v_mul_f32_e32 v61, v67, v61
	v_mul_f32_e32 v64, s30, v64
	v_mul_f32_e32 v65, s30, v65
	v_mul_f32_e32 v66, v54, v60
	v_mul_f32_e32 v67, v55, v61
	v_fma_f32 v60, -v54, v60, v54
	v_fma_f32 v61, -v55, v61, v55
	v_exp_f32_e32 v64, v64
	v_cndmask_b32_e32 v54, v60, v66, vcc
	v_cmp_gt_f32_e32 vcc, 0, v55
	v_and_b32_e32 v60, 0x7fffffff, v52
	v_exp_f32_e32 v65, v65
	v_cndmask_b32_e32 v55, v61, v67, vcc
	v_and_b32_e32 v61, 0x7fffffff, v53
	v_fma_f32 v60, v60, s18, 1.0
	v_fma_f32 v61, v61, s18, 1.0
	v_cmp_gt_f32_e32 vcc, 0, v52
	v_rcp_f32_e32 v60, v60
	v_rcp_f32_e32 v61, v61
	s_nop 0
	v_fma_f32 v66, v60, s20, v62
	v_fma_f32 v67, v61, s20, v62
	s_nop 0
	v_fma_f32 v66, v60, v66, s24
	v_fma_f32 v67, v61, v67, s24
	s_nop 0
	v_fma_f32 v66, v60, v66, s26
	v_fma_f32 v67, v61, v67, s26
	s_nop 0
	v_fma_f32 v66, v60, v66, s28
	v_fma_f32 v67, v61, v67, s28
	s_nop 0
	v_mul_f32_e32 v60, v60, v66
	v_mul_f32_e32 v61, v61, v67
	v_mul_f32_e32 v66, v56, v56
	v_mul_f32_e32 v67, v57, v57
	v_mul_f32_e32 v60, v64, v60
	v_mul_f32_e32 v61, v65, v61
	v_mul_f32_e32 v66, s30, v66
	v_mul_f32_e32 v67, s30, v67
	v_mul_f32_e32 v64, v52, v60
	v_mul_f32_e32 v65, v53, v61
	v_fma_f32 v60, -v52, v60, v52
	v_fma_f32 v61, -v53, v61, v53
	v_exp_f32_e32 v66, v66
	v_cndmask_b32_e32 v52, v60, v64, vcc
	v_cmp_gt_f32_e32 vcc, 0, v53
	v_and_b32_e32 v60, 0x7fffffff, v56
	v_exp_f32_e32 v67, v67
	v_cndmask_b32_e32 v53, v61, v65, vcc
	v_and_b32_e32 v61, 0x7fffffff, v57
	v_fma_f32 v60, v60, s18, 1.0
	v_fma_f32 v61, v61, s18, 1.0
	v_cmp_gt_f32_e32 vcc, 0, v56
	v_rcp_f32_e32 v60, v60
	v_rcp_f32_e32 v61, v61
	s_nop 0
	v_fma_f32 v64, v60, s20, v62
	v_fma_f32 v65, v61, s20, v62
	s_nop 0
	v_fma_f32 v64, v60, v64, s24
	v_fma_f32 v65, v61, v65, s24
	s_nop 0
	v_fma_f32 v64, v60, v64, s26
	v_fma_f32 v65, v61, v65, s26
	s_nop 0
	v_fma_f32 v64, v60, v64, s28
	v_fma_f32 v65, v61, v65, s28
	s_nop 0
	v_mul_f32_e32 v60, v60, v64
	v_mul_f32_e32 v61, v61, v65
	v_mul_f32_e32 v64, v50, v50
	v_mul_f32_e32 v65, v51, v51
	v_mul_f32_e32 v60, v66, v60
	v_mul_f32_e32 v61, v67, v61
	s_nop 0
	v_mul_f32_e32 v66, v56, v60
	v_mul_f32_e32 v67, v57, v61
	v_fma_f32 v60, -v56, v60, v56
	v_fma_f32 v61, -v57, v61, v57
	s_nop 0
	v_cndmask_b32_e32 v56, v60, v66, vcc
	v_cmp_gt_f32_e32 vcc, 0, v57
	v_and_b32_e32 v60, 0x7fffffff, v50
	s_nop 0
	v_cndmask_b32_e32 v57, v61, v67, vcc
	v_and_b32_e32 v61, 0x7fffffff, v51
	v_fma_f32 v60, v60, s18, 1.0
	v_fma_f32 v61, v61, s18, 1.0
	v_cmp_gt_f32_e32 vcc, 0, v50
	v_rcp_f32_e32 v60, v60
	v_rcp_f32_e32 v61, v61
	s_nop 0
	v_fma_f32 v63, v61, s20, v62
	v_fma_f32 v62, v60, s20, v62
	s_nop 0
	v_fma_f32 v62, v60, v62, s24
	v_fma_f32 v63, v61, v63, s24
	s_nop 0
	v_fma_f32 v62, v60, v62, s26
	v_fma_f32 v63, v61, v63, s26
	s_nop 0
	v_fma_f32 v62, v60, v62, s28
	v_fma_f32 v63, v61, v63, s28
	s_nop 0
	v_mul_f32_e32 v60, v60, v62
	v_mul_f32_e32 v61, v61, v63
	v_mul_f32_e32 v62, s30, v64
	v_mul_f32_e32 v63, s30, v65
	s_nop 0
	v_exp_f32_e32 v62, v62
	v_exp_f32_e32 v63, v63
	s_nop 0
	v_mul_f32_e32 v60, v62, v60
	v_mul_f32_e32 v61, v63, v61
	s_nop 0
	v_mul_f32_e32 v62, v50, v60
	v_mul_f32_e32 v63, v51, v61
	v_fma_f32 v60, -v50, v60, v50
	v_fma_f32 v61, -v51, v61, v51
	s_nop 0
	v_cndmask_b32_e32 v50, v60, v62, vcc
	v_cmp_gt_f32_e32 vcc, 0, v51
	s_nop 1
	v_cndmask_b32_e32 v51, v61, v63, vcc
; __device__ __forceinline__ unsigned cvt_pk_bf16(float lo, float hi) { unsigned r; asm volatile("v_cvt_pk_bf16_f32 %0, %1, %2" : "=v"(r) : "v"(lo), "v"(hi)); return r; }
; __device__ __forceinline__ f32x2 gelu_pk(f32x2 v) {
;     const f32x2 av = __builtin_elementwise_abs(v), d = av * 0.2316418882f + 1.0f;
;     f32x2 t; t.x = __builtin_amdgcn_rcpf(d.x); t.y = __builtin_amdgcn_rcpf(d.y);
;     f32x2 q = t * 0.5307027145f + (-0.7265760135f); q = q * t + 0.7107068705f; q = q * t + (-0.142248368f); q = q * t + 0.127414796f; q = q * t;
;     const f32x2 s = (v * v) * (-0.72134752044f);
;     f32x2 e; e.x = __builtin_amdgcn_exp2f(s.x); e.y = __builtin_amdgcn_exp2f(s.y);
;     const f32x2 m = v * (q * e), r = v - m;
;     f32x2 o; o.x = v.x < 0.f ? m.x : r.x; o.y = v.y < 0.f ? m.y : r.y; return o;
;     __device__ __forceinline__ void operator()(const f32x4 (&acc)[2][2][4][2], const Unit& u, int wr, int wc, int fr, int fq) const {
;     ...
;             for (int m = 0; m < 4; ++m) { const int row = row0 + ai * HALF + m * 16; const float rsc = rsv[ai][m]; bf16_t* rowp = O + (size_t)row * ldc + col0;
; #pragma unroll
;                 for (int bj = 0; bj < 2; ++bj) { const i32x4 a0 = __builtin_bit_cast(i32x4, acc[ai][bj][m][0]), a1 = __builtin_bit_cast(i32x4, acc[ai][bj][m][1]);
;                     f32x4 v0 = (f32x4){(float)a0[0], (float)a0[1], (float)a0[2], (float)a0[3]} * rsc * cv[bj][0], v1 = (f32x4){(float)a1[0], (float)a1[1], (float)a1[2], (float)a1[3]} * rsc * cv[bj][1];
;                     if (act) { f32x2 a = gelu_pk((f32x2){v0[0], v0[1]}), b = gelu_pk((f32x2){v0[2], v0[3]}), c = gelu_pk((f32x2){v1[0], v1[1]}), d = gelu_pk((f32x2){v1[2], v1[3]});
;                         v0 = (f32x4){a.x, a.y, b.x, b.y}; v1 = (f32x4){c.x, c.y, d.x, d.y}; }
;                     u32x4 w; w.x = cvt_pk_bf16(v0[0], v0[1]); w.y = cvt_pk_bf16(v0[2], v0[3]); w.z = cvt_pk_bf16(v1[0], v1[1]); w.w = cvt_pk_bf16(v1[2], v1[3]);
;                     if (nt) __builtin_nontemporal_store(w, (u32x4*)(rowp + bj * HALF)); else *(u32x4*)(rowp + bj * HALF) = w; } }
.LBB0_303:
	v_cvt_f32_i32_e32 v49, v49
	v_cvt_f32_i32_e32 v48, v48
	v_cvt_pk_bf16_f32 v54, v54, v55
	v_cvt_pk_bf16_f32 v55, v52, v53
	v_cvt_pk_bf16_f32 v56, v56, v57
	v_cvt_f32_i32_e32 v47, v47
	v_cvt_f32_i32_e32 v46, v46
	v_cvt_pk_bf16_f32 v57, v50, v51
	v_cvt_f32_i32_e32 v51, v45
	v_cvt_f32_i32_e32 v43, v43
	v_cvt_f32_i32_e32 v42, v42
	v_cvt_f32_i32_e32 v50, v44
	v_mul_f32_e32 v48, v174, v48
	v_mul_f32_e32 v49, v174, v49
	v_mul_f32_e32 v46, v174, v46
	v_mul_f32_e32 v47, v174, v47
	v_mul_f32_e32 v44, v40, v48
	v_mul_f32_e32 v45, v41, v49
	v_mul_f32_e32 v42, v174, v42
	v_mul_f32_e32 v43, v174, v43
	v_mul_f32_e32 v48, v174, v50
	v_mul_f32_e32 v49, v174, v51
	v_mul_f32_e32 v46, v38, v46
	v_mul_f32_e32 v47, v39, v47
	v_mul_f32_e32 v48, v36, v48
	v_mul_f32_e32 v49, v37, v49
	s_and_b64 vcc, exec, s[4:5]
	v_mul_f32_e32 v50, v34, v42
	v_mul_f32_e32 v51, v35, v43
	global_store_dwordx4 v[58:59], v[54:57], off offset:256
	s_cbranch_vccnz .LBB0_305
	v_and_b32_e32 v43, 0x7fffffff, v47
	v_and_b32_e32 v42, 0x7fffffff, v46
	v_fma_f32 v42, v42, s18, 1.0
	v_fma_f32 v43, v43, s18, 1.0
	v_mov_b64_e32 v[52:53], s[22:23]
	v_rcp_f32_e32 v42, v42
	v_rcp_f32_e32 v43, v43
	v_mul_f32_e32 v56, v46, v46
	v_mul_f32_e32 v57, v47, v47
	v_cmp_gt_f32_e32 vcc, 0, v46
	v_mul_f32_e32 v56, s30, v56
	v_mul_f32_e32 v57, s30, v57
	v_fma_f32 v54, v42, s20, v52
	v_fma_f32 v55, v43, s20, v52
	v_exp_f32_e32 v56, v56
	v_fma_f32 v54, v42, v54, s24
	v_fma_f32 v55, v43, v55, s24
	v_exp_f32_e32 v57, v57
	v_fma_f32 v54, v42, v54, s26
	v_fma_f32 v55, v43, v55, s26
	s_nop 0
	v_fma_f32 v54, v42, v54, s28
	v_fma_f32 v55, v43, v55, s28
	s_nop 0
	v_mul_f32_e32 v42, v42, v54
	v_mul_f32_e32 v43, v43, v55
	v_mul_f32_e32 v54, v44, v44
	v_mul_f32_e32 v55, v45, v45
	v_mul_f32_e32 v42, v56, v42
	v_mul_f32_e32 v43, v57, v43
	v_mul_f32_e32 v54, s30, v54
	v_mul_f32_e32 v55, s30, v55
	v_mul_f32_e32 v56, v46, v42
	v_mul_f32_e32 v57, v47, v43
	v_fma_f32 v42, -v46, v42, v46
	v_fma_f32 v43, -v47, v43, v47
	v_exp_f32_e32 v54, v54
	v_cndmask_b32_e32 v46, v42, v56, vcc
	v_cmp_gt_f32_e32 vcc, 0, v47
	v_and_b32_e32 v42, 0x7fffffff, v44
	v_exp_f32_e32 v55, v55
	v_cndmask_b32_e32 v47, v43, v57, vcc
	v_and_b32_e32 v43, 0x7fffffff, v45
	v_fma_f32 v42, v42, s18, 1.0
	v_fma_f32 v43, v43, s18, 1.0
	v_cmp_gt_f32_e32 vcc, 0, v44
	v_rcp_f32_e32 v42, v42
	v_rcp_f32_e32 v43, v43
	s_nop 0
	v_fma_f32 v56, v42, s20, v52
	v_fma_f32 v57, v43, s20, v52
	s_nop 0
	v_fma_f32 v56, v42, v56, s24
	v_fma_f32 v57, v43, v57, s24
	s_nop 0
	v_fma_f32 v56, v42, v56, s26
	v_fma_f32 v57, v43, v57, s26
	s_nop 0
	v_fma_f32 v56, v42, v56, s28
	v_fma_f32 v57, v43, v57, s28
	s_nop 0
	v_mul_f32_e32 v42, v42, v56
	v_mul_f32_e32 v43, v43, v57
	v_mul_f32_e32 v56, v50, v50
	v_mul_f32_e32 v57, v51, v51
	v_mul_f32_e32 v42, v54, v42
	v_mul_f32_e32 v43, v55, v43
	v_mul_f32_e32 v56, s30, v56
	v_mul_f32_e32 v57, s30, v57
	v_mul_f32_e32 v54, v44, v42
	v_mul_f32_e32 v55, v45, v43
	v_fma_f32 v42, -v44, v42, v44
	v_fma_f32 v43, -v45, v43, v45
	v_exp_f32_e32 v56, v56
	v_cndmask_b32_e32 v44, v42, v54, vcc
	v_cmp_gt_f32_e32 vcc, 0, v45
	v_and_b32_e32 v42, 0x7fffffff, v50
	v_exp_f32_e32 v57, v57
	v_cndmask_b32_e32 v45, v43, v55, vcc
	v_and_b32_e32 v43, 0x7fffffff, v51
	v_fma_f32 v42, v42, s18, 1.0
	v_fma_f32 v43, v43, s18, 1.0
	v_cmp_gt_f32_e32 vcc, 0, v50
	v_rcp_f32_e32 v42, v42
	v_rcp_f32_e32 v43, v43
	s_nop 0
	v_fma_f32 v54, v42, s20, v52
	v_fma_f32 v55, v43, s20, v52
	s_nop 0
	v_fma_f32 v54, v42, v54, s24
	v_fma_f32 v55, v43, v55, s24
	s_nop 0
	v_fma_f32 v54, v42, v54, s26
	v_fma_f32 v55, v43, v55, s26
	s_nop 0
	v_fma_f32 v54, v42, v54, s28
	v_fma_f32 v55, v43, v55, s28
	s_nop 0
	v_mul_f32_e32 v42, v42, v54
	v_mul_f32_e32 v43, v43, v55
	v_mul_f32_e32 v54, v48, v48
	v_mul_f32_e32 v55, v49, v49
	v_mul_f32_e32 v42, v56, v42
	v_mul_f32_e32 v43, v57, v43
	s_nop 0
	v_mul_f32_e32 v56, v50, v42
	v_mul_f32_e32 v57, v51, v43
	v_fma_f32 v42, -v50, v42, v50
	v_fma_f32 v43, -v51, v43, v51
	s_nop 0
	v_cndmask_b32_e32 v50, v42, v56, vcc
	v_cmp_gt_f32_e32 vcc, 0, v51
	v_and_b32_e32 v42, 0x7fffffff, v48
	s_nop 0
	v_cndmask_b32_e32 v51, v43, v57, vcc
	v_and_b32_e32 v43, 0x7fffffff, v49
	v_fma_f32 v42, v42, s18, 1.0
	v_fma_f32 v43, v43, s18, 1.0
	v_cmp_gt_f32_e32 vcc, 0, v48
	v_rcp_f32_e32 v42, v42
	v_rcp_f32_e32 v43, v43
	s_nop 0
	v_fma_f32 v53, v43, s20, v52
	v_fma_f32 v52, v42, s20, v52
	s_nop 0
	v_fma_f32 v52, v42, v52, s24
	v_fma_f32 v53, v43, v53, s24
	s_nop 0
	v_fma_f32 v52, v42, v52, s26
	v_fma_f32 v53, v43, v53, s26
	s_nop 0
	v_fma_f32 v52, v42, v52, s28
	v_fma_f32 v53, v43, v53, s28
	s_nop 0
	v_mul_f32_e32 v42, v42, v52
	v_mul_f32_e32 v43, v43, v53
	v_mul_f32_e32 v52, s30, v54
	v_mul_f32_e32 v53, s30, v55
	s_nop 0
	v_exp_f32_e32 v52, v52
	v_exp_f32_e32 v53, v53
	s_nop 0
	v_mul_f32_e32 v42, v52, v42
	v_mul_f32_e32 v43, v53, v43
	s_nop 0
	v_mul_f32_e32 v52, v48, v42
	v_mul_f32_e32 v53, v49, v43
	v_fma_f32 v42, -v48, v42, v48
	v_fma_f32 v43, -v49, v43, v49
	s_nop 0
	v_cndmask_b32_e32 v48, v42, v52, vcc
	v_cmp_gt_f32_e32 vcc, 0, v49
	s_nop 1
	v_cndmask_b32_e32 v49, v43, v53, vcc
; __device__ __forceinline__ unsigned cvt_pk_bf16(float lo, float hi) { unsigned r; asm volatile("v_cvt_pk_bf16_f32 %0, %1, %2" : "=v"(r) : "v"(lo), "v"(hi)); return r; }
; __device__ __forceinline__ f32x2 gelu_pk(f32x2 v) {
;     const f32x2 av = __builtin_elementwise_abs(v), d = av * 0.2316418882f + 1.0f;
;     f32x2 t; t.x = __builtin_amdgcn_rcpf(d.x); t.y = __builtin_amdgcn_rcpf(d.y);
;     f32x2 q = t * 0.5307027145f + (-0.7265760135f); q = q * t + 0.7107068705f; q = q * t + (-0.142248368f); q = q * t + 0.127414796f; q = q * t;
;     const f32x2 s = (v * v) * (-0.72134752044f);
;     f32x2 e; e.x = __builtin_amdgcn_exp2f(s.x); e.y = __builtin_amdgcn_exp2f(s.y);
;     const f32x2 m = v * (q * e), r = v - m;
;     f32x2 o; o.x = v.x < 0.f ? m.x : r.x; o.y = v.y < 0.f ? m.y : r.y; return o;
;     __device__ __forceinline__ void operator()(const f32x4 (&acc)[2][2][4][2], const Unit& u, int wr, int wc, int fr, int fq) const {
;     ...
;             for (int m = 0; m < 4; ++m) { const int row = row0 + ai * HALF + m * 16; const float rsc = rsv[ai][m]; bf16_t* rowp = O + (size_t)row * ldc + col0;
; #pragma unroll
;                 for (int bj = 0; bj < 2; ++bj) { const i32x4 a0 = __builtin_bit_cast(i32x4, acc[ai][bj][m][0]), a1 = __builtin_bit_cast(i32x4, acc[ai][bj][m][1]);
;                     f32x4 v0 = (f32x4){(float)a0[0], (float)a0[1], (float)a0[2], (float)a0[3]} * rsc * cv[bj][0], v1 = (f32x4){(float)a1[0], (float)a1[1], (float)a1[2], (float)a1[3]} * rsc * cv[bj][1];
;                     if (act) { f32x2 a = gelu_pk((f32x2){v0[0], v0[1]}), b = gelu_pk((f32x2){v0[2], v0[3]}), c = gelu_pk((f32x2){v1[0], v1[1]}), d = gelu_pk((f32x2){v1[2], v1[3]});
;                         v0 = (f32x4){a.x, a.y, b.x, b.y}; v1 = (f32x4){c.x, c.y, d.x, d.y}; }
;                     u32x4 w; w.x = cvt_pk_bf16(v0[0], v0[1]); w.y = cvt_pk_bf16(v0[2], v0[3]); w.z = cvt_pk_bf16(v1[0], v1[1]); w.w = cvt_pk_bf16(v1[2], v1[3]);
;                     if (nt) __builtin_nontemporal_store(w, (u32x4*)(rowp + bj * HALF)); else *(u32x4*)(rowp + bj * HALF) = w; } }
.LBB0_305:
	v_add_u32_e32 v52, 0xa0, v172
	v_mov_b64_e32 v[42:43], s[66:67]
	v_cvt_f32_i32_e32 v29, v29
	v_cvt_f32_i32_e32 v28, v28
	v_mad_i64_i32 v[42:43], s[42:43], v52, s86, v[42:43]
	v_cvt_pk_bf16_f32 v52, v46, v47
	v_cvt_f32_i32_e32 v27, v27
	v_cvt_f32_i32_e32 v26, v26
	v_cvt_f32_i32_e32 v19, v19
	v_cvt_f32_i32_e32 v47, v21
	v_cvt_f32_i32_e32 v46, v20
	v_cvt_f32_i32_e32 v18, v18
	v_cvt_pk_bf16_f32 v53, v44, v45
	v_mov_b32_e32 v44, v174
	v_mov_b32_e32 v45, v174
	v_mov_b32_e32 v175, v174
	v_mul_f32_e32 v28, v44, v28
	v_mul_f32_e32 v29, v45, v29
	v_mul_f32_e32 v26, v174, v26
	v_mul_f32_e32 v27, v175, v27
	v_mul_f32_e32 v20, v32, v28
	v_mul_f32_e32 v21, v33, v29
	v_mul_f32_e32 v28, v44, v46
	v_mul_f32_e32 v29, v45, v47
	v_mul_f32_e32 v44, v174, v18
	v_mul_f32_e32 v45, v175, v19
	v_lshl_add_u64 v[42:43], v[170:171], 1, v[42:43]
	v_mul_f32_e32 v26, v30, v26
	v_mul_f32_e32 v27, v31, v27
	v_mul_f32_e32 v18, v24, v28
	v_mul_f32_e32 v19, v25, v29
	s_and_b64 vcc, exec, s[4:5]
	v_mul_f32_e32 v28, v22, v44
	v_mul_f32_e32 v29, v23, v45
	v_cvt_pk_bf16_f32 v54, v50, v51
	v_cvt_pk_bf16_f32 v55, v48, v49
	global_store_dwordx4 v[42:43], v[52:55], off
	s_cbranch_vccnz .LBB0_307
	v_and_b32_e32 v45, 0x7fffffff, v27
	v_and_b32_e32 v44, 0x7fffffff, v26
	v_fma_f32 v44, v44, s18, 1.0
	v_fma_f32 v45, v45, s18, 1.0
	v_mov_b64_e32 v[46:47], s[22:23]
	v_rcp_f32_e32 v44, v44
	v_rcp_f32_e32 v45, v45
	v_mul_f32_e32 v50, v26, v26
	v_mul_f32_e32 v51, v27, v27
	v_cmp_gt_f32_e32 vcc, 0, v26
	v_mul_f32_e32 v50, s30, v50
	v_mul_f32_e32 v51, s30, v51
	v_fma_f32 v48, v44, s20, v46
	v_fma_f32 v49, v45, s20, v46
	v_exp_f32_e32 v50, v50
	v_fma_f32 v48, v44, v48, s24
	v_fma_f32 v49, v45, v49, s24
	v_exp_f32_e32 v51, v51
	v_fma_f32 v48, v44, v48, s26
	v_fma_f32 v49, v45, v49, s26
	s_nop 0
	v_fma_f32 v48, v44, v48, s28
	v_fma_f32 v49, v45, v49, s28
	s_nop 0
	v_mul_f32_e32 v44, v44, v48
	v_mul_f32_e32 v45, v45, v49
	v_mul_f32_e32 v48, v20, v20
	v_mul_f32_e32 v49, v21, v21
	v_mul_f32_e32 v44, v50, v44
	v_mul_f32_e32 v45, v51, v45
	v_mul_f32_e32 v48, s30, v48
	v_mul_f32_e32 v49, s30, v49
	v_mul_f32_e32 v50, v26, v44
	v_mul_f32_e32 v51, v27, v45
	v_fma_f32 v44, -v26, v44, v26
	v_fma_f32 v45, -v27, v45, v27
	v_exp_f32_e32 v48, v48
	v_cndmask_b32_e32 v26, v44, v50, vcc
	v_cmp_gt_f32_e32 vcc, 0, v27
	v_and_b32_e32 v44, 0x7fffffff, v20
	v_exp_f32_e32 v49, v49
	v_cndmask_b32_e32 v27, v45, v51, vcc
	v_and_b32_e32 v45, 0x7fffffff, v21
	v_fma_f32 v44, v44, s18, 1.0
	v_fma_f32 v45, v45, s18, 1.0
	v_cmp_gt_f32_e32 vcc, 0, v20
	v_rcp_f32_e32 v44, v44
	v_rcp_f32_e32 v45, v45
	s_nop 0
	v_fma_f32 v50, v44, s20, v46
	v_fma_f32 v51, v45, s20, v46
	s_nop 0
	v_fma_f32 v50, v44, v50, s24
	v_fma_f32 v51, v45, v51, s24
	s_nop 0
	v_fma_f32 v50, v44, v50, s26
	v_fma_f32 v51, v45, v51, s26
	s_nop 0
	v_fma_f32 v50, v44, v50, s28
	v_fma_f32 v51, v45, v51, s28
	s_nop 0
	v_mul_f32_e32 v44, v44, v50
	v_mul_f32_e32 v45, v45, v51
	v_mul_f32_e32 v50, v28, v28
	v_mul_f32_e32 v51, v29, v29
	v_mul_f32_e32 v44, v48, v44
	v_mul_f32_e32 v45, v49, v45
	v_mul_f32_e32 v50, s30, v50
	v_mul_f32_e32 v51, s30, v51
	v_mul_f32_e32 v48, v20, v44
	v_mul_f32_e32 v49, v21, v45
	v_fma_f32 v44, -v20, v44, v20
	v_fma_f32 v45, -v21, v45, v21
	v_exp_f32_e32 v50, v50
	v_cndmask_b32_e32 v20, v44, v48, vcc
	v_cmp_gt_f32_e32 vcc, 0, v21
	v_and_b32_e32 v44, 0x7fffffff, v28
	v_exp_f32_e32 v51, v51
	v_cndmask_b32_e32 v21, v45, v49, vcc
	v_and_b32_e32 v45, 0x7fffffff, v29
	v_fma_f32 v44, v44, s18, 1.0
	v_fma_f32 v45, v45, s18, 1.0
	v_cmp_gt_f32_e32 vcc, 0, v28
	v_rcp_f32_e32 v44, v44
	v_rcp_f32_e32 v45, v45
	s_nop 0
	v_fma_f32 v48, v44, s20, v46
	v_fma_f32 v49, v45, s20, v46
	s_nop 0
	v_fma_f32 v48, v44, v48, s24
	v_fma_f32 v49, v45, v49, s24
	s_nop 0
	v_fma_f32 v48, v44, v48, s26
	v_fma_f32 v49, v45, v49, s26
	s_nop 0
	v_fma_f32 v48, v44, v48, s28
	v_fma_f32 v49, v45, v49, s28
	s_nop 0
	v_mul_f32_e32 v44, v44, v48
	v_mul_f32_e32 v45, v45, v49
	v_mul_f32_e32 v48, v18, v18
	v_mul_f32_e32 v49, v19, v19
	v_mul_f32_e32 v44, v50, v44
	v_mul_f32_e32 v45, v51, v45
	s_nop 0
	v_mul_f32_e32 v50, v28, v44
	v_mul_f32_e32 v51, v29, v45
	v_fma_f32 v44, -v28, v44, v28
	v_fma_f32 v45, -v29, v45, v29
	s_nop 0
	v_cndmask_b32_e32 v28, v44, v50, vcc
	v_cmp_gt_f32_e32 vcc, 0, v29
	v_and_b32_e32 v44, 0x7fffffff, v18
	s_nop 0
	v_cndmask_b32_e32 v29, v45, v51, vcc
	v_and_b32_e32 v45, 0x7fffffff, v19
	v_fma_f32 v44, v44, s18, 1.0
	v_fma_f32 v45, v45, s18, 1.0
	v_cmp_gt_f32_e32 vcc, 0, v18
	v_rcp_f32_e32 v44, v44
	v_rcp_f32_e32 v45, v45
	s_nop 0
	v_fma_f32 v47, v45, s20, v46
	v_fma_f32 v46, v44, s20, v46
	s_nop 0
	v_fma_f32 v46, v44, v46, s24
	v_fma_f32 v47, v45, v47, s24
	s_nop 0
	v_fma_f32 v46, v44, v46, s26
	v_fma_f32 v47, v45, v47, s26
	s_nop 0
	v_fma_f32 v46, v44, v46, s28
	v_fma_f32 v47, v45, v47, s28
	s_nop 0
	v_mul_f32_e32 v44, v44, v46
	v_mul_f32_e32 v45, v45, v47
	v_mul_f32_e32 v46, s30, v48
	v_mul_f32_e32 v47, s30, v49
	s_nop 0
	v_exp_f32_e32 v46, v46
	v_exp_f32_e32 v47, v47
	s_nop 0
	v_mul_f32_e32 v44, v46, v44
	v_mul_f32_e32 v45, v47, v45
	s_nop 0
	v_mul_f32_e32 v46, v18, v44
	v_mul_f32_e32 v47, v19, v45
	v_fma_f32 v44, -v18, v44, v18
	v_fma_f32 v45, -v19, v45, v19
	s_nop 0
	v_cndmask_b32_e32 v18, v44, v46, vcc
	v_cmp_gt_f32_e32 vcc, 0, v19
	s_nop 1
	v_cndmask_b32_e32 v19, v45, v47, vcc
; __device__ __forceinline__ unsigned cvt_pk_bf16(float lo, float hi) { unsigned r; asm volatile("v_cvt_pk_bf16_f32 %0, %1, %2" : "=v"(r) : "v"(lo), "v"(hi)); return r; }
; __device__ __forceinline__ f32x2 gelu_pk(f32x2 v) {
;     const f32x2 av = __builtin_elementwise_abs(v), d = av * 0.2316418882f + 1.0f;
;     f32x2 t; t.x = __builtin_amdgcn_rcpf(d.x); t.y = __builtin_amdgcn_rcpf(d.y);
;     f32x2 q = t * 0.5307027145f + (-0.7265760135f); q = q * t + 0.7107068705f; q = q * t + (-0.142248368f); q = q * t + 0.127414796f; q = q * t;
;     const f32x2 s = (v * v) * (-0.72134752044f);
;     f32x2 e; e.x = __builtin_amdgcn_exp2f(s.x); e.y = __builtin_amdgcn_exp2f(s.y);
;     const f32x2 m = v * (q * e), r = v - m;
;     f32x2 o; o.x = v.x < 0.f ? m.x : r.x; o.y = v.y < 0.f ? m.y : r.y; return o;
;     __device__ __forceinline__ void operator()(const f32x4 (&acc)[2][2][4][2], const Unit& u, int wr, int wc, int fr, int fq) const {
;     ...
;             for (int m = 0; m < 4; ++m) { const int row = row0 + ai * HALF + m * 16; const float rsc = rsv[ai][m]; bf16_t* rowp = O + (size_t)row * ldc + col0;
; #pragma unroll
;                 for (int bj = 0; bj < 2; ++bj) { const i32x4 a0 = __builtin_bit_cast(i32x4, acc[ai][bj][m][0]), a1 = __builtin_bit_cast(i32x4, acc[ai][bj][m][1]);
;                     f32x4 v0 = (f32x4){(float)a0[0], (float)a0[1], (float)a0[2], (float)a0[3]} * rsc * cv[bj][0], v1 = (f32x4){(float)a1[0], (float)a1[1], (float)a1[2], (float)a1[3]} * rsc * cv[bj][1];
;                     if (act) { f32x2 a = gelu_pk((f32x2){v0[0], v0[1]}), b = gelu_pk((f32x2){v0[2], v0[3]}), c = gelu_pk((f32x2){v1[0], v1[1]}), d = gelu_pk((f32x2){v1[2], v1[3]});
;                         v0 = (f32x4){a.x, a.y, b.x, b.y}; v1 = (f32x4){c.x, c.y, d.x, d.y}; }
;                     u32x4 w; w.x = cvt_pk_bf16(v0[0], v0[1]); w.y = cvt_pk_bf16(v0[2], v0[3]); w.z = cvt_pk_bf16(v1[0], v1[1]); w.w = cvt_pk_bf16(v1[2], v1[3]);
;                     if (nt) __builtin_nontemporal_store(w, (u32x4*)(rowp + bj * HALF)); else *(u32x4*)(rowp + bj * HALF) = w; } }
.LBB0_307:
	v_cvt_f32_i32_e32 v17, v17
	v_cvt_f32_i32_e32 v16, v16
	v_cvt_pk_bf16_f32 v26, v26, v27
	v_cvt_pk_bf16_f32 v27, v20, v21
	v_cvt_pk_bf16_f32 v28, v28, v29
	v_cvt_f32_i32_e32 v15, v15
	v_cvt_f32_i32_e32 v14, v14
	v_cvt_pk_bf16_f32 v29, v18, v19
	v_cvt_f32_i32_e32 v19, v13
	v_cvt_f32_i32_e32 v11, v11
	v_cvt_f32_i32_e32 v10, v10
	v_cvt_f32_i32_e32 v18, v12
	v_mul_f32_e32 v16, v168, v16
	v_mul_f32_e32 v17, v168, v17
	v_mul_f32_e32 v14, v168, v14
	v_mul_f32_e32 v15, v168, v15
	v_mul_f32_e32 v12, v40, v16
	v_mul_f32_e32 v13, v41, v17
	v_mul_f32_e32 v10, v168, v10
	v_mul_f32_e32 v11, v168, v11
	v_mul_f32_e32 v16, v168, v18
	v_mul_f32_e32 v17, v168, v19
	v_mul_f32_e32 v14, v38, v14
	v_mul_f32_e32 v15, v39, v15
	v_mul_f32_e32 v16, v36, v16
	v_mul_f32_e32 v17, v37, v17
	s_and_b64 vcc, exec, s[4:5]
	v_mul_f32_e32 v18, v34, v10
	v_mul_f32_e32 v19, v35, v11
	global_store_dwordx4 v[42:43], v[26:29], off offset:256
	s_cbranch_vccnz .LBB0_309
	v_and_b32_e32 v11, 0x7fffffff, v15
	v_and_b32_e32 v10, 0x7fffffff, v14
	v_fma_f32 v10, v10, s18, 1.0
	v_fma_f32 v11, v11, s18, 1.0
	v_mov_b64_e32 v[20:21], s[22:23]
	v_rcp_f32_e32 v10, v10
	v_rcp_f32_e32 v11, v11
	v_mul_f32_e32 v28, v14, v14
	v_mul_f32_e32 v29, v15, v15
	v_cmp_gt_f32_e32 vcc, 0, v14
	v_mul_f32_e32 v28, s30, v28
	v_mul_f32_e32 v29, s30, v29
	v_fma_f32 v26, v10, s20, v20
	v_fma_f32 v27, v11, s20, v20
	v_exp_f32_e32 v28, v28
	v_fma_f32 v26, v10, v26, s24
	v_fma_f32 v27, v11, v27, s24
	v_exp_f32_e32 v29, v29
	v_fma_f32 v26, v10, v26, s26
	v_fma_f32 v27, v11, v27, s26
	s_nop 0
	v_fma_f32 v26, v10, v26, s28
	v_fma_f32 v27, v11, v27, s28
	s_nop 0
	v_mul_f32_e32 v10, v10, v26
	v_mul_f32_e32 v11, v11, v27
	v_mul_f32_e32 v26, v12, v12
	v_mul_f32_e32 v27, v13, v13
	v_mul_f32_e32 v10, v28, v10
	v_mul_f32_e32 v11, v29, v11
	v_mul_f32_e32 v26, s30, v26
	v_mul_f32_e32 v27, s30, v27
	v_mul_f32_e32 v28, v14, v10
	v_mul_f32_e32 v29, v15, v11
	v_fma_f32 v10, -v14, v10, v14
	v_fma_f32 v11, -v15, v11, v15
	v_exp_f32_e32 v26, v26
	v_cndmask_b32_e32 v14, v10, v28, vcc
	v_cmp_gt_f32_e32 vcc, 0, v15
	v_and_b32_e32 v10, 0x7fffffff, v12
	v_exp_f32_e32 v27, v27
	v_cndmask_b32_e32 v15, v11, v29, vcc
	v_and_b32_e32 v11, 0x7fffffff, v13
	v_fma_f32 v10, v10, s18, 1.0
	v_fma_f32 v11, v11, s18, 1.0
	v_cmp_gt_f32_e32 vcc, 0, v12
	v_rcp_f32_e32 v10, v10
	v_rcp_f32_e32 v11, v11
	s_nop 0
	v_fma_f32 v28, v10, s20, v20
	v_fma_f32 v29, v11, s20, v20
	s_nop 0
	v_fma_f32 v28, v10, v28, s24
	v_fma_f32 v29, v11, v29, s24
	s_nop 0
	v_fma_f32 v28, v10, v28, s26
	v_fma_f32 v29, v11, v29, s26
	s_nop 0
	v_fma_f32 v28, v10, v28, s28
	v_fma_f32 v29, v11, v29, s28
	s_nop 0
	v_mul_f32_e32 v10, v10, v28
	v_mul_f32_e32 v11, v11, v29
	v_mul_f32_e32 v28, v18, v18
	v_mul_f32_e32 v29, v19, v19
	v_mul_f32_e32 v10, v26, v10
	v_mul_f32_e32 v11, v27, v11
	v_mul_f32_e32 v28, s30, v28
	v_mul_f32_e32 v29, s30, v29
	v_mul_f32_e32 v26, v12, v10
	v_mul_f32_e32 v27, v13, v11
	v_fma_f32 v10, -v12, v10, v12
	v_fma_f32 v11, -v13, v11, v13
	v_exp_f32_e32 v28, v28
	v_cndmask_b32_e32 v12, v10, v26, vcc
	v_cmp_gt_f32_e32 vcc, 0, v13
	v_and_b32_e32 v10, 0x7fffffff, v18
	v_exp_f32_e32 v29, v29
	v_cndmask_b32_e32 v13, v11, v27, vcc
	v_and_b32_e32 v11, 0x7fffffff, v19
	v_fma_f32 v10, v10, s18, 1.0
	v_fma_f32 v11, v11, s18, 1.0
	v_cmp_gt_f32_e32 vcc, 0, v18
	v_rcp_f32_e32 v10, v10
	v_rcp_f32_e32 v11, v11
	s_nop 0
	v_fma_f32 v26, v10, s20, v20
	v_fma_f32 v27, v11, s20, v20
	s_nop 0
	v_fma_f32 v26, v10, v26, s24
	v_fma_f32 v27, v11, v27, s24
	s_nop 0
	v_fma_f32 v26, v10, v26, s26
	v_fma_f32 v27, v11, v27, s26
	s_nop 0
	v_fma_f32 v26, v10, v26, s28
	v_fma_f32 v27, v11, v27, s28
	s_nop 0
	v_mul_f32_e32 v10, v10, v26
	v_mul_f32_e32 v11, v11, v27
	v_mul_f32_e32 v26, v16, v16
	v_mul_f32_e32 v27, v17, v17
	v_mul_f32_e32 v10, v28, v10
	v_mul_f32_e32 v11, v29, v11
	s_nop 0
	v_mul_f32_e32 v28, v18, v10
	v_mul_f32_e32 v29, v19, v11
	v_fma_f32 v10, -v18, v10, v18
	v_fma_f32 v11, -v19, v11, v19
	s_nop 0
	v_cndmask_b32_e32 v18, v10, v28, vcc
	v_cmp_gt_f32_e32 vcc, 0, v19
	v_and_b32_e32 v10, 0x7fffffff, v16
	s_nop 0
	v_cndmask_b32_e32 v19, v11, v29, vcc
	v_and_b32_e32 v11, 0x7fffffff, v17
	v_fma_f32 v10, v10, s18, 1.0
	v_fma_f32 v11, v11, s18, 1.0
	v_cmp_gt_f32_e32 vcc, 0, v16
	v_rcp_f32_e32 v10, v10
	v_rcp_f32_e32 v11, v11
	s_nop 0
	v_fma_f32 v21, v11, s20, v20
	v_fma_f32 v20, v10, s20, v20
	s_nop 0
	v_fma_f32 v20, v10, v20, s24
	v_fma_f32 v21, v11, v21, s24
	s_nop 0
	v_fma_f32 v20, v10, v20, s26
	v_fma_f32 v21, v11, v21, s26
	s_nop 0
	v_fma_f32 v20, v10, v20, s28
	v_fma_f32 v21, v11, v21, s28
	s_nop 0
	v_mul_f32_e32 v10, v10, v20
	v_mul_f32_e32 v11, v11, v21
	v_mul_f32_e32 v20, s30, v26
	v_mul_f32_e32 v21, s30, v27
	s_nop 0
	v_exp_f32_e32 v20, v20
	v_exp_f32_e32 v21, v21
	s_nop 0
	v_mul_f32_e32 v10, v20, v10
	v_mul_f32_e32 v11, v21, v11
	s_nop 0
	v_mul_f32_e32 v20, v16, v10
	v_mul_f32_e32 v21, v17, v11
	v_fma_f32 v10, -v16, v10, v16
	v_fma_f32 v11, -v17, v11, v17
	s_nop 0
	v_cndmask_b32_e32 v16, v10, v20, vcc
	v_cmp_gt_f32_e32 vcc, 0, v17
	s_nop 1
	v_cndmask_b32_e32 v17, v11, v21, vcc
; __device__ __forceinline__ unsigned cvt_pk_bf16(float lo, float hi) { unsigned r; asm volatile("v_cvt_pk_bf16_f32 %0, %1, %2" : "=v"(r) : "v"(lo), "v"(hi)); return r; }
; __device__ __forceinline__ f32x2 gelu_pk(f32x2 v) {
;     const f32x2 av = __builtin_elementwise_abs(v), d = av * 0.2316418882f + 1.0f;
;     f32x2 t; t.x = __builtin_amdgcn_rcpf(d.x); t.y = __builtin_amdgcn_rcpf(d.y);
;     f32x2 q = t * 0.5307027145f + (-0.7265760135f); q = q * t + 0.7107068705f; q = q * t + (-0.142248368f); q = q * t + 0.127414796f; q = q * t;
;     const f32x2 s = (v * v) * (-0.72134752044f);
;     f32x2 e; e.x = __builtin_amdgcn_exp2f(s.x); e.y = __builtin_amdgcn_exp2f(s.y);
;     const f32x2 m = v * (q * e), r = v - m;
;     f32x2 o; o.x = v.x < 0.f ? m.x : r.x; o.y = v.y < 0.f ? m.y : r.y; return o;
;     __device__ __forceinline__ void operator()(const f32x4 (&acc)[2][2][4][2], const Unit& u, int wr, int wc, int fr, int fq) const {
;     ...
;             for (int m = 0; m < 4; ++m) { const int row = row0 + ai * HALF + m * 16; const float rsc = rsv[ai][m]; bf16_t* rowp = O + (size_t)row * ldc + col0;
; #pragma unroll
;                 for (int bj = 0; bj < 2; ++bj) { const i32x4 a0 = __builtin_bit_cast(i32x4, acc[ai][bj][m][0]), a1 = __builtin_bit_cast(i32x4, acc[ai][bj][m][1]);
;                     f32x4 v0 = (f32x4){(float)a0[0], (float)a0[1], (float)a0[2], (float)a0[3]} * rsc * cv[bj][0], v1 = (f32x4){(float)a1[0], (float)a1[1], (float)a1[2], (float)a1[3]} * rsc * cv[bj][1];
;                     if (act) { f32x2 a = gelu_pk((f32x2){v0[0], v0[1]}), b = gelu_pk((f32x2){v0[2], v0[3]}), c = gelu_pk((f32x2){v1[0], v1[1]}), d = gelu_pk((f32x2){v1[2], v1[3]});
;                         v0 = (f32x4){a.x, a.y, b.x, b.y}; v1 = (f32x4){c.x, c.y, d.x, d.y}; }
;                     u32x4 w; w.x = cvt_pk_bf16(v0[0], v0[1]); w.y = cvt_pk_bf16(v0[2], v0[3]); w.z = cvt_pk_bf16(v1[0], v1[1]); w.w = cvt_pk_bf16(v1[2], v1[3]);
;                     if (nt) __builtin_nontemporal_store(w, (u32x4*)(rowp + bj * HALF)); else *(u32x4*)(rowp + bj * HALF) = w; } }
.LBB0_309:
	v_cvt_f32_i32_e32 v7, v7
	v_cvt_f32_i32_e32 v9, v9
	v_cvt_f32_i32_e32 v8, v8
	v_cvt_f32_i32_e32 v6, v6
	v_cvt_pk_bf16_f32 v26, v14, v15
	v_cvt_pk_bf16_f32 v27, v12, v13
	v_cvt_pk_bf16_f32 v28, v18, v19
	v_cvt_pk_bf16_f32 v29, v16, v17
	v_cvt_f32_i32_e32 v15, v3
	v_cvt_f32_i32_e32 v17, v5
	v_cvt_f32_i32_e32 v16, v4
	v_cvt_f32_i32_e32 v14, v2
	v_mov_b32_e32 v169, v168
	v_mov_b32_e32 v12, v168
	v_mov_b32_e32 v13, v168
	v_add_u32_e32 v20, 0xb0, v172
	v_mov_b64_e32 v[10:11], s[66:67]
	v_mul_f32_e32 v8, v12, v8
	v_mul_f32_e32 v9, v13, v9
	v_mul_f32_e32 v6, v168, v6
	v_mul_f32_e32 v7, v169, v7
	v_mad_i64_i32 v[10:11], s[42:43], v20, s86, v[10:11]
	v_mul_f32_e32 v2, v32, v8
	v_mul_f32_e32 v3, v33, v9
	v_mul_f32_e32 v4, v30, v6
	v_mul_f32_e32 v5, v31, v7
	v_mul_f32_e32 v6, v12, v16
	v_mul_f32_e32 v7, v13, v17
	v_mul_f32_e32 v8, v168, v14
	v_mul_f32_e32 v9, v169, v15
	v_lshl_add_u64 v[10:11], v[170:171], 1, v[10:11]
	v_mul_f32_e32 v6, v24, v6
	v_mul_f32_e32 v7, v25, v7
	s_and_b64 vcc, exec, s[4:5]
	v_mul_f32_e32 v8, v22, v8
	v_mul_f32_e32 v9, v23, v9
	global_store_dwordx4 v[10:11], v[26:29], off
	s_cbranch_vccnz .LBB0_311
	v_and_b32_e32 v13, 0x7fffffff, v5
	v_and_b32_e32 v12, 0x7fffffff, v4
	v_fma_f32 v12, v12, s18, 1.0
	v_fma_f32 v13, v13, s18, 1.0
	v_mov_b64_e32 v[14:15], s[22:23]
	v_rcp_f32_e32 v12, v12
	v_rcp_f32_e32 v13, v13
	v_mul_f32_e32 v18, v4, v4
	v_mul_f32_e32 v19, v5, v5
	v_cmp_gt_f32_e32 vcc, 0, v4
	v_mul_f32_e32 v18, s30, v18
	v_mul_f32_e32 v19, s30, v19
	v_fma_f32 v16, v12, s20, v14
	v_fma_f32 v17, v13, s20, v14
	v_exp_f32_e32 v18, v18
	v_fma_f32 v16, v12, v16, s24
	v_fma_f32 v17, v13, v17, s24
	v_exp_f32_e32 v19, v19
	v_fma_f32 v16, v12, v16, s26
	v_fma_f32 v17, v13, v17, s26
	s_nop 0
	v_fma_f32 v16, v12, v16, s28
	v_fma_f32 v17, v13, v17, s28
	s_nop 0
	v_mul_f32_e32 v12, v12, v16
	v_mul_f32_e32 v13, v13, v17
	v_mul_f32_e32 v16, v2, v2
	v_mul_f32_e32 v17, v3, v3
	v_mul_f32_e32 v12, v18, v12
	v_mul_f32_e32 v13, v19, v13
	v_mul_f32_e32 v16, s30, v16
	v_mul_f32_e32 v17, s30, v17
	v_mul_f32_e32 v18, v4, v12
	v_mul_f32_e32 v19, v5, v13
	v_fma_f32 v12, -v4, v12, v4
	v_fma_f32 v13, -v5, v13, v5
	v_exp_f32_e32 v16, v16
	v_cndmask_b32_e32 v4, v12, v18, vcc
	v_cmp_gt_f32_e32 vcc, 0, v5
	v_and_b32_e32 v12, 0x7fffffff, v2
	v_exp_f32_e32 v17, v17
	v_cndmask_b32_e32 v5, v13, v19, vcc
	v_and_b32_e32 v13, 0x7fffffff, v3
	v_fma_f32 v12, v12, s18, 1.0
	v_fma_f32 v13, v13, s18, 1.0
	v_cmp_gt_f32_e32 vcc, 0, v2
	v_rcp_f32_e32 v12, v12
	v_rcp_f32_e32 v13, v13
	s_nop 0
	v_fma_f32 v18, v12, s20, v14
	v_fma_f32 v19, v13, s20, v14
	s_nop 0
	v_fma_f32 v18, v12, v18, s24
	v_fma_f32 v19, v13, v19, s24
	s_nop 0
	v_fma_f32 v18, v12, v18, s26
	v_fma_f32 v19, v13, v19, s26
	s_nop 0
	v_fma_f32 v18, v12, v18, s28
	v_fma_f32 v19, v13, v19, s28
	s_nop 0
	v_mul_f32_e32 v12, v12, v18
	v_mul_f32_e32 v13, v13, v19
	v_mul_f32_e32 v18, v8, v8
	v_mul_f32_e32 v19, v9, v9
	v_mul_f32_e32 v12, v16, v12
	v_mul_f32_e32 v13, v17, v13
	v_mul_f32_e32 v18, s30, v18
	v_mul_f32_e32 v19, s30, v19
	v_mul_f32_e32 v16, v2, v12
	v_mul_f32_e32 v17, v3, v13
	v_fma_f32 v12, -v2, v12, v2
	v_fma_f32 v13, -v3, v13, v3
	v_exp_f32_e32 v18, v18
	v_cndmask_b32_e32 v2, v12, v16, vcc
	v_cmp_gt_f32_e32 vcc, 0, v3
	v_and_b32_e32 v12, 0x7fffffff, v8
	v_exp_f32_e32 v19, v19
	v_cndmask_b32_e32 v3, v13, v17, vcc
	v_and_b32_e32 v13, 0x7fffffff, v9
	v_fma_f32 v12, v12, s18, 1.0
	v_fma_f32 v13, v13, s18, 1.0
	v_cmp_gt_f32_e32 vcc, 0, v8
	v_rcp_f32_e32 v12, v12
	v_rcp_f32_e32 v13, v13
	s_nop 0
	v_fma_f32 v16, v12, s20, v14
	v_fma_f32 v17, v13, s20, v14
	s_nop 0
	v_fma_f32 v16, v12, v16, s24
	v_fma_f32 v17, v13, v17, s24
	s_nop 0
	v_fma_f32 v16, v12, v16, s26
	v_fma_f32 v17, v13, v17, s26
	s_nop 0
	v_fma_f32 v16, v12, v16, s28
	v_fma_f32 v17, v13, v17, s28
	s_nop 0
	v_mul_f32_e32 v12, v12, v16
	v_mul_f32_e32 v13, v13, v17
	v_mul_f32_e32 v16, v6, v6
	v_mul_f32_e32 v17, v7, v7
	v_mul_f32_e32 v12, v18, v12
	v_mul_f32_e32 v13, v19, v13
	s_nop 0
	v_mul_f32_e32 v18, v8, v12
	v_mul_f32_e32 v19, v9, v13
	v_fma_f32 v12, -v8, v12, v8
	v_fma_f32 v13, -v9, v13, v9
	s_nop 0
	v_cndmask_b32_e32 v8, v12, v18, vcc
	v_cmp_gt_f32_e32 vcc, 0, v9
	v_and_b32_e32 v12, 0x7fffffff, v6
	s_nop 0
	v_cndmask_b32_e32 v9, v13, v19, vcc
	v_and_b32_e32 v13, 0x7fffffff, v7
	v_fma_f32 v12, v12, s18, 1.0
	v_fma_f32 v13, v13, s18, 1.0
	v_cmp_gt_f32_e32 vcc, 0, v6
	v_rcp_f32_e32 v12, v12
	v_rcp_f32_e32 v13, v13
	s_nop 0
	v_fma_f32 v15, v13, s20, v14
	v_fma_f32 v14, v12, s20, v14
	s_nop 0
	v_fma_f32 v14, v12, v14, s24
	v_fma_f32 v15, v13, v15, s24
	s_nop 0
	v_fma_f32 v14, v12, v14, s26
	v_fma_f32 v15, v13, v15, s26
	s_nop 0
	v_fma_f32 v14, v12, v14, s28
	v_fma_f32 v15, v13, v15, s28
	s_nop 0
	v_mul_f32_e32 v12, v12, v14
	v_mul_f32_e32 v13, v13, v15
	v_mul_f32_e32 v14, s30, v16
	v_mul_f32_e32 v15, s30, v17
	s_nop 0
	v_exp_f32_e32 v14, v14
	v_exp_f32_e32 v15, v15
	s_nop 0
	v_mul_f32_e32 v12, v14, v12
	v_mul_f32_e32 v13, v15, v13
	s_nop 0
	v_mul_f32_e32 v14, v6, v12
	v_mul_f32_e32 v15, v7, v13
	v_fma_f32 v12, -v6, v12, v6
	v_fma_f32 v13, -v7, v13, v7
	s_nop 0
	v_cndmask_b32_e32 v6, v12, v14, vcc
	v_cmp_gt_f32_e32 vcc, 0, v7
	s_nop 1
	v_cndmask_b32_e32 v7, v13, v15, vcc

; __device__ __forceinline__ f32x2 gelu_pk(f32x2 v) {
;     const f32x2 av = __builtin_elementwise_abs(v), d = av * 0.2316418882f + 1.0f;
;     f32x2 t; t.x = __builtin_amdgcn_rcpf(d.x); t.y = __builtin_amdgcn_rcpf(d.y);
;     f32x2 q = t * 0.5307027145f + (-0.7265760135f); q = q * t + 0.7107068705f; q = q * t + (-0.142248368f); q = q * t + 0.127414796f; q = q * t;
;     const f32x2 s = (v * v) * (-0.72134752044f);
;     f32x2 e; e.x = __builtin_amdgcn_exp2f(s.x); e.y = __builtin_amdgcn_exp2f(s.y);
;     const f32x2 m = v * (q * e), r = v - m;
;     f32x2 o; o.x = v.x < 0.f ? m.x : r.x; o.y = v.y < 0.f ? m.y : r.y; return o;
;     __device__ __forceinline__ void operator()(const f32x4 (&acc)[2][2][4][2], const Unit& u, int wr, int wc, int fr, int fq) const {
;     ...
;             for (int n = 0; n < 2; ++n) cv[bj][n] = *(const f32x4*)(cs + col0 + bj * HALF + 4 * n);
;         float rsv[2][4];
; #pragma unroll
;         for (int ai = 0; ai < 2; ++ai)
; #pragma unroll
;             for (int m = 0; m < 4; ++m) rsv[ai][m] = rs[row0 + ai * HALF + m * 16];
; #pragma unroll
;         for (int ai = 0; ai < 2; ++ai)
; #pragma unroll
;             for (int m = 0; m < 4; ++m) { const int row = row0 + ai * HALF + m * 16; const float rsc = rsv[ai][m]; bf16_t* rowp = O + (size_t)row * ldc + col0;
; #pragma unroll
;                 for (int bj = 0; bj < 2; ++bj) { const i32x4 a0 = __builtin_bit_cast(i32x4, acc[ai][bj][m][0]), a1 = __builtin_bit_cast(i32x4, acc[ai][bj][m][1]);
;                     f32x4 v0 = (f32x4){(float)a0[0], (float)a0[1], (float)a0[2], (float)a0[3]} * rsc * cv[bj][0], v1 = (f32x4){(float)a1[0], (float)a1[1], (float)a1[2], (float)a1[3]} * rsc * cv[bj][1];
;                     if (act) { f32x2 a = gelu_pk((f32x2){v0[0], v0[1]}), b = gelu_pk((f32x2){v0[2], v0[3]}), c = gelu_pk((f32x2){v1[0], v1[1]}), d = gelu_pk((f32x2){v1[2], v1[3]});
;                         v0 = (f32x4){a.x, a.y, b.x, b.y}; v1 = (f32x4){c.x, c.y, d.x, d.y}; }
.LBB0_337:
	v_lshl_add_u32 v172, s4, 8, v200
	v_lshl_or_b32 v170, s2, 8, v196
	v_or_b32_e32 v190, 16, v172
	v_or_b32_e32 v186, 32, v172
	v_or_b32_e32 v182, 48, v172
	v_ashrrev_i32_e32 v171, 31, v170
	v_ashrrev_i32_e32 v173, 31, v172
	v_ashrrev_i32_e32 v191, 31, v190
	v_ashrrev_i32_e32 v187, 31, v186
	v_ashrrev_i32_e32 v183, 31, v182
	v_lshl_add_u64 v[26:27], v[170:171], 2, s[64:65]
	v_lshl_add_u64 v[168:169], v[172:173], 2, s[10:11]
	v_lshl_add_u64 v[174:175], v[190:191], 2, s[10:11]
	v_lshl_add_u64 v[176:177], v[186:187], 2, s[10:11]
	v_lshl_add_u64 v[178:179], v[182:183], 2, s[10:11]
	global_load_dwordx4 v[34:37], v[26:27], off offset:16
	global_load_dwordx4 v[38:41], v[26:27], off
	global_load_dwordx4 v[22:25], v[26:27], off offset:528
	s_nop 0
	global_load_dwordx4 v[26:29], v[26:27], off offset:512
	v_cvt_f32_i32_e32 v145, v145
	global_load_dword v192, v[168:169], off
	global_load_dword v188, v[174:175], off
	global_load_dword v184, v[176:177], off
	global_load_dword v180, v[178:179], off
	s_nop 0
	global_load_dword v178, v[168:169], off offset:512
	global_load_dword v176, v[168:169], off offset:576
	global_load_dword v174, v[168:169], off offset:640
	s_nop 0
	global_load_dword v168, v[168:169], off offset:704
	v_cvt_f32_i32_e32 v144, v144
	v_cvt_f32_i32_e32 v143, v143
	v_cvt_f32_i32_e32 v142, v142
	v_cvt_f32_i32_e32 v141, v141
	v_cvt_f32_i32_e32 v140, v140
	v_cvt_f32_i32_e32 v139, v139
	v_cvt_f32_i32_e32 v138, v138
	s_cmp_lt_i32 s2, 0
	s_cselect_b64 s[40:41], -1, 0
	s_cmp_gt_i32 s2, -1
	s_waitcnt vmcnt(0)
	v_mul_f32_e32 v142, v192, v142
	v_mul_f32_e32 v143, v192, v143
	v_mul_f32_e32 v144, v192, v144
	v_mul_f32_e32 v145, v192, v145
	v_mul_f32_e32 v138, v192, v138
	v_mul_f32_e32 v139, v192, v139
	v_mul_f32_e32 v194, v192, v140
	v_mul_f32_e32 v195, v192, v141
	v_mul_f32_e32 v140, v40, v144
	v_mul_f32_e32 v141, v41, v145
	v_mul_f32_e32 v144, v38, v142
	v_mul_f32_e32 v145, v39, v143
	v_mul_f32_e32 v142, v36, v194
	v_mul_f32_e32 v143, v37, v195
	v_mul_f32_e32 v194, v34, v138
	v_mul_f32_e32 v195, v35, v139
	s_cbranch_scc1 .LBB0_339
	v_and_b32_e32 v139, 0x7fffffff, v145
	v_and_b32_e32 v138, 0x7fffffff, v144
	v_fma_f32 v138, v138, s16, 1.0
	v_fma_f32 v139, v139, s16, 1.0
	v_mov_b64_e32 v[198:199], s[20:21]
	v_rcp_f32_e32 v138, v138
	v_rcp_f32_e32 v139, v139
	v_mul_f32_e32 v204, v144, v144
	v_mul_f32_e32 v205, v145, v145
	v_cmp_gt_f32_e32 vcc, 0, v144
	v_mul_f32_e32 v204, s28, v204
	v_mul_f32_e32 v205, s28, v205
	v_fma_f32 v202, v138, s18, v198
	v_fma_f32 v203, v139, s18, v198
	v_exp_f32_e32 v204, v204
	v_fma_f32 v202, v138, v202, s22
	v_fma_f32 v203, v139, v203, s22
	v_exp_f32_e32 v205, v205
	v_fma_f32 v202, v138, v202, s24
	v_fma_f32 v203, v139, v203, s24
	s_nop 0
	v_fma_f32 v202, v138, v202, s26
	v_fma_f32 v203, v139, v203, s26
	s_nop 0
	v_mul_f32_e32 v138, v138, v202
	v_mul_f32_e32 v139, v139, v203
	v_mul_f32_e32 v202, v140, v140
	v_mul_f32_e32 v203, v141, v141
	v_mul_f32_e32 v138, v204, v138
	v_mul_f32_e32 v139, v205, v139
	v_mul_f32_e32 v202, s28, v202
	v_mul_f32_e32 v203, s28, v203
	v_mul_f32_e32 v204, v144, v138
	v_mul_f32_e32 v205, v145, v139
	v_fma_f32 v138, -v144, v138, v144
	v_fma_f32 v139, -v145, v139, v145
	v_exp_f32_e32 v202, v202
	v_cndmask_b32_e32 v144, v138, v204, vcc
	v_cmp_gt_f32_e32 vcc, 0, v145
	v_and_b32_e32 v138, 0x7fffffff, v140
	v_exp_f32_e32 v203, v203
	v_cndmask_b32_e32 v145, v139, v205, vcc
	v_and_b32_e32 v139, 0x7fffffff, v141
	v_fma_f32 v138, v138, s16, 1.0
	v_fma_f32 v139, v139, s16, 1.0
	v_cmp_gt_f32_e32 vcc, 0, v140
	v_rcp_f32_e32 v138, v138
	v_rcp_f32_e32 v139, v139
	s_nop 0
	v_fma_f32 v204, v138, s18, v198
	v_fma_f32 v205, v139, s18, v198
	s_nop 0
	v_fma_f32 v204, v138, v204, s22
	v_fma_f32 v205, v139, v205, s22
	s_nop 0
	v_fma_f32 v204, v138, v204, s24
	v_fma_f32 v205, v139, v205, s24
	s_nop 0
	v_fma_f32 v204, v138, v204, s26
	v_fma_f32 v205, v139, v205, s26
	s_nop 0
	v_mul_f32_e32 v138, v138, v204
	v_mul_f32_e32 v139, v139, v205
	v_mul_f32_e32 v204, v194, v194
	v_mul_f32_e32 v205, v195, v195
	v_mul_f32_e32 v138, v202, v138
	v_mul_f32_e32 v139, v203, v139
	v_mul_f32_e32 v204, s28, v204
	v_mul_f32_e32 v205, s28, v205
	v_mul_f32_e32 v202, v140, v138
	v_mul_f32_e32 v203, v141, v139
	v_fma_f32 v138, -v140, v138, v140
	v_fma_f32 v139, -v141, v139, v141
	v_exp_f32_e32 v204, v204
	v_cndmask_b32_e32 v140, v138, v202, vcc
	v_cmp_gt_f32_e32 vcc, 0, v141
	v_and_b32_e32 v138, 0x7fffffff, v194
	v_exp_f32_e32 v205, v205
	v_cndmask_b32_e32 v141, v139, v203, vcc
	v_and_b32_e32 v139, 0x7fffffff, v195
	v_fma_f32 v138, v138, s16, 1.0
	v_fma_f32 v139, v139, s16, 1.0
	v_cmp_gt_f32_e32 vcc, 0, v194
	v_rcp_f32_e32 v138, v138
	v_rcp_f32_e32 v139, v139
	s_nop 0
	v_fma_f32 v202, v138, s18, v198
	v_fma_f32 v203, v139, s18, v198
	s_nop 0
	v_fma_f32 v202, v138, v202, s22
	v_fma_f32 v203, v139, v203, s22
	s_nop 0
	v_fma_f32 v202, v138, v202, s24
	v_fma_f32 v203, v139, v203, s24
	s_nop 0
	v_fma_f32 v202, v138, v202, s26
	v_fma_f32 v203, v139, v203, s26
	s_nop 0
	v_mul_f32_e32 v138, v138, v202
	v_mul_f32_e32 v139, v139, v203
	v_mul_f32_e32 v202, v142, v142
	v_mul_f32_e32 v203, v143, v143
	v_mul_f32_e32 v138, v204, v138
	v_mul_f32_e32 v139, v205, v139
	s_nop 0
	v_mul_f32_e32 v204, v194, v138
	v_mul_f32_e32 v205, v195, v139
	v_fma_f32 v138, -v194, v138, v194
	v_fma_f32 v139, -v195, v139, v195
	s_nop 0
	v_cndmask_b32_e32 v194, v138, v204, vcc
	v_cmp_gt_f32_e32 vcc, 0, v195
	v_and_b32_e32 v138, 0x7fffffff, v142
	s_nop 0
	v_cndmask_b32_e32 v195, v139, v205, vcc
	v_and_b32_e32 v139, 0x7fffffff, v143
	v_fma_f32 v138, v138, s16, 1.0
	v_fma_f32 v139, v139, s16, 1.0
	v_cmp_gt_f32_e32 vcc, 0, v142
	v_rcp_f32_e32 v138, v138
	v_rcp_f32_e32 v139, v139
	s_nop 0
	v_fma_f32 v199, v139, s18, v198
	v_fma_f32 v198, v138, s18, v198
	s_nop 0
	v_fma_f32 v198, v138, v198, s22
	v_fma_f32 v199, v139, v199, s22
	s_nop 0
	v_fma_f32 v198, v138, v198, s24
	v_fma_f32 v199, v139, v199, s24
	s_nop 0
	v_fma_f32 v198, v138, v198, s26
	v_fma_f32 v199, v139, v199, s26
	s_nop 0
	v_mul_f32_e32 v138, v138, v198
	v_mul_f32_e32 v139, v139, v199
	v_mul_f32_e32 v198, s28, v202
	v_mul_f32_e32 v199, s28, v203
	s_nop 0
	v_exp_f32_e32 v198, v198
	v_exp_f32_e32 v199, v199
	s_nop 0
	v_mul_f32_e32 v138, v198, v138
	v_mul_f32_e32 v139, v199, v139
	s_nop 0
	v_mul_f32_e32 v198, v142, v138
	v_mul_f32_e32 v199, v143, v139
	v_fma_f32 v138, -v142, v138, v142
	v_fma_f32 v139, -v143, v139, v143
	s_nop 0
	v_cndmask_b32_e32 v142, v138, v198, vcc
	v_cmp_gt_f32_e32 vcc, 0, v143
	s_nop 1
	v_cndmask_b32_e32 v143, v139, v199, vcc
; __device__ __forceinline__ unsigned cvt_pk_bf16(float lo, float hi) { unsigned r; asm volatile("v_cvt_pk_bf16_f32 %0, %1, %2" : "=v"(r) : "v"(lo), "v"(hi)); return r; }
; __device__ __forceinline__ f32x2 gelu_pk(f32x2 v) {
;     const f32x2 av = __builtin_elementwise_abs(v), d = av * 0.2316418882f + 1.0f;
;     f32x2 t; t.x = __builtin_amdgcn_rcpf(d.x); t.y = __builtin_amdgcn_rcpf(d.y);
;     f32x2 q = t * 0.5307027145f + (-0.7265760135f); q = q * t + 0.7107068705f; q = q * t + (-0.142248368f); q = q * t + 0.127414796f; q = q * t;
;     const f32x2 s = (v * v) * (-0.72134752044f);
;     f32x2 e; e.x = __builtin_amdgcn_exp2f(s.x); e.y = __builtin_amdgcn_exp2f(s.y);
;     const f32x2 m = v * (q * e), r = v - m;
;     f32x2 o; o.x = v.x < 0.f ? m.x : r.x; o.y = v.y < 0.f ? m.y : r.y; return o;
;     __device__ __forceinline__ void operator()(const f32x4 (&acc)[2][2][4][2], const Unit& u, int wr, int wc, int fr, int fq) const {
;     ...
;                 for (int bj = 0; bj < 2; ++bj) { const i32x4 a0 = __builtin_bit_cast(i32x4, acc[ai][bj][m][0]), a1 = __builtin_bit_cast(i32x4, acc[ai][bj][m][1]);
;                     f32x4 v0 = (f32x4){(float)a0[0], (float)a0[1], (float)a0[2], (float)a0[3]} * rsc * cv[bj][0], v1 = (f32x4){(float)a1[0], (float)a1[1], (float)a1[2], (float)a1[3]} * rsc * cv[bj][1];
;                     if (act) { f32x2 a = gelu_pk((f32x2){v0[0], v0[1]}), b = gelu_pk((f32x2){v0[2], v0[3]}), c = gelu_pk((f32x2){v1[0], v1[1]}), d = gelu_pk((f32x2){v1[2], v1[3]});
;                         v0 = (f32x4){a.x, a.y, b.x, b.y}; v1 = (f32x4){c.x, c.y, d.x, d.y}; }
;                     u32x4 w; w.x = cvt_pk_bf16(v0[0], v0[1]); w.y = cvt_pk_bf16(v0[2], v0[3]); w.z = cvt_pk_bf16(v1[0], v1[1]); w.w = cvt_pk_bf16(v1[2], v1[3]);
;                     if (nt) __builtin_nontemporal_store(w, (u32x4*)(rowp + bj * HALF)); else *(u32x4*)(rowp + bj * HALF) = w; } }
.LBB0_339:
	v_cvt_f32_i32_e32 v137, v137
	v_cvt_f32_i32_e32 v136, v136
	v_cvt_pk_bf16_f32 v202, v144, v145
	v_cvt_pk_bf16_f32 v203, v140, v141
	v_cvt_pk_bf16_f32 v204, v194, v195
	v_cvt_pk_bf16_f32 v205, v142, v143
	v_cvt_f32_i32_e32 v143, v133
	v_cvt_f32_i32_e32 v142, v132
	v_cvt_f32_i32_e32 v135, v135
	v_cvt_f32_i32_e32 v134, v134
	v_cvt_f32_i32_e32 v131, v131
	v_cvt_f32_i32_e32 v130, v130
	v_mov_b32_e32 v140, v192
	v_mov_b32_e32 v141, v192
	v_mul_f32_e32 v136, v140, v136
	v_mul_f32_e32 v137, v141, v137
	v_mov_b32_e32 v193, v192
	v_lshlrev_b64 v[138:139], 15, v[172:173]
	v_mul_f32_e32 v132, v28, v136
	v_mul_f32_e32 v133, v29, v137
	v_mul_f32_e32 v136, v140, v142
	v_mul_f32_e32 v137, v141, v143
	v_lshl_add_u64 v[138:139], s[70:71], 0, v[138:139]
	v_mul_f32_e32 v134, v192, v134
	v_mul_f32_e32 v135, v193, v135
	v_mul_f32_e32 v140, v192, v130
	v_mul_f32_e32 v141, v193, v131
	v_mul_f32_e32 v130, v24, v136
	v_mul_f32_e32 v131, v25, v137
	v_cndmask_b32_e64 v136, 0, 1, s[40:41]
	v_lshl_add_u64 v[138:139], v[170:171], 1, v[138:139]
	v_mul_f32_e32 v134, v26, v134
	v_mul_f32_e32 v135, v27, v135
	v_cmp_ne_u32_e64 s[4:5], 1, v136
	s_andn2_b64 vcc, exec, s[40:41]
	v_mul_f32_e32 v136, v22, v140
	v_mul_f32_e32 v137, v23, v141
	global_store_dwordx4 v[138:139], v[202:205], off
	s_cbranch_vccnz .LBB0_341
	v_and_b32_e32 v141, 0x7fffffff, v135
	v_and_b32_e32 v140, 0x7fffffff, v134
	v_fma_f32 v140, v140, s16, 1.0
	v_fma_f32 v141, v141, s16, 1.0
	v_mov_b64_e32 v[142:143], s[20:21]
	v_rcp_f32_e32 v140, v140
	v_rcp_f32_e32 v141, v141
	v_mul_f32_e32 v192, v134, v134
	v_mul_f32_e32 v193, v135, v135
	v_cmp_gt_f32_e32 vcc, 0, v134
	v_mul_f32_e32 v192, s28, v192
	v_mul_f32_e32 v193, s28, v193
	v_fma_f32 v144, v140, s18, v142
	v_fma_f32 v145, v141, s18, v142
	v_exp_f32_e32 v192, v192
	v_fma_f32 v144, v140, v144, s22
	v_fma_f32 v145, v141, v145, s22
	v_exp_f32_e32 v193, v193
	v_fma_f32 v144, v140, v144, s24
	v_fma_f32 v145, v141, v145, s24
	s_nop 0
	v_fma_f32 v144, v140, v144, s26
	v_fma_f32 v145, v141, v145, s26
	s_nop 0
	v_mul_f32_e32 v140, v140, v144
	v_mul_f32_e32 v141, v141, v145
	v_mul_f32_e32 v144, v132, v132
	v_mul_f32_e32 v145, v133, v133
	v_mul_f32_e32 v140, v192, v140
	v_mul_f32_e32 v141, v193, v141
	v_mul_f32_e32 v144, s28, v144
	v_mul_f32_e32 v145, s28, v145
	v_mul_f32_e32 v192, v134, v140
	v_mul_f32_e32 v193, v135, v141
	v_fma_f32 v140, -v134, v140, v134
	v_fma_f32 v141, -v135, v141, v135
	v_exp_f32_e32 v144, v144
	v_cndmask_b32_e32 v134, v140, v192, vcc
	v_cmp_gt_f32_e32 vcc, 0, v135
	v_and_b32_e32 v140, 0x7fffffff, v132
	v_exp_f32_e32 v145, v145
	v_cndmask_b32_e32 v135, v141, v193, vcc
	v_and_b32_e32 v141, 0x7fffffff, v133
	v_fma_f32 v140, v140, s16, 1.0
	v_fma_f32 v141, v141, s16, 1.0
	v_cmp_gt_f32_e32 vcc, 0, v132
	v_rcp_f32_e32 v140, v140
	v_rcp_f32_e32 v141, v141
	s_nop 0
	v_fma_f32 v192, v140, s18, v142
	v_fma_f32 v193, v141, s18, v142
	s_nop 0
	v_fma_f32 v192, v140, v192, s22
	v_fma_f32 v193, v141, v193, s22
	s_nop 0
	v_fma_f32 v192, v140, v192, s24
	v_fma_f32 v193, v141, v193, s24
	s_nop 0
	v_fma_f32 v192, v140, v192, s26
	v_fma_f32 v193, v141, v193, s26
	s_nop 0
	v_mul_f32_e32 v140, v140, v192
	v_mul_f32_e32 v141, v141, v193
	v_mul_f32_e32 v192, v136, v136
	v_mul_f32_e32 v193, v137, v137
	v_mul_f32_e32 v140, v144, v140
	v_mul_f32_e32 v141, v145, v141
	v_mul_f32_e32 v192, s28, v192
	v_mul_f32_e32 v193, s28, v193
	v_mul_f32_e32 v144, v132, v140
	v_mul_f32_e32 v145, v133, v141
	v_fma_f32 v140, -v132, v140, v132
	v_fma_f32 v141, -v133, v141, v133
	v_exp_f32_e32 v192, v192
	v_cndmask_b32_e32 v132, v140, v144, vcc
	v_cmp_gt_f32_e32 vcc, 0, v133
	v_and_b32_e32 v140, 0x7fffffff, v136
	v_exp_f32_e32 v193, v193
	v_cndmask_b32_e32 v133, v141, v145, vcc
	v_and_b32_e32 v141, 0x7fffffff, v137
	v_fma_f32 v140, v140, s16, 1.0
	v_fma_f32 v141, v141, s16, 1.0
	v_cmp_gt_f32_e32 vcc, 0, v136
	v_rcp_f32_e32 v140, v140
	v_rcp_f32_e32 v141, v141
	s_nop 0
	v_fma_f32 v144, v140, s18, v142
	v_fma_f32 v145, v141, s18, v142
	s_nop 0
	v_fma_f32 v144, v140, v144, s22
	v_fma_f32 v145, v141, v145, s22
	s_nop 0
	v_fma_f32 v144, v140, v144, s24
	v_fma_f32 v145, v141, v145, s24
	s_nop 0
	v_fma_f32 v144, v140, v144, s26
	v_fma_f32 v145, v141, v145, s26
	s_nop 0
	v_mul_f32_e32 v140, v140, v144
	v_mul_f32_e32 v141, v141, v145
	v_mul_f32_e32 v144, v130, v130
	v_mul_f32_e32 v145, v131, v131
	v_mul_f32_e32 v140, v192, v140
	v_mul_f32_e32 v141, v193, v141
	s_nop 0
	v_mul_f32_e32 v192, v136, v140
	v_mul_f32_e32 v193, v137, v141
	v_fma_f32 v140, -v136, v140, v136
	v_fma_f32 v141, -v137, v141, v137
	s_nop 0
	v_cndmask_b32_e32 v136, v140, v192, vcc
	v_cmp_gt_f32_e32 vcc, 0, v137
	v_and_b32_e32 v140, 0x7fffffff, v130
	s_nop 0
	v_cndmask_b32_e32 v137, v141, v193, vcc
	v_and_b32_e32 v141, 0x7fffffff, v131
	v_fma_f32 v140, v140, s16, 1.0
	v_fma_f32 v141, v141, s16, 1.0
	v_cmp_gt_f32_e32 vcc, 0, v130
	v_rcp_f32_e32 v140, v140
	v_rcp_f32_e32 v141, v141
	s_nop 0
	v_fma_f32 v143, v141, s18, v142
	v_fma_f32 v142, v140, s18, v142
	s_nop 0
	v_fma_f32 v142, v140, v142, s22
	v_fma_f32 v143, v141, v143, s22
	s_nop 0
	v_fma_f32 v142, v140, v142, s24
	v_fma_f32 v143, v141, v143, s24
	s_nop 0
	v_fma_f32 v142, v140, v142, s26
	v_fma_f32 v143, v141, v143, s26
	s_nop 0
	v_mul_f32_e32 v140, v140, v142
	v_mul_f32_e32 v141, v141, v143
	v_mul_f32_e32 v142, s28, v144
	v_mul_f32_e32 v143, s28, v145
	s_nop 0
	v_exp_f32_e32 v142, v142
	v_exp_f32_e32 v143, v143
	s_nop 0
	v_mul_f32_e32 v140, v142, v140
	v_mul_f32_e32 v141, v143, v141
	s_nop 0
	v_mul_f32_e32 v142, v130, v140
	v_mul_f32_e32 v143, v131, v141
	v_fma_f32 v140, -v130, v140, v130
	v_fma_f32 v141, -v131, v141, v131
	s_nop 0
	v_cndmask_b32_e32 v130, v140, v142, vcc
	v_cmp_gt_f32_e32 vcc, 0, v131
	s_nop 1
	v_cndmask_b32_e32 v131, v141, v143, vcc
; __device__ __forceinline__ unsigned cvt_pk_bf16(float lo, float hi) { unsigned r; asm volatile("v_cvt_pk_bf16_f32 %0, %1, %2" : "=v"(r) : "v"(lo), "v"(hi)); return r; }
; __device__ __forceinline__ f32x2 gelu_pk(f32x2 v) {
;     const f32x2 av = __builtin_elementwise_abs(v), d = av * 0.2316418882f + 1.0f;
;     f32x2 t; t.x = __builtin_amdgcn_rcpf(d.x); t.y = __builtin_amdgcn_rcpf(d.y);
;     f32x2 q = t * 0.5307027145f + (-0.7265760135f); q = q * t + 0.7107068705f; q = q * t + (-0.142248368f); q = q * t + 0.127414796f; q = q * t;
;     const f32x2 s = (v * v) * (-0.72134752044f);
;     f32x2 e; e.x = __builtin_amdgcn_exp2f(s.x); e.y = __builtin_amdgcn_exp2f(s.y);
;     const f32x2 m = v * (q * e), r = v - m;
;     f32x2 o; o.x = v.x < 0.f ? m.x : r.x; o.y = v.y < 0.f ? m.y : r.y; return o;
;     __device__ __forceinline__ void operator()(const f32x4 (&acc)[2][2][4][2], const Unit& u, int wr, int wc, int fr, int fq) const {
;     ...
;                 for (int bj = 0; bj < 2; ++bj) { const i32x4 a0 = __builtin_bit_cast(i32x4, acc[ai][bj][m][0]), a1 = __builtin_bit_cast(i32x4, acc[ai][bj][m][1]);
;                     f32x4 v0 = (f32x4){(float)a0[0], (float)a0[1], (float)a0[2], (float)a0[3]} * rsc * cv[bj][0], v1 = (f32x4){(float)a1[0], (float)a1[1], (float)a1[2], (float)a1[3]} * rsc * cv[bj][1];
;                     if (act) { f32x2 a = gelu_pk((f32x2){v0[0], v0[1]}), b = gelu_pk((f32x2){v0[2], v0[3]}), c = gelu_pk((f32x2){v1[0], v1[1]}), d = gelu_pk((f32x2){v1[2], v1[3]});
;                         v0 = (f32x4){a.x, a.y, b.x, b.y}; v1 = (f32x4){c.x, c.y, d.x, d.y}; }
;                     u32x4 w; w.x = cvt_pk_bf16(v0[0], v0[1]); w.y = cvt_pk_bf16(v0[2], v0[3]); w.z = cvt_pk_bf16(v1[0], v1[1]); w.w = cvt_pk_bf16(v1[2], v1[3]);
;                     if (nt) __builtin_nontemporal_store(w, (u32x4*)(rowp + bj * HALF)); else *(u32x4*)(rowp + bj * HALF) = w; } }
.LBB0_341:
	v_cvt_f32_i32_e32 v129, v129
	v_cvt_f32_i32_e32 v128, v128
	v_cvt_pk_bf16_f32 v134, v134, v135
	v_cvt_pk_bf16_f32 v135, v132, v133
	v_cvt_pk_bf16_f32 v136, v136, v137
	v_cvt_f32_i32_e32 v127, v127
	v_cvt_f32_i32_e32 v126, v126
	v_cvt_pk_bf16_f32 v137, v130, v131
	v_cvt_f32_i32_e32 v131, v125
	v_cvt_f32_i32_e32 v123, v123
	v_cvt_f32_i32_e32 v122, v122
	v_cvt_f32_i32_e32 v130, v124
	v_mul_f32_e32 v128, v188, v128
	v_mul_f32_e32 v129, v188, v129
	v_mul_f32_e32 v126, v188, v126
	v_mul_f32_e32 v127, v188, v127
	v_mul_f32_e32 v124, v40, v128
	v_mul_f32_e32 v125, v41, v129
	v_mul_f32_e32 v122, v188, v122
	v_mul_f32_e32 v123, v188, v123
	v_mul_f32_e32 v128, v188, v130
	v_mul_f32_e32 v129, v188, v131
	v_mul_f32_e32 v126, v38, v126
	v_mul_f32_e32 v127, v39, v127
	v_mul_f32_e32 v128, v36, v128
	v_mul_f32_e32 v129, v37, v129
	s_and_b64 vcc, exec, s[4:5]
	v_mul_f32_e32 v130, v34, v122
	v_mul_f32_e32 v131, v35, v123
	global_store_dwordx4 v[138:139], v[134:137], off offset:256
	s_cbranch_vccnz .LBB0_343
	v_and_b32_e32 v123, 0x7fffffff, v127
	v_and_b32_e32 v122, 0x7fffffff, v126
	v_fma_f32 v122, v122, s16, 1.0
	v_fma_f32 v123, v123, s16, 1.0
	v_mov_b64_e32 v[132:133], s[20:21]
	v_rcp_f32_e32 v122, v122
	v_rcp_f32_e32 v123, v123
	v_mul_f32_e32 v136, v126, v126
	v_mul_f32_e32 v137, v127, v127
	v_cmp_gt_f32_e32 vcc, 0, v126
	v_mul_f32_e32 v136, s28, v136
	v_mul_f32_e32 v137, s28, v137
	v_fma_f32 v134, v122, s18, v132
	v_fma_f32 v135, v123, s18, v132
	v_exp_f32_e32 v136, v136
	v_fma_f32 v134, v122, v134, s22
	v_fma_f32 v135, v123, v135, s22
	v_exp_f32_e32 v137, v137
	v_fma_f32 v134, v122, v134, s24
	v_fma_f32 v135, v123, v135, s24
	s_nop 0
	v_fma_f32 v134, v122, v134, s26
	v_fma_f32 v135, v123, v135, s26
	s_nop 0
	v_mul_f32_e32 v122, v122, v134
	v_mul_f32_e32 v123, v123, v135
	v_mul_f32_e32 v134, v124, v124
	v_mul_f32_e32 v135, v125, v125
	v_mul_f32_e32 v122, v136, v122
	v_mul_f32_e32 v123, v137, v123
	v_mul_f32_e32 v134, s28, v134
	v_mul_f32_e32 v135, s28, v135
	v_mul_f32_e32 v136, v126, v122
	v_mul_f32_e32 v137, v127, v123
	v_fma_f32 v122, -v126, v122, v126
	v_fma_f32 v123, -v127, v123, v127
	v_exp_f32_e32 v134, v134
	v_cndmask_b32_e32 v126, v122, v136, vcc
	v_cmp_gt_f32_e32 vcc, 0, v127
	v_and_b32_e32 v122, 0x7fffffff, v124
	v_exp_f32_e32 v135, v135
	v_cndmask_b32_e32 v127, v123, v137, vcc
	v_and_b32_e32 v123, 0x7fffffff, v125
	v_fma_f32 v122, v122, s16, 1.0
	v_fma_f32 v123, v123, s16, 1.0
	v_cmp_gt_f32_e32 vcc, 0, v124
	v_rcp_f32_e32 v122, v122
	v_rcp_f32_e32 v123, v123
	s_nop 0
	v_fma_f32 v136, v122, s18, v132
	v_fma_f32 v137, v123, s18, v132
	s_nop 0
	v_fma_f32 v136, v122, v136, s22
	v_fma_f32 v137, v123, v137, s22
	s_nop 0
	v_fma_f32 v136, v122, v136, s24
	v_fma_f32 v137, v123, v137, s24
	s_nop 0
	v_fma_f32 v136, v122, v136, s26
	v_fma_f32 v137, v123, v137, s26
	s_nop 0
	v_mul_f32_e32 v122, v122, v136
	v_mul_f32_e32 v123, v123, v137
	v_mul_f32_e32 v136, v130, v130
	v_mul_f32_e32 v137, v131, v131
	v_mul_f32_e32 v122, v134, v122
	v_mul_f32_e32 v123, v135, v123
	v_mul_f32_e32 v136, s28, v136
	v_mul_f32_e32 v137, s28, v137
	v_mul_f32_e32 v134, v124, v122
	v_mul_f32_e32 v135, v125, v123
	v_fma_f32 v122, -v124, v122, v124
	v_fma_f32 v123, -v125, v123, v125
	v_exp_f32_e32 v136, v136
	v_cndmask_b32_e32 v124, v122, v134, vcc
	v_cmp_gt_f32_e32 vcc, 0, v125
	v_and_b32_e32 v122, 0x7fffffff, v130
	v_exp_f32_e32 v137, v137
	v_cndmask_b32_e32 v125, v123, v135, vcc
	v_and_b32_e32 v123, 0x7fffffff, v131
	v_fma_f32 v122, v122, s16, 1.0
	v_fma_f32 v123, v123, s16, 1.0
	v_cmp_gt_f32_e32 vcc, 0, v130
	v_rcp_f32_e32 v122, v122
	v_rcp_f32_e32 v123, v123
	s_nop 0
	v_fma_f32 v134, v122, s18, v132
	v_fma_f32 v135, v123, s18, v132
	s_nop 0
	v_fma_f32 v134, v122, v134, s22
	v_fma_f32 v135, v123, v135, s22
	s_nop 0
	v_fma_f32 v134, v122, v134, s24
	v_fma_f32 v135, v123, v135, s24
	s_nop 0
	v_fma_f32 v134, v122, v134, s26
	v_fma_f32 v135, v123, v135, s26
	s_nop 0
	v_mul_f32_e32 v122, v122, v134
	v_mul_f32_e32 v123, v123, v135
	v_mul_f32_e32 v134, v128, v128
	v_mul_f32_e32 v135, v129, v129
	v_mul_f32_e32 v122, v136, v122
	v_mul_f32_e32 v123, v137, v123
	s_nop 0
	v_mul_f32_e32 v136, v130, v122
	v_mul_f32_e32 v137, v131, v123
	v_fma_f32 v122, -v130, v122, v130
	v_fma_f32 v123, -v131, v123, v131
	s_nop 0
	v_cndmask_b32_e32 v130, v122, v136, vcc
	v_cmp_gt_f32_e32 vcc, 0, v131
	v_and_b32_e32 v122, 0x7fffffff, v128
	s_nop 0
	v_cndmask_b32_e32 v131, v123, v137, vcc
	v_and_b32_e32 v123, 0x7fffffff, v129
	v_fma_f32 v122, v122, s16, 1.0
	v_fma_f32 v123, v123, s16, 1.0
	v_cmp_gt_f32_e32 vcc, 0, v128
	v_rcp_f32_e32 v122, v122
	v_rcp_f32_e32 v123, v123
	s_nop 0
	v_fma_f32 v133, v123, s18, v132
	v_fma_f32 v132, v122, s18, v132
	s_nop 0
	v_fma_f32 v132, v122, v132, s22
	v_fma_f32 v133, v123, v133, s22
	s_nop 0
	v_fma_f32 v132, v122, v132, s24
	v_fma_f32 v133, v123, v133, s24
	s_nop 0
	v_fma_f32 v132, v122, v132, s26
	v_fma_f32 v133, v123, v133, s26
	s_nop 0
	v_mul_f32_e32 v122, v122, v132
	v_mul_f32_e32 v123, v123, v133
	v_mul_f32_e32 v132, s28, v134
	v_mul_f32_e32 v133, s28, v135
	s_nop 0
	v_exp_f32_e32 v132, v132
	v_exp_f32_e32 v133, v133
	s_nop 0
	v_mul_f32_e32 v122, v132, v122
	v_mul_f32_e32 v123, v133, v123
	s_nop 0
	v_mul_f32_e32 v132, v128, v122
	v_mul_f32_e32 v133, v129, v123
	v_fma_f32 v122, -v128, v122, v128
	v_fma_f32 v123, -v129, v123, v129
	s_nop 0
	v_cndmask_b32_e32 v128, v122, v132, vcc
	v_cmp_gt_f32_e32 vcc, 0, v129
	s_nop 1
	v_cndmask_b32_e32 v129, v123, v133, vcc
; __device__ __forceinline__ unsigned cvt_pk_bf16(float lo, float hi) { unsigned r; asm volatile("v_cvt_pk_bf16_f32 %0, %1, %2" : "=v"(r) : "v"(lo), "v"(hi)); return r; }
; __device__ __forceinline__ f32x2 gelu_pk(f32x2 v) {
;     const f32x2 av = __builtin_elementwise_abs(v), d = av * 0.2316418882f + 1.0f;
;     f32x2 t; t.x = __builtin_amdgcn_rcpf(d.x); t.y = __builtin_amdgcn_rcpf(d.y);
;     f32x2 q = t * 0.5307027145f + (-0.7265760135f); q = q * t + 0.7107068705f; q = q * t + (-0.142248368f); q = q * t + 0.127414796f; q = q * t;
;     const f32x2 s = (v * v) * (-0.72134752044f);
;     f32x2 e; e.x = __builtin_amdgcn_exp2f(s.x); e.y = __builtin_amdgcn_exp2f(s.y);
;     const f32x2 m = v * (q * e), r = v - m;
;     f32x2 o; o.x = v.x < 0.f ? m.x : r.x; o.y = v.y < 0.f ? m.y : r.y; return o;
;     __device__ __forceinline__ void operator()(const f32x4 (&acc)[2][2][4][2], const Unit& u, int wr, int wc, int fr, int fq) const {
;     ...
;                 for (int bj = 0; bj < 2; ++bj) { const i32x4 a0 = __builtin_bit_cast(i32x4, acc[ai][bj][m][0]), a1 = __builtin_bit_cast(i32x4, acc[ai][bj][m][1]);
;                     f32x4 v0 = (f32x4){(float)a0[0], (float)a0[1], (float)a0[2], (float)a0[3]} * rsc * cv[bj][0], v1 = (f32x4){(float)a1[0], (float)a1[1], (float)a1[2], (float)a1[3]} * rsc * cv[bj][1];
;                     if (act) { f32x2 a = gelu_pk((f32x2){v0[0], v0[1]}), b = gelu_pk((f32x2){v0[2], v0[3]}), c = gelu_pk((f32x2){v1[0], v1[1]}), d = gelu_pk((f32x2){v1[2], v1[3]});
;                         v0 = (f32x4){a.x, a.y, b.x, b.y}; v1 = (f32x4){c.x, c.y, d.x, d.y}; }
;                     u32x4 w; w.x = cvt_pk_bf16(v0[0], v0[1]); w.y = cvt_pk_bf16(v0[2], v0[3]); w.z = cvt_pk_bf16(v1[0], v1[1]); w.w = cvt_pk_bf16(v1[2], v1[3]);
;                     if (nt) __builtin_nontemporal_store(w, (u32x4*)(rowp + bj * HALF)); else *(u32x4*)(rowp + bj * HALF) = w; } }
.LBB0_343:
	v_cvt_f32_i32_e32 v121, v121
	v_cvt_f32_i32_e32 v120, v120
	v_cvt_pk_bf16_f32 v132, v126, v127
	v_cvt_f32_i32_e32 v119, v119
	v_cvt_f32_i32_e32 v118, v118
	v_cvt_f32_i32_e32 v115, v115
	v_cvt_f32_i32_e32 v127, v117
	v_cvt_f32_i32_e32 v126, v116
	v_cvt_f32_i32_e32 v114, v114
	v_cvt_pk_bf16_f32 v133, v124, v125
	v_mov_b32_e32 v124, v188
	v_mov_b32_e32 v125, v188
	v_mov_b32_e32 v189, v188
	v_lshlrev_b64 v[122:123], 15, v[190:191]
	v_mul_f32_e32 v120, v124, v120
	v_mul_f32_e32 v121, v125, v121
	v_lshl_add_u64 v[122:123], s[70:71], 0, v[122:123]
	v_mul_f32_e32 v118, v188, v118
	v_mul_f32_e32 v119, v189, v119
	v_mul_f32_e32 v116, v28, v120
	v_mul_f32_e32 v117, v29, v121
	v_mul_f32_e32 v120, v124, v126
	v_mul_f32_e32 v121, v125, v127
	v_mul_f32_e32 v124, v188, v114
	v_mul_f32_e32 v125, v189, v115
	v_lshl_add_u64 v[122:123], v[170:171], 1, v[122:123]
	v_mul_f32_e32 v118, v26, v118
	v_mul_f32_e32 v119, v27, v119
	v_mul_f32_e32 v114, v24, v120
	v_mul_f32_e32 v115, v25, v121
	s_and_b64 vcc, exec, s[4:5]
	v_mul_f32_e32 v120, v22, v124
	v_mul_f32_e32 v121, v23, v125
	v_cvt_pk_bf16_f32 v134, v130, v131
	v_cvt_pk_bf16_f32 v135, v128, v129
	global_store_dwordx4 v[122:123], v[132:135], off
	s_cbranch_vccnz .LBB0_345
	v_and_b32_e32 v125, 0x7fffffff, v119
	v_and_b32_e32 v124, 0x7fffffff, v118
	v_fma_f32 v124, v124, s16, 1.0
	v_fma_f32 v125, v125, s16, 1.0
	v_mov_b64_e32 v[126:127], s[20:21]
	v_rcp_f32_e32 v124, v124
	v_rcp_f32_e32 v125, v125
	v_mul_f32_e32 v130, v118, v118
	v_mul_f32_e32 v131, v119, v119
	v_cmp_gt_f32_e32 vcc, 0, v118
	v_mul_f32_e32 v130, s28, v130
	v_mul_f32_e32 v131, s28, v131
	v_fma_f32 v128, v124, s18, v126
	v_fma_f32 v129, v125, s18, v126
	v_exp_f32_e32 v130, v130
	v_fma_f32 v128, v124, v128, s22
	v_fma_f32 v129, v125, v129, s22
	v_exp_f32_e32 v131, v131
	v_fma_f32 v128, v124, v128, s24
	v_fma_f32 v129, v125, v129, s24
	s_nop 0
	v_fma_f32 v128, v124, v128, s26
	v_fma_f32 v129, v125, v129, s26
	s_nop 0
	v_mul_f32_e32 v124, v124, v128
	v_mul_f32_e32 v125, v125, v129
	v_mul_f32_e32 v128, v116, v116
	v_mul_f32_e32 v129, v117, v117
	v_mul_f32_e32 v124, v130, v124
	v_mul_f32_e32 v125, v131, v125
	v_mul_f32_e32 v128, s28, v128
	v_mul_f32_e32 v129, s28, v129
	v_mul_f32_e32 v130, v118, v124
	v_mul_f32_e32 v131, v119, v125
	v_fma_f32 v124, -v118, v124, v118
	v_fma_f32 v125, -v119, v125, v119
	v_exp_f32_e32 v128, v128
	v_cndmask_b32_e32 v118, v124, v130, vcc
	v_cmp_gt_f32_e32 vcc, 0, v119
	v_and_b32_e32 v124, 0x7fffffff, v116
	v_exp_f32_e32 v129, v129
	v_cndmask_b32_e32 v119, v125, v131, vcc
	v_and_b32_e32 v125, 0x7fffffff, v117
	v_fma_f32 v124, v124, s16, 1.0
	v_fma_f32 v125, v125, s16, 1.0
	v_cmp_gt_f32_e32 vcc, 0, v116
	v_rcp_f32_e32 v124, v124
	v_rcp_f32_e32 v125, v125
	s_nop 0
	v_fma_f32 v130, v124, s18, v126
	v_fma_f32 v131, v125, s18, v126
	s_nop 0
	v_fma_f32 v130, v124, v130, s22
	v_fma_f32 v131, v125, v131, s22
	s_nop 0
	v_fma_f32 v130, v124, v130, s24
	v_fma_f32 v131, v125, v131, s24
	s_nop 0
	v_fma_f32 v130, v124, v130, s26
	v_fma_f32 v131, v125, v131, s26
	s_nop 0
	v_mul_f32_e32 v124, v124, v130
	v_mul_f32_e32 v125, v125, v131
	v_mul_f32_e32 v130, v120, v120
	v_mul_f32_e32 v131, v121, v121
	v_mul_f32_e32 v124, v128, v124
	v_mul_f32_e32 v125, v129, v125
	v_mul_f32_e32 v130, s28, v130
	v_mul_f32_e32 v131, s28, v131
	v_mul_f32_e32 v128, v116, v124
	v_mul_f32_e32 v129, v117, v125
	v_fma_f32 v124, -v116, v124, v116
	v_fma_f32 v125, -v117, v125, v117
	v_exp_f32_e32 v130, v130
	v_cndmask_b32_e32 v116, v124, v128, vcc
	v_cmp_gt_f32_e32 vcc, 0, v117
	v_and_b32_e32 v124, 0x7fffffff, v120
	v_exp_f32_e32 v131, v131
	v_cndmask_b32_e32 v117, v125, v129, vcc
	v_and_b32_e32 v125, 0x7fffffff, v121
	v_fma_f32 v124, v124, s16, 1.0
	v_fma_f32 v125, v125, s16, 1.0
	v_cmp_gt_f32_e32 vcc, 0, v120
	v_rcp_f32_e32 v124, v124
	v_rcp_f32_e32 v125, v125
	s_nop 0
	v_fma_f32 v128, v124, s18, v126
	v_fma_f32 v129, v125, s18, v126
	s_nop 0
	v_fma_f32 v128, v124, v128, s22
	v_fma_f32 v129, v125, v129, s22
	s_nop 0
	v_fma_f32 v128, v124, v128, s24
	v_fma_f32 v129, v125, v129, s24
	s_nop 0
	v_fma_f32 v128, v124, v128, s26
	v_fma_f32 v129, v125, v129, s26
	s_nop 0
	v_mul_f32_e32 v124, v124, v128
	v_mul_f32_e32 v125, v125, v129
	v_mul_f32_e32 v128, v114, v114
	v_mul_f32_e32 v129, v115, v115
	v_mul_f32_e32 v124, v130, v124
	v_mul_f32_e32 v125, v131, v125
	s_nop 0
	v_mul_f32_e32 v130, v120, v124
	v_mul_f32_e32 v131, v121, v125
	v_fma_f32 v124, -v120, v124, v120
	v_fma_f32 v125, -v121, v125, v121
	s_nop 0
	v_cndmask_b32_e32 v120, v124, v130, vcc
	v_cmp_gt_f32_e32 vcc, 0, v121
	v_and_b32_e32 v124, 0x7fffffff, v114
	s_nop 0
	v_cndmask_b32_e32 v121, v125, v131, vcc
	v_and_b32_e32 v125, 0x7fffffff, v115
	v_fma_f32 v124, v124, s16, 1.0
	v_fma_f32 v125, v125, s16, 1.0
	v_cmp_gt_f32_e32 vcc, 0, v114
	v_rcp_f32_e32 v124, v124
	v_rcp_f32_e32 v125, v125
	s_nop 0
	v_fma_f32 v127, v125, s18, v126
	v_fma_f32 v126, v124, s18, v126
	s_nop 0
	v_fma_f32 v126, v124, v126, s22
	v_fma_f32 v127, v125, v127, s22
	s_nop 0
	v_fma_f32 v126, v124, v126, s24
	v_fma_f32 v127, v125, v127, s24
	s_nop 0
	v_fma_f32 v126, v124, v126, s26
	v_fma_f32 v127, v125, v127, s26
	s_nop 0
	v_mul_f32_e32 v124, v124, v126
	v_mul_f32_e32 v125, v125, v127
	v_mul_f32_e32 v126, s28, v128
	v_mul_f32_e32 v127, s28, v129
	s_nop 0
	v_exp_f32_e32 v126, v126
	v_exp_f32_e32 v127, v127
	s_nop 0
	v_mul_f32_e32 v124, v126, v124
	v_mul_f32_e32 v125, v127, v125
	s_nop 0
	v_mul_f32_e32 v126, v114, v124
	v_mul_f32_e32 v127, v115, v125
	v_fma_f32 v124, -v114, v124, v114
	v_fma_f32 v125, -v115, v125, v115
	s_nop 0
	v_cndmask_b32_e32 v114, v124, v126, vcc
	v_cmp_gt_f32_e32 vcc, 0, v115
	s_nop 1
	v_cndmask_b32_e32 v115, v125, v127, vcc
; __device__ __forceinline__ unsigned cvt_pk_bf16(float lo, float hi) { unsigned r; asm volatile("v_cvt_pk_bf16_f32 %0, %1, %2" : "=v"(r) : "v"(lo), "v"(hi)); return r; }
; __device__ __forceinline__ f32x2 gelu_pk(f32x2 v) {
;     const f32x2 av = __builtin_elementwise_abs(v), d = av * 0.2316418882f + 1.0f;
;     f32x2 t; t.x = __builtin_amdgcn_rcpf(d.x); t.y = __builtin_amdgcn_rcpf(d.y);
;     f32x2 q = t * 0.5307027145f + (-0.7265760135f); q = q * t + 0.7107068705f; q = q * t + (-0.142248368f); q = q * t + 0.127414796f; q = q * t;
;     const f32x2 s = (v * v) * (-0.72134752044f);
;     f32x2 e; e.x = __builtin_amdgcn_exp2f(s.x); e.y = __builtin_amdgcn_exp2f(s.y);
;     const f32x2 m = v * (q * e), r = v - m;
;     f32x2 o; o.x = v.x < 0.f ? m.x : r.x; o.y = v.y < 0.f ? m.y : r.y; return o;
;     __device__ __forceinline__ void operator()(const f32x4 (&acc)[2][2][4][2], const Unit& u, int wr, int wc, int fr, int fq) const {
;     ...
;                 for (int bj = 0; bj < 2; ++bj) { const i32x4 a0 = __builtin_bit_cast(i32x4, acc[ai][bj][m][0]), a1 = __builtin_bit_cast(i32x4, acc[ai][bj][m][1]);
;                     f32x4 v0 = (f32x4){(float)a0[0], (float)a0[1], (float)a0[2], (float)a0[3]} * rsc * cv[bj][0], v1 = (f32x4){(float)a1[0], (float)a1[1], (float)a1[2], (float)a1[3]} * rsc * cv[bj][1];
;                     if (act) { f32x2 a = gelu_pk((f32x2){v0[0], v0[1]}), b = gelu_pk((f32x2){v0[2], v0[3]}), c = gelu_pk((f32x2){v1[0], v1[1]}), d = gelu_pk((f32x2){v1[2], v1[3]});
;                         v0 = (f32x4){a.x, a.y, b.x, b.y}; v1 = (f32x4){c.x, c.y, d.x, d.y}; }
;                     u32x4 w; w.x = cvt_pk_bf16(v0[0], v0[1]); w.y = cvt_pk_bf16(v0[2], v0[3]); w.z = cvt_pk_bf16(v1[0], v1[1]); w.w = cvt_pk_bf16(v1[2], v1[3]);
;                     if (nt) __builtin_nontemporal_store(w, (u32x4*)(rowp + bj * HALF)); else *(u32x4*)(rowp + bj * HALF) = w; } }
.LBB0_345:
	v_cvt_f32_i32_e32 v113, v113
	v_cvt_f32_i32_e32 v112, v112
	v_cvt_pk_bf16_f32 v118, v118, v119
	v_cvt_pk_bf16_f32 v119, v116, v117
	v_cvt_pk_bf16_f32 v120, v120, v121
	v_cvt_f32_i32_e32 v111, v111
	v_cvt_f32_i32_e32 v110, v110
	v_cvt_pk_bf16_f32 v121, v114, v115
	v_cvt_f32_i32_e32 v115, v109
	v_cvt_f32_i32_e32 v107, v107
	v_cvt_f32_i32_e32 v106, v106
	v_cvt_f32_i32_e32 v114, v108
	v_mul_f32_e32 v112, v184, v112
	v_mul_f32_e32 v113, v184, v113
	v_mul_f32_e32 v110, v184, v110
	v_mul_f32_e32 v111, v184, v111
	v_mul_f32_e32 v108, v40, v112
	v_mul_f32_e32 v109, v41, v113
	v_mul_f32_e32 v106, v184, v106
	v_mul_f32_e32 v107, v184, v107
	v_mul_f32_e32 v112, v184, v114
	v_mul_f32_e32 v113, v184, v115
	v_mul_f32_e32 v110, v38, v110
	v_mul_f32_e32 v111, v39, v111
	v_mul_f32_e32 v112, v36, v112
	v_mul_f32_e32 v113, v37, v113
	s_and_b64 vcc, exec, s[4:5]
	v_mul_f32_e32 v114, v34, v106
	v_mul_f32_e32 v115, v35, v107
	global_store_dwordx4 v[122:123], v[118:121], off offset:256
	s_cbranch_vccnz .LBB0_347
	v_and_b32_e32 v107, 0x7fffffff, v111
	v_and_b32_e32 v106, 0x7fffffff, v110
	v_fma_f32 v106, v106, s16, 1.0
	v_fma_f32 v107, v107, s16, 1.0
	v_mov_b64_e32 v[116:117], s[20:21]
	v_rcp_f32_e32 v106, v106
	v_rcp_f32_e32 v107, v107
	v_mul_f32_e32 v120, v110, v110
	v_mul_f32_e32 v121, v111, v111
	v_cmp_gt_f32_e32 vcc, 0, v110
	v_mul_f32_e32 v120, s28, v120
	v_mul_f32_e32 v121, s28, v121
	v_fma_f32 v118, v106, s18, v116
	v_fma_f32 v119, v107, s18, v116
	v_exp_f32_e32 v120, v120
	v_fma_f32 v118, v106, v118, s22
	v_fma_f32 v119, v107, v119, s22
	v_exp_f32_e32 v121, v121
	v_fma_f32 v118, v106, v118, s24
	v_fma_f32 v119, v107, v119, s24
	s_nop 0
	v_fma_f32 v118, v106, v118, s26
	v_fma_f32 v119, v107, v119, s26
	s_nop 0
	v_mul_f32_e32 v106, v106, v118
	v_mul_f32_e32 v107, v107, v119
	v_mul_f32_e32 v118, v108, v108
	v_mul_f32_e32 v119, v109, v109
	v_mul_f32_e32 v106, v120, v106
	v_mul_f32_e32 v107, v121, v107
	v_mul_f32_e32 v118, s28, v118
	v_mul_f32_e32 v119, s28, v119
	v_mul_f32_e32 v120, v110, v106
	v_mul_f32_e32 v121, v111, v107
	v_fma_f32 v106, -v110, v106, v110
	v_fma_f32 v107, -v111, v107, v111
	v_exp_f32_e32 v118, v118
	v_cndmask_b32_e32 v110, v106, v120, vcc
	v_cmp_gt_f32_e32 vcc, 0, v111
	v_and_b32_e32 v106, 0x7fffffff, v108
	v_exp_f32_e32 v119, v119
	v_cndmask_b32_e32 v111, v107, v121, vcc
	v_and_b32_e32 v107, 0x7fffffff, v109
	v_fma_f32 v106, v106, s16, 1.0
	v_fma_f32 v107, v107, s16, 1.0
	v_cmp_gt_f32_e32 vcc, 0, v108
	v_rcp_f32_e32 v106, v106
	v_rcp_f32_e32 v107, v107
	s_nop 0
	v_fma_f32 v120, v106, s18, v116
	v_fma_f32 v121, v107, s18, v116
	s_nop 0
	v_fma_f32 v120, v106, v120, s22
	v_fma_f32 v121, v107, v121, s22
	s_nop 0
	v_fma_f32 v120, v106, v120, s24
	v_fma_f32 v121, v107, v121, s24
	s_nop 0
	v_fma_f32 v120, v106, v120, s26
	v_fma_f32 v121, v107, v121, s26
	s_nop 0
	v_mul_f32_e32 v106, v106, v120
	v_mul_f32_e32 v107, v107, v121
	v_mul_f32_e32 v120, v114, v114
	v_mul_f32_e32 v121, v115, v115
	v_mul_f32_e32 v106, v118, v106
	v_mul_f32_e32 v107, v119, v107
	v_mul_f32_e32 v120, s28, v120
	v_mul_f32_e32 v121, s28, v121
	v_mul_f32_e32 v118, v108, v106
	v_mul_f32_e32 v119, v109, v107
	v_fma_f32 v106, -v108, v106, v108
	v_fma_f32 v107, -v109, v107, v109
	v_exp_f32_e32 v120, v120
	v_cndmask_b32_e32 v108, v106, v118, vcc
	v_cmp_gt_f32_e32 vcc, 0, v109
	v_and_b32_e32 v106, 0x7fffffff, v114
	v_exp_f32_e32 v121, v121
	v_cndmask_b32_e32 v109, v107, v119, vcc
	v_and_b32_e32 v107, 0x7fffffff, v115
	v_fma_f32 v106, v106, s16, 1.0
	v_fma_f32 v107, v107, s16, 1.0
	v_cmp_gt_f32_e32 vcc, 0, v114
	v_rcp_f32_e32 v106, v106
	v_rcp_f32_e32 v107, v107
	s_nop 0
	v_fma_f32 v118, v106, s18, v116
	v_fma_f32 v119, v107, s18, v116
	s_nop 0
	v_fma_f32 v118, v106, v118, s22
	v_fma_f32 v119, v107, v119, s22
	s_nop 0
	v_fma_f32 v118, v106, v118, s24
	v_fma_f32 v119, v107, v119, s24
	s_nop 0
	v_fma_f32 v118, v106, v118, s26
	v_fma_f32 v119, v107, v119, s26
	s_nop 0
	v_mul_f32_e32 v106, v106, v118
	v_mul_f32_e32 v107, v107, v119
	v_mul_f32_e32 v118, v112, v112
	v_mul_f32_e32 v119, v113, v113
	v_mul_f32_e32 v106, v120, v106
	v_mul_f32_e32 v107, v121, v107
	s_nop 0
	v_mul_f32_e32 v120, v114, v106
	v_mul_f32_e32 v121, v115, v107
	v_fma_f32 v106, -v114, v106, v114
	v_fma_f32 v107, -v115, v107, v115
	s_nop 0
	v_cndmask_b32_e32 v114, v106, v120, vcc
	v_cmp_gt_f32_e32 vcc, 0, v115
	v_and_b32_e32 v106, 0x7fffffff, v112
	s_nop 0
	v_cndmask_b32_e32 v115, v107, v121, vcc
	v_and_b32_e32 v107, 0x7fffffff, v113
	v_fma_f32 v106, v106, s16, 1.0
	v_fma_f32 v107, v107, s16, 1.0
	v_cmp_gt_f32_e32 vcc, 0, v112
	v_rcp_f32_e32 v106, v106
	v_rcp_f32_e32 v107, v107
	s_nop 0
	v_fma_f32 v117, v107, s18, v116
	v_fma_f32 v116, v106, s18, v116
	s_nop 0
	v_fma_f32 v116, v106, v116, s22
	v_fma_f32 v117, v107, v117, s22
	s_nop 0
	v_fma_f32 v116, v106, v116, s24
	v_fma_f32 v117, v107, v117, s24
	s_nop 0
	v_fma_f32 v116, v106, v116, s26
	v_fma_f32 v117, v107, v117, s26
	s_nop 0
	v_mul_f32_e32 v106, v106, v116
	v_mul_f32_e32 v107, v107, v117
	v_mul_f32_e32 v116, s28, v118
	v_mul_f32_e32 v117, s28, v119
	s_nop 0
	v_exp_f32_e32 v116, v116
	v_exp_f32_e32 v117, v117
	s_nop 0
	v_mul_f32_e32 v106, v116, v106
	v_mul_f32_e32 v107, v117, v107
	s_nop 0
	v_mul_f32_e32 v116, v112, v106
	v_mul_f32_e32 v117, v113, v107
	v_fma_f32 v106, -v112, v106, v112
	v_fma_f32 v107, -v113, v107, v113
	s_nop 0
	v_cndmask_b32_e32 v112, v106, v116, vcc
	v_cmp_gt_f32_e32 vcc, 0, v113
	s_nop 1
	v_cndmask_b32_e32 v113, v107, v117, vcc
; __device__ __forceinline__ unsigned cvt_pk_bf16(float lo, float hi) { unsigned r; asm volatile("v_cvt_pk_bf16_f32 %0, %1, %2" : "=v"(r) : "v"(lo), "v"(hi)); return r; }
; __device__ __forceinline__ f32x2 gelu_pk(f32x2 v) {
;     const f32x2 av = __builtin_elementwise_abs(v), d = av * 0.2316418882f + 1.0f;
;     f32x2 t; t.x = __builtin_amdgcn_rcpf(d.x); t.y = __builtin_amdgcn_rcpf(d.y);
;     f32x2 q = t * 0.5307027145f + (-0.7265760135f); q = q * t + 0.7107068705f; q = q * t + (-0.142248368f); q = q * t + 0.127414796f; q = q * t;
;     const f32x2 s = (v * v) * (-0.72134752044f);
;     f32x2 e; e.x = __builtin_amdgcn_exp2f(s.x); e.y = __builtin_amdgcn_exp2f(s.y);
;     const f32x2 m = v * (q * e), r = v - m;
;     f32x2 o; o.x = v.x < 0.f ? m.x : r.x; o.y = v.y < 0.f ? m.y : r.y; return o;
;     __device__ __forceinline__ void operator()(const f32x4 (&acc)[2][2][4][2], const Unit& u, int wr, int wc, int fr, int fq) const {
;     ...
;                 for (int bj = 0; bj < 2; ++bj) { const i32x4 a0 = __builtin_bit_cast(i32x4, acc[ai][bj][m][0]), a1 = __builtin_bit_cast(i32x4, acc[ai][bj][m][1]);
;                     f32x4 v0 = (f32x4){(float)a0[0], (float)a0[1], (float)a0[2], (float)a0[3]} * rsc * cv[bj][0], v1 = (f32x4){(float)a1[0], (float)a1[1], (float)a1[2], (float)a1[3]} * rsc * cv[bj][1];
;                     if (act) { f32x2 a = gelu_pk((f32x2){v0[0], v0[1]}), b = gelu_pk((f32x2){v0[2], v0[3]}), c = gelu_pk((f32x2){v1[0], v1[1]}), d = gelu_pk((f32x2){v1[2], v1[3]});
;                         v0 = (f32x4){a.x, a.y, b.x, b.y}; v1 = (f32x4){c.x, c.y, d.x, d.y}; }
;                     u32x4 w; w.x = cvt_pk_bf16(v0[0], v0[1]); w.y = cvt_pk_bf16(v0[2], v0[3]); w.z = cvt_pk_bf16(v1[0], v1[1]); w.w = cvt_pk_bf16(v1[2], v1[3]);
;                     if (nt) __builtin_nontemporal_store(w, (u32x4*)(rowp + bj * HALF)); else *(u32x4*)(rowp + bj * HALF) = w; } }
.LBB0_347:
	v_cvt_f32_i32_e32 v105, v105
	v_cvt_f32_i32_e32 v104, v104
	v_cvt_pk_bf16_f32 v116, v110, v111
	v_cvt_f32_i32_e32 v103, v103
	v_cvt_f32_i32_e32 v102, v102
	v_cvt_f32_i32_e32 v99, v99
	v_cvt_f32_i32_e32 v111, v101
	v_cvt_f32_i32_e32 v110, v100
	v_cvt_f32_i32_e32 v98, v98
	v_cvt_pk_bf16_f32 v117, v108, v109
	v_mov_b32_e32 v108, v184
	v_mov_b32_e32 v109, v184
	v_mov_b32_e32 v185, v184
	v_lshlrev_b64 v[106:107], 15, v[186:187]
	v_mul_f32_e32 v104, v108, v104
	v_mul_f32_e32 v105, v109, v105
	v_lshl_add_u64 v[106:107], s[70:71], 0, v[106:107]
	v_mul_f32_e32 v102, v184, v102
	v_mul_f32_e32 v103, v185, v103
	v_mul_f32_e32 v100, v28, v104
	v_mul_f32_e32 v101, v29, v105
	v_mul_f32_e32 v104, v108, v110
	v_mul_f32_e32 v105, v109, v111
	v_mul_f32_e32 v108, v184, v98
	v_mul_f32_e32 v109, v185, v99
	v_lshl_add_u64 v[106:107], v[170:171], 1, v[106:107]
	v_mul_f32_e32 v102, v26, v102
	v_mul_f32_e32 v103, v27, v103
	v_mul_f32_e32 v98, v24, v104
	v_mul_f32_e32 v99, v25, v105
	s_and_b64 vcc, exec, s[4:5]
	v_mul_f32_e32 v104, v22, v108
	v_mul_f32_e32 v105, v23, v109
	v_cvt_pk_bf16_f32 v118, v114, v115
	v_cvt_pk_bf16_f32 v119, v112, v113
	global_store_dwordx4 v[106:107], v[116:119], off
	s_cbranch_vccnz .LBB0_349
	v_and_b32_e32 v109, 0x7fffffff, v103
	v_and_b32_e32 v108, 0x7fffffff, v102
	v_fma_f32 v108, v108, s16, 1.0
	v_fma_f32 v109, v109, s16, 1.0
	v_mov_b64_e32 v[110:111], s[20:21]
	v_rcp_f32_e32 v108, v108
	v_rcp_f32_e32 v109, v109
	v_mul_f32_e32 v114, v102, v102
	v_mul_f32_e32 v115, v103, v103
	v_cmp_gt_f32_e32 vcc, 0, v102
	v_mul_f32_e32 v114, s28, v114
	v_mul_f32_e32 v115, s28, v115
	v_fma_f32 v112, v108, s18, v110
	v_fma_f32 v113, v109, s18, v110
	v_exp_f32_e32 v114, v114
	v_fma_f32 v112, v108, v112, s22
	v_fma_f32 v113, v109, v113, s22
	v_exp_f32_e32 v115, v115
	v_fma_f32 v112, v108, v112, s24
	v_fma_f32 v113, v109, v113, s24
	s_nop 0
	v_fma_f32 v112, v108, v112, s26
	v_fma_f32 v113, v109, v113, s26
	s_nop 0
	v_mul_f32_e32 v108, v108, v112
	v_mul_f32_e32 v109, v109, v113
	v_mul_f32_e32 v112, v100, v100
	v_mul_f32_e32 v113, v101, v101
	v_mul_f32_e32 v108, v114, v108
	v_mul_f32_e32 v109, v115, v109
	v_mul_f32_e32 v112, s28, v112
	v_mul_f32_e32 v113, s28, v113
	v_mul_f32_e32 v114, v102, v108
	v_mul_f32_e32 v115, v103, v109
	v_fma_f32 v108, -v102, v108, v102
	v_fma_f32 v109, -v103, v109, v103
	v_exp_f32_e32 v112, v112
	v_cndmask_b32_e32 v102, v108, v114, vcc
	v_cmp_gt_f32_e32 vcc, 0, v103
	v_and_b32_e32 v108, 0x7fffffff, v100
	v_exp_f32_e32 v113, v113
	v_cndmask_b32_e32 v103, v109, v115, vcc
	v_and_b32_e32 v109, 0x7fffffff, v101
	v_fma_f32 v108, v108, s16, 1.0
	v_fma_f32 v109, v109, s16, 1.0
	v_cmp_gt_f32_e32 vcc, 0, v100
	v_rcp_f32_e32 v108, v108
	v_rcp_f32_e32 v109, v109
	s_nop 0
	v_fma_f32 v114, v108, s18, v110
	v_fma_f32 v115, v109, s18, v110
	s_nop 0
	v_fma_f32 v114, v108, v114, s22
	v_fma_f32 v115, v109, v115, s22
	s_nop 0
	v_fma_f32 v114, v108, v114, s24
	v_fma_f32 v115, v109, v115, s24
	s_nop 0
	v_fma_f32 v114, v108, v114, s26
	v_fma_f32 v115, v109, v115, s26
	s_nop 0
	v_mul_f32_e32 v108, v108, v114
	v_mul_f32_e32 v109, v109, v115
	v_mul_f32_e32 v114, v104, v104
	v_mul_f32_e32 v115, v105, v105
	v_mul_f32_e32 v108, v112, v108
	v_mul_f32_e32 v109, v113, v109
	v_mul_f32_e32 v114, s28, v114
	v_mul_f32_e32 v115, s28, v115
	v_mul_f32_e32 v112, v100, v108
	v_mul_f32_e32 v113, v101, v109
	v_fma_f32 v108, -v100, v108, v100
	v_fma_f32 v109, -v101, v109, v101
	v_exp_f32_e32 v114, v114
	v_cndmask_b32_e32 v100, v108, v112, vcc
	v_cmp_gt_f32_e32 vcc, 0, v101
	v_and_b32_e32 v108, 0x7fffffff, v104
	v_exp_f32_e32 v115, v115
	v_cndmask_b32_e32 v101, v109, v113, vcc
	v_and_b32_e32 v109, 0x7fffffff, v105
	v_fma_f32 v108, v108, s16, 1.0
	v_fma_f32 v109, v109, s16, 1.0
	v_cmp_gt_f32_e32 vcc, 0, v104
	v_rcp_f32_e32 v108, v108
	v_rcp_f32_e32 v109, v109
	s_nop 0
	v_fma_f32 v112, v108, s18, v110
	v_fma_f32 v113, v109, s18, v110
	s_nop 0
	v_fma_f32 v112, v108, v112, s22
	v_fma_f32 v113, v109, v113, s22
	s_nop 0
	v_fma_f32 v112, v108, v112, s24
	v_fma_f32 v113, v109, v113, s24
	s_nop 0
	v_fma_f32 v112, v108, v112, s26
	v_fma_f32 v113, v109, v113, s26
	s_nop 0
	v_mul_f32_e32 v108, v108, v112
	v_mul_f32_e32 v109, v109, v113
	v_mul_f32_e32 v112, v98, v98
	v_mul_f32_e32 v113, v99, v99
	v_mul_f32_e32 v108, v114, v108
	v_mul_f32_e32 v109, v115, v109
	s_nop 0
	v_mul_f32_e32 v114, v104, v108
	v_mul_f32_e32 v115, v105, v109
	v_fma_f32 v108, -v104, v108, v104
	v_fma_f32 v109, -v105, v109, v105
	s_nop 0
	v_cndmask_b32_e32 v104, v108, v114, vcc
	v_cmp_gt_f32_e32 vcc, 0, v105
	v_and_b32_e32 v108, 0x7fffffff, v98
	s_nop 0
	v_cndmask_b32_e32 v105, v109, v115, vcc
	v_and_b32_e32 v109, 0x7fffffff, v99
	v_fma_f32 v108, v108, s16, 1.0
	v_fma_f32 v109, v109, s16, 1.0
	v_cmp_gt_f32_e32 vcc, 0, v98
	v_rcp_f32_e32 v108, v108
	v_rcp_f32_e32 v109, v109
	s_nop 0
	v_fma_f32 v111, v109, s18, v110
	v_fma_f32 v110, v108, s18, v110
	s_nop 0
	v_fma_f32 v110, v108, v110, s22
	v_fma_f32 v111, v109, v111, s22
	s_nop 0
	v_fma_f32 v110, v108, v110, s24
	v_fma_f32 v111, v109, v111, s24
	s_nop 0
	v_fma_f32 v110, v108, v110, s26
	v_fma_f32 v111, v109, v111, s26
	s_nop 0
	v_mul_f32_e32 v108, v108, v110
	v_mul_f32_e32 v109, v109, v111
	v_mul_f32_e32 v110, s28, v112
	v_mul_f32_e32 v111, s28, v113
	s_nop 0
	v_exp_f32_e32 v110, v110
	v_exp_f32_e32 v111, v111
	s_nop 0
	v_mul_f32_e32 v108, v110, v108
	v_mul_f32_e32 v109, v111, v109
	s_nop 0
	v_mul_f32_e32 v110, v98, v108
	v_mul_f32_e32 v111, v99, v109
	v_fma_f32 v108, -v98, v108, v98
	v_fma_f32 v109, -v99, v109, v99
	s_nop 0
	v_cndmask_b32_e32 v98, v108, v110, vcc
	v_cmp_gt_f32_e32 vcc, 0, v99
	s_nop 1
	v_cndmask_b32_e32 v99, v109, v111, vcc
; __device__ __forceinline__ unsigned cvt_pk_bf16(float lo, float hi) { unsigned r; asm volatile("v_cvt_pk_bf16_f32 %0, %1, %2" : "=v"(r) : "v"(lo), "v"(hi)); return r; }
; __device__ __forceinline__ f32x2 gelu_pk(f32x2 v) {
;     const f32x2 av = __builtin_elementwise_abs(v), d = av * 0.2316418882f + 1.0f;
;     f32x2 t; t.x = __builtin_amdgcn_rcpf(d.x); t.y = __builtin_amdgcn_rcpf(d.y);
;     f32x2 q = t * 0.5307027145f + (-0.7265760135f); q = q * t + 0.7107068705f; q = q * t + (-0.142248368f); q = q * t + 0.127414796f; q = q * t;
;     const f32x2 s = (v * v) * (-0.72134752044f);
;     f32x2 e; e.x = __builtin_amdgcn_exp2f(s.x); e.y = __builtin_amdgcn_exp2f(s.y);
;     const f32x2 m = v * (q * e), r = v - m;
;     f32x2 o; o.x = v.x < 0.f ? m.x : r.x; o.y = v.y < 0.f ? m.y : r.y; return o;
;     __device__ __forceinline__ void operator()(const f32x4 (&acc)[2][2][4][2], const Unit& u, int wr, int wc, int fr, int fq) const {
;     ...
;                 for (int bj = 0; bj < 2; ++bj) { const i32x4 a0 = __builtin_bit_cast(i32x4, acc[ai][bj][m][0]), a1 = __builtin_bit_cast(i32x4, acc[ai][bj][m][1]);
;                     f32x4 v0 = (f32x4){(float)a0[0], (float)a0[1], (float)a0[2], (float)a0[3]} * rsc * cv[bj][0], v1 = (f32x4){(float)a1[0], (float)a1[1], (float)a1[2], (float)a1[3]} * rsc * cv[bj][1];
;                     if (act) { f32x2 a = gelu_pk((f32x2){v0[0], v0[1]}), b = gelu_pk((f32x2){v0[2], v0[3]}), c = gelu_pk((f32x2){v1[0], v1[1]}), d = gelu_pk((f32x2){v1[2], v1[3]});
;                         v0 = (f32x4){a.x, a.y, b.x, b.y}; v1 = (f32x4){c.x, c.y, d.x, d.y}; }
;                     u32x4 w; w.x = cvt_pk_bf16(v0[0], v0[1]); w.y = cvt_pk_bf16(v0[2], v0[3]); w.z = cvt_pk_bf16(v1[0], v1[1]); w.w = cvt_pk_bf16(v1[2], v1[3]);
;                     if (nt) __builtin_nontemporal_store(w, (u32x4*)(rowp + bj * HALF)); else *(u32x4*)(rowp + bj * HALF) = w; } }
.LBB0_349:
	v_cvt_f32_i32_e32 v97, v97
	v_cvt_f32_i32_e32 v96, v96
	v_cvt_pk_bf16_f32 v102, v102, v103
	v_cvt_pk_bf16_f32 v103, v100, v101
	v_cvt_pk_bf16_f32 v104, v104, v105
	v_cvt_f32_i32_e32 v95, v95
	v_cvt_f32_i32_e32 v94, v94
	v_cvt_pk_bf16_f32 v105, v98, v99
	v_cvt_f32_i32_e32 v99, v93
	v_cvt_f32_i32_e32 v91, v91
	v_cvt_f32_i32_e32 v90, v90
	v_cvt_f32_i32_e32 v98, v92
	v_mul_f32_e32 v96, v180, v96
	v_mul_f32_e32 v97, v180, v97
	v_mul_f32_e32 v94, v180, v94
	v_mul_f32_e32 v95, v180, v95
	v_mul_f32_e32 v92, v40, v96
	v_mul_f32_e32 v93, v41, v97
	v_mul_f32_e32 v90, v180, v90
	v_mul_f32_e32 v91, v180, v91
	v_mul_f32_e32 v96, v180, v98
	v_mul_f32_e32 v97, v180, v99
	v_mul_f32_e32 v94, v38, v94
	v_mul_f32_e32 v95, v39, v95
	v_mul_f32_e32 v96, v36, v96
	v_mul_f32_e32 v97, v37, v97
	s_and_b64 vcc, exec, s[4:5]
	v_mul_f32_e32 v98, v34, v90
	v_mul_f32_e32 v99, v35, v91
	global_store_dwordx4 v[106:107], v[102:105], off offset:256
	s_cbranch_vccnz .LBB0_351
	v_and_b32_e32 v91, 0x7fffffff, v95
	v_and_b32_e32 v90, 0x7fffffff, v94
	v_fma_f32 v90, v90, s16, 1.0
	v_fma_f32 v91, v91, s16, 1.0
	v_mov_b64_e32 v[100:101], s[20:21]
	v_rcp_f32_e32 v90, v90
	v_rcp_f32_e32 v91, v91
	v_mul_f32_e32 v104, v94, v94
	v_mul_f32_e32 v105, v95, v95
	v_cmp_gt_f32_e32 vcc, 0, v94
	v_mul_f32_e32 v104, s28, v104
	v_mul_f32_e32 v105, s28, v105
	v_fma_f32 v102, v90, s18, v100
	v_fma_f32 v103, v91, s18, v100
	v_exp_f32_e32 v104, v104
	v_fma_f32 v102, v90, v102, s22
	v_fma_f32 v103, v91, v103, s22
	v_exp_f32_e32 v105, v105
	v_fma_f32 v102, v90, v102, s24
	v_fma_f32 v103, v91, v103, s24
	s_nop 0
	v_fma_f32 v102, v90, v102, s26
	v_fma_f32 v103, v91, v103, s26
	s_nop 0
	v_mul_f32_e32 v90, v90, v102
	v_mul_f32_e32 v91, v91, v103
	v_mul_f32_e32 v102, v92, v92
	v_mul_f32_e32 v103, v93, v93
	v_mul_f32_e32 v90, v104, v90
	v_mul_f32_e32 v91, v105, v91
	v_mul_f32_e32 v102, s28, v102
	v_mul_f32_e32 v103, s28, v103
	v_mul_f32_e32 v104, v94, v90
	v_mul_f32_e32 v105, v95, v91
	v_fma_f32 v90, -v94, v90, v94
	v_fma_f32 v91, -v95, v91, v95
	v_exp_f32_e32 v102, v102
	v_cndmask_b32_e32 v94, v90, v104, vcc
	v_cmp_gt_f32_e32 vcc, 0, v95
	v_and_b32_e32 v90, 0x7fffffff, v92
	v_exp_f32_e32 v103, v103
	v_cndmask_b32_e32 v95, v91, v105, vcc
	v_and_b32_e32 v91, 0x7fffffff, v93
	v_fma_f32 v90, v90, s16, 1.0
	v_fma_f32 v91, v91, s16, 1.0
	v_cmp_gt_f32_e32 vcc, 0, v92
	v_rcp_f32_e32 v90, v90
	v_rcp_f32_e32 v91, v91
	s_nop 0
	v_fma_f32 v104, v90, s18, v100
	v_fma_f32 v105, v91, s18, v100
	s_nop 0
	v_fma_f32 v104, v90, v104, s22
	v_fma_f32 v105, v91, v105, s22
	s_nop 0
	v_fma_f32 v104, v90, v104, s24
	v_fma_f32 v105, v91, v105, s24
	s_nop 0
	v_fma_f32 v104, v90, v104, s26
	v_fma_f32 v105, v91, v105, s26
	s_nop 0
	v_mul_f32_e32 v90, v90, v104
	v_mul_f32_e32 v91, v91, v105
	v_mul_f32_e32 v104, v98, v98
	v_mul_f32_e32 v105, v99, v99
	v_mul_f32_e32 v90, v102, v90
	v_mul_f32_e32 v91, v103, v91
	v_mul_f32_e32 v104, s28, v104
	v_mul_f32_e32 v105, s28, v105
	v_mul_f32_e32 v102, v92, v90
	v_mul_f32_e32 v103, v93, v91
	v_fma_f32 v90, -v92, v90, v92
	v_fma_f32 v91, -v93, v91, v93
	v_exp_f32_e32 v104, v104
	v_cndmask_b32_e32 v92, v90, v102, vcc
	v_cmp_gt_f32_e32 vcc, 0, v93
	v_and_b32_e32 v90, 0x7fffffff, v98
	v_exp_f32_e32 v105, v105
	v_cndmask_b32_e32 v93, v91, v103, vcc
	v_and_b32_e32 v91, 0x7fffffff, v99
	v_fma_f32 v90, v90, s16, 1.0
	v_fma_f32 v91, v91, s16, 1.0
	v_cmp_gt_f32_e32 vcc, 0, v98
	v_rcp_f32_e32 v90, v90
	v_rcp_f32_e32 v91, v91
	s_nop 0
	v_fma_f32 v102, v90, s18, v100
	v_fma_f32 v103, v91, s18, v100
	s_nop 0
	v_fma_f32 v102, v90, v102, s22
	v_fma_f32 v103, v91, v103, s22
	s_nop 0
	v_fma_f32 v102, v90, v102, s24
	v_fma_f32 v103, v91, v103, s24
	s_nop 0
	v_fma_f32 v102, v90, v102, s26
	v_fma_f32 v103, v91, v103, s26
	s_nop 0
	v_mul_f32_e32 v90, v90, v102
	v_mul_f32_e32 v91, v91, v103
	v_mul_f32_e32 v102, v96, v96
	v_mul_f32_e32 v103, v97, v97
	v_mul_f32_e32 v90, v104, v90
	v_mul_f32_e32 v91, v105, v91
	s_nop 0
	v_mul_f32_e32 v104, v98, v90
	v_mul_f32_e32 v105, v99, v91
	v_fma_f32 v90, -v98, v90, v98
	v_fma_f32 v91, -v99, v91, v99
	s_nop 0
	v_cndmask_b32_e32 v98, v90, v104, vcc
	v_cmp_gt_f32_e32 vcc, 0, v99
	v_and_b32_e32 v90, 0x7fffffff, v96
	s_nop 0
	v_cndmask_b32_e32 v99, v91, v105, vcc
	v_and_b32_e32 v91, 0x7fffffff, v97
	v_fma_f32 v90, v90, s16, 1.0
	v_fma_f32 v91, v91, s16, 1.0
	v_cmp_gt_f32_e32 vcc, 0, v96
	v_rcp_f32_e32 v90, v90
	v_rcp_f32_e32 v91, v91
	s_nop 0
	v_fma_f32 v101, v91, s18, v100
	v_fma_f32 v100, v90, s18, v100
	s_nop 0
	v_fma_f32 v100, v90, v100, s22
	v_fma_f32 v101, v91, v101, s22
	s_nop 0
	v_fma_f32 v100, v90, v100, s24
	v_fma_f32 v101, v91, v101, s24
	s_nop 0
	v_fma_f32 v100, v90, v100, s26
	v_fma_f32 v101, v91, v101, s26
	s_nop 0
	v_mul_f32_e32 v90, v90, v100
	v_mul_f32_e32 v91, v91, v101
	v_mul_f32_e32 v100, s28, v102
	v_mul_f32_e32 v101, s28, v103
	s_nop 0
	v_exp_f32_e32 v100, v100
	v_exp_f32_e32 v101, v101
	s_nop 0
	v_mul_f32_e32 v90, v100, v90
	v_mul_f32_e32 v91, v101, v91
	s_nop 0
	v_mul_f32_e32 v100, v96, v90
	v_mul_f32_e32 v101, v97, v91
	v_fma_f32 v90, -v96, v90, v96
	v_fma_f32 v91, -v97, v91, v97
	s_nop 0
	v_cndmask_b32_e32 v96, v90, v100, vcc
	v_cmp_gt_f32_e32 vcc, 0, v97
	s_nop 1
	v_cndmask_b32_e32 v97, v91, v101, vcc
; __device__ __forceinline__ unsigned cvt_pk_bf16(float lo, float hi) { unsigned r; asm volatile("v_cvt_pk_bf16_f32 %0, %1, %2" : "=v"(r) : "v"(lo), "v"(hi)); return r; }
; __device__ __forceinline__ f32x2 gelu_pk(f32x2 v) {
;     const f32x2 av = __builtin_elementwise_abs(v), d = av * 0.2316418882f + 1.0f;
;     f32x2 t; t.x = __builtin_amdgcn_rcpf(d.x); t.y = __builtin_amdgcn_rcpf(d.y);
;     f32x2 q = t * 0.5307027145f + (-0.7265760135f); q = q * t + 0.7107068705f; q = q * t + (-0.142248368f); q = q * t + 0.127414796f; q = q * t;
;     const f32x2 s = (v * v) * (-0.72134752044f);
;     f32x2 e; e.x = __builtin_amdgcn_exp2f(s.x); e.y = __builtin_amdgcn_exp2f(s.y);
;     const f32x2 m = v * (q * e), r = v - m;
;     f32x2 o; o.x = v.x < 0.f ? m.x : r.x; o.y = v.y < 0.f ? m.y : r.y; return o;
;     __device__ __forceinline__ void operator()(const f32x4 (&acc)[2][2][4][2], const Unit& u, int wr, int wc, int fr, int fq) const {
;     ...
;                 for (int bj = 0; bj < 2; ++bj) { const i32x4 a0 = __builtin_bit_cast(i32x4, acc[ai][bj][m][0]), a1 = __builtin_bit_cast(i32x4, acc[ai][bj][m][1]);
;                     f32x4 v0 = (f32x4){(float)a0[0], (float)a0[1], (float)a0[2], (float)a0[3]} * rsc * cv[bj][0], v1 = (f32x4){(float)a1[0], (float)a1[1], (float)a1[2], (float)a1[3]} * rsc * cv[bj][1];
;                     if (act) { f32x2 a = gelu_pk((f32x2){v0[0], v0[1]}), b = gelu_pk((f32x2){v0[2], v0[3]}), c = gelu_pk((f32x2){v1[0], v1[1]}), d = gelu_pk((f32x2){v1[2], v1[3]});
;                         v0 = (f32x4){a.x, a.y, b.x, b.y}; v1 = (f32x4){c.x, c.y, d.x, d.y}; }
;                     u32x4 w; w.x = cvt_pk_bf16(v0[0], v0[1]); w.y = cvt_pk_bf16(v0[2], v0[3]); w.z = cvt_pk_bf16(v1[0], v1[1]); w.w = cvt_pk_bf16(v1[2], v1[3]);
;                     if (nt) __builtin_nontemporal_store(w, (u32x4*)(rowp + bj * HALF)); else *(u32x4*)(rowp + bj * HALF) = w; } }
.LBB0_351:
	v_cvt_f32_i32_e32 v89, v89
	v_cvt_f32_i32_e32 v88, v88
	v_cvt_pk_bf16_f32 v100, v94, v95
	v_cvt_f32_i32_e32 v87, v87
	v_cvt_f32_i32_e32 v86, v86
	v_cvt_f32_i32_e32 v83, v83
	v_cvt_f32_i32_e32 v95, v85
	v_cvt_f32_i32_e32 v94, v84
	v_cvt_f32_i32_e32 v82, v82
	v_cvt_pk_bf16_f32 v101, v92, v93
	v_mov_b32_e32 v92, v180
	v_mov_b32_e32 v93, v180
	v_mov_b32_e32 v181, v180
	v_lshlrev_b64 v[90:91], 15, v[182:183]
	v_mul_f32_e32 v88, v92, v88
	v_mul_f32_e32 v89, v93, v89
	v_lshl_add_u64 v[90:91], s[70:71], 0, v[90:91]
	v_mul_f32_e32 v86, v180, v86
	v_mul_f32_e32 v87, v181, v87
	v_mul_f32_e32 v84, v28, v88
	v_mul_f32_e32 v85, v29, v89
	v_mul_f32_e32 v88, v92, v94
	v_mul_f32_e32 v89, v93, v95
	v_mul_f32_e32 v92, v180, v82
	v_mul_f32_e32 v93, v181, v83
	v_lshl_add_u64 v[90:91], v[170:171], 1, v[90:91]
	v_mul_f32_e32 v86, v26, v86
	v_mul_f32_e32 v87, v27, v87
	v_mul_f32_e32 v82, v24, v88
	v_mul_f32_e32 v83, v25, v89
	s_and_b64 vcc, exec, s[4:5]
	v_mul_f32_e32 v88, v22, v92
	v_mul_f32_e32 v89, v23, v93
	v_cvt_pk_bf16_f32 v102, v98, v99
	v_cvt_pk_bf16_f32 v103, v96, v97
	global_store_dwordx4 v[90:91], v[100:103], off
	s_cbranch_vccnz .LBB0_353
	v_and_b32_e32 v93, 0x7fffffff, v87
	v_and_b32_e32 v92, 0x7fffffff, v86
	v_fma_f32 v92, v92, s16, 1.0
	v_fma_f32 v93, v93, s16, 1.0
	v_mov_b64_e32 v[94:95], s[20:21]
	v_rcp_f32_e32 v92, v92
	v_rcp_f32_e32 v93, v93
	v_mul_f32_e32 v98, v86, v86
	v_mul_f32_e32 v99, v87, v87
	v_cmp_gt_f32_e32 vcc, 0, v86
	v_mul_f32_e32 v98, s28, v98
	v_mul_f32_e32 v99, s28, v99
	v_fma_f32 v96, v92, s18, v94
	v_fma_f32 v97, v93, s18, v94
	v_exp_f32_e32 v98, v98
	v_fma_f32 v96, v92, v96, s22
	v_fma_f32 v97, v93, v97, s22
	v_exp_f32_e32 v99, v99
	v_fma_f32 v96, v92, v96, s24
	v_fma_f32 v97, v93, v97, s24
	s_nop 0
	v_fma_f32 v96, v92, v96, s26
	v_fma_f32 v97, v93, v97, s26
	s_nop 0
	v_mul_f32_e32 v92, v92, v96
	v_mul_f32_e32 v93, v93, v97
	v_mul_f32_e32 v96, v84, v84
	v_mul_f32_e32 v97, v85, v85
	v_mul_f32_e32 v92, v98, v92
	v_mul_f32_e32 v93, v99, v93
	v_mul_f32_e32 v96, s28, v96
	v_mul_f32_e32 v97, s28, v97
	v_mul_f32_e32 v98, v86, v92
	v_mul_f32_e32 v99, v87, v93
	v_fma_f32 v92, -v86, v92, v86
	v_fma_f32 v93, -v87, v93, v87
	v_exp_f32_e32 v96, v96
	v_cndmask_b32_e32 v86, v92, v98, vcc
	v_cmp_gt_f32_e32 vcc, 0, v87
	v_and_b32_e32 v92, 0x7fffffff, v84
	v_exp_f32_e32 v97, v97
	v_cndmask_b32_e32 v87, v93, v99, vcc
	v_and_b32_e32 v93, 0x7fffffff, v85
	v_fma_f32 v92, v92, s16, 1.0
	v_fma_f32 v93, v93, s16, 1.0
	v_cmp_gt_f32_e32 vcc, 0, v84
	v_rcp_f32_e32 v92, v92
	v_rcp_f32_e32 v93, v93
	s_nop 0
	v_fma_f32 v98, v92, s18, v94
	v_fma_f32 v99, v93, s18, v94
	s_nop 0
	v_fma_f32 v98, v92, v98, s22
	v_fma_f32 v99, v93, v99, s22
	s_nop 0
	v_fma_f32 v98, v92, v98, s24
	v_fma_f32 v99, v93, v99, s24
	s_nop 0
	v_fma_f32 v98, v92, v98, s26
	v_fma_f32 v99, v93, v99, s26
	s_nop 0
	v_mul_f32_e32 v92, v92, v98
	v_mul_f32_e32 v93, v93, v99
	v_mul_f32_e32 v98, v88, v88
	v_mul_f32_e32 v99, v89, v89
	v_mul_f32_e32 v92, v96, v92
	v_mul_f32_e32 v93, v97, v93
	v_mul_f32_e32 v98, s28, v98
	v_mul_f32_e32 v99, s28, v99
	v_mul_f32_e32 v96, v84, v92
	v_mul_f32_e32 v97, v85, v93
	v_fma_f32 v92, -v84, v92, v84
	v_fma_f32 v93, -v85, v93, v85
	v_exp_f32_e32 v98, v98
	v_cndmask_b32_e32 v84, v92, v96, vcc
	v_cmp_gt_f32_e32 vcc, 0, v85
	v_and_b32_e32 v92, 0x7fffffff, v88
	v_exp_f32_e32 v99, v99
	v_cndmask_b32_e32 v85, v93, v97, vcc
	v_and_b32_e32 v93, 0x7fffffff, v89
	v_fma_f32 v92, v92, s16, 1.0
	v_fma_f32 v93, v93, s16, 1.0
	v_cmp_gt_f32_e32 vcc, 0, v88
	v_rcp_f32_e32 v92, v92
	v_rcp_f32_e32 v93, v93
	s_nop 0
	v_fma_f32 v96, v92, s18, v94
	v_fma_f32 v97, v93, s18, v94
	s_nop 0
	v_fma_f32 v96, v92, v96, s22
	v_fma_f32 v97, v93, v97, s22
	s_nop 0
	v_fma_f32 v96, v92, v96, s24
	v_fma_f32 v97, v93, v97, s24
	s_nop 0
	v_fma_f32 v96, v92, v96, s26
	v_fma_f32 v97, v93, v97, s26
	s_nop 0
	v_mul_f32_e32 v92, v92, v96
	v_mul_f32_e32 v93, v93, v97
	v_mul_f32_e32 v96, v82, v82
	v_mul_f32_e32 v97, v83, v83
	v_mul_f32_e32 v92, v98, v92
	v_mul_f32_e32 v93, v99, v93
	s_nop 0
	v_mul_f32_e32 v98, v88, v92
	v_mul_f32_e32 v99, v89, v93
	v_fma_f32 v92, -v88, v92, v88
	v_fma_f32 v93, -v89, v93, v89
	s_nop 0
	v_cndmask_b32_e32 v88, v92, v98, vcc
	v_cmp_gt_f32_e32 vcc, 0, v89
	v_and_b32_e32 v92, 0x7fffffff, v82
	s_nop 0
	v_cndmask_b32_e32 v89, v93, v99, vcc
	v_and_b32_e32 v93, 0x7fffffff, v83
	v_fma_f32 v92, v92, s16, 1.0
	v_fma_f32 v93, v93, s16, 1.0
	v_cmp_gt_f32_e32 vcc, 0, v82
	v_rcp_f32_e32 v92, v92
	v_rcp_f32_e32 v93, v93
	s_nop 0
	v_fma_f32 v95, v93, s18, v94
	v_fma_f32 v94, v92, s18, v94
	s_nop 0
	v_fma_f32 v94, v92, v94, s22
	v_fma_f32 v95, v93, v95, s22
	s_nop 0
	v_fma_f32 v94, v92, v94, s24
	v_fma_f32 v95, v93, v95, s24
	s_nop 0
	v_fma_f32 v94, v92, v94, s26
	v_fma_f32 v95, v93, v95, s26
	s_nop 0
	v_mul_f32_e32 v92, v92, v94
	v_mul_f32_e32 v93, v93, v95
	v_mul_f32_e32 v94, s28, v96
	v_mul_f32_e32 v95, s28, v97
	s_nop 0
	v_exp_f32_e32 v94, v94
	v_exp_f32_e32 v95, v95
	s_nop 0
	v_mul_f32_e32 v92, v94, v92
	v_mul_f32_e32 v93, v95, v93
	s_nop 0
	v_mul_f32_e32 v94, v82, v92
	v_mul_f32_e32 v95, v83, v93
	v_fma_f32 v92, -v82, v92, v82
	v_fma_f32 v93, -v83, v93, v83
	s_nop 0
	v_cndmask_b32_e32 v82, v92, v94, vcc
	v_cmp_gt_f32_e32 vcc, 0, v83
	s_nop 1
	v_cndmask_b32_e32 v83, v93, v95, vcc
; __device__ __forceinline__ unsigned cvt_pk_bf16(float lo, float hi) { unsigned r; asm volatile("v_cvt_pk_bf16_f32 %0, %1, %2" : "=v"(r) : "v"(lo), "v"(hi)); return r; }
; __device__ __forceinline__ f32x2 gelu_pk(f32x2 v) {
;     const f32x2 av = __builtin_elementwise_abs(v), d = av * 0.2316418882f + 1.0f;
;     f32x2 t; t.x = __builtin_amdgcn_rcpf(d.x); t.y = __builtin_amdgcn_rcpf(d.y);
;     f32x2 q = t * 0.5307027145f + (-0.7265760135f); q = q * t + 0.7107068705f; q = q * t + (-0.142248368f); q = q * t + 0.127414796f; q = q * t;
;     const f32x2 s = (v * v) * (-0.72134752044f);
;     f32x2 e; e.x = __builtin_amdgcn_exp2f(s.x); e.y = __builtin_amdgcn_exp2f(s.y);
;     const f32x2 m = v * (q * e), r = v - m;
;     f32x2 o; o.x = v.x < 0.f ? m.x : r.x; o.y = v.y < 0.f ? m.y : r.y; return o;
;     __device__ __forceinline__ void operator()(const f32x4 (&acc)[2][2][4][2], const Unit& u, int wr, int wc, int fr, int fq) const {
;     ...
;                 for (int bj = 0; bj < 2; ++bj) { const i32x4 a0 = __builtin_bit_cast(i32x4, acc[ai][bj][m][0]), a1 = __builtin_bit_cast(i32x4, acc[ai][bj][m][1]);
;                     f32x4 v0 = (f32x4){(float)a0[0], (float)a0[1], (float)a0[2], (float)a0[3]} * rsc * cv[bj][0], v1 = (f32x4){(float)a1[0], (float)a1[1], (float)a1[2], (float)a1[3]} * rsc * cv[bj][1];
;                     if (act) { f32x2 a = gelu_pk((f32x2){v0[0], v0[1]}), b = gelu_pk((f32x2){v0[2], v0[3]}), c = gelu_pk((f32x2){v1[0], v1[1]}), d = gelu_pk((f32x2){v1[2], v1[3]});
;                         v0 = (f32x4){a.x, a.y, b.x, b.y}; v1 = (f32x4){c.x, c.y, d.x, d.y}; }
;                     u32x4 w; w.x = cvt_pk_bf16(v0[0], v0[1]); w.y = cvt_pk_bf16(v0[2], v0[3]); w.z = cvt_pk_bf16(v1[0], v1[1]); w.w = cvt_pk_bf16(v1[2], v1[3]);
;                     if (nt) __builtin_nontemporal_store(w, (u32x4*)(rowp + bj * HALF)); else *(u32x4*)(rowp + bj * HALF) = w; } }
.LBB0_353:
	v_cvt_f32_i32_e32 v81, v81
	v_cvt_f32_i32_e32 v80, v80
	v_cvt_pk_bf16_f32 v86, v86, v87
	v_cvt_pk_bf16_f32 v87, v84, v85
	v_cvt_pk_bf16_f32 v88, v88, v89
	v_cvt_f32_i32_e32 v79, v79
	v_cvt_f32_i32_e32 v78, v78
	v_cvt_pk_bf16_f32 v89, v82, v83
	v_cvt_f32_i32_e32 v83, v77
	v_cvt_f32_i32_e32 v75, v75
	v_cvt_f32_i32_e32 v74, v74
	v_cvt_f32_i32_e32 v82, v76
	v_mul_f32_e32 v80, v178, v80
	v_mul_f32_e32 v81, v178, v81
	v_mul_f32_e32 v78, v178, v78
	v_mul_f32_e32 v79, v178, v79
	v_mul_f32_e32 v76, v40, v80
	v_mul_f32_e32 v77, v41, v81
	v_mul_f32_e32 v74, v178, v74
	v_mul_f32_e32 v75, v178, v75
	v_mul_f32_e32 v80, v178, v82
	v_mul_f32_e32 v81, v178, v83
	v_mul_f32_e32 v78, v38, v78
	v_mul_f32_e32 v79, v39, v79
	v_mul_f32_e32 v80, v36, v80
	v_mul_f32_e32 v81, v37, v81
	s_and_b64 vcc, exec, s[4:5]
	v_mul_f32_e32 v82, v34, v74
	v_mul_f32_e32 v83, v35, v75
	global_store_dwordx4 v[90:91], v[86:89], off offset:256
	s_cbranch_vccnz .LBB0_355
	v_and_b32_e32 v75, 0x7fffffff, v79
	v_and_b32_e32 v74, 0x7fffffff, v78
	v_fma_f32 v74, v74, s16, 1.0
	v_fma_f32 v75, v75, s16, 1.0
	v_mov_b64_e32 v[84:85], s[20:21]
	v_rcp_f32_e32 v74, v74
	v_rcp_f32_e32 v75, v75
	v_mul_f32_e32 v88, v78, v78
	v_mul_f32_e32 v89, v79, v79
	v_cmp_gt_f32_e32 vcc, 0, v78
	v_mul_f32_e32 v88, s28, v88
	v_mul_f32_e32 v89, s28, v89
	v_fma_f32 v86, v74, s18, v84
	v_fma_f32 v87, v75, s18, v84
	v_exp_f32_e32 v88, v88
	v_fma_f32 v86, v74, v86, s22
	v_fma_f32 v87, v75, v87, s22
	v_exp_f32_e32 v89, v89
	v_fma_f32 v86, v74, v86, s24
	v_fma_f32 v87, v75, v87, s24
	s_nop 0
	v_fma_f32 v86, v74, v86, s26
	v_fma_f32 v87, v75, v87, s26
	s_nop 0
	v_mul_f32_e32 v74, v74, v86
	v_mul_f32_e32 v75, v75, v87
	v_mul_f32_e32 v86, v76, v76
	v_mul_f32_e32 v87, v77, v77
	v_mul_f32_e32 v74, v88, v74
	v_mul_f32_e32 v75, v89, v75
	v_mul_f32_e32 v86, s28, v86
	v_mul_f32_e32 v87, s28, v87
	v_mul_f32_e32 v88, v78, v74
	v_mul_f32_e32 v89, v79, v75
	v_fma_f32 v74, -v78, v74, v78
	v_fma_f32 v75, -v79, v75, v79
	v_exp_f32_e32 v86, v86
	v_cndmask_b32_e32 v78, v74, v88, vcc
	v_cmp_gt_f32_e32 vcc, 0, v79
	v_and_b32_e32 v74, 0x7fffffff, v76
	v_exp_f32_e32 v87, v87
	v_cndmask_b32_e32 v79, v75, v89, vcc
	v_and_b32_e32 v75, 0x7fffffff, v77
	v_fma_f32 v74, v74, s16, 1.0
	v_fma_f32 v75, v75, s16, 1.0
	v_cmp_gt_f32_e32 vcc, 0, v76
	v_rcp_f32_e32 v74, v74
	v_rcp_f32_e32 v75, v75
	s_nop 0
	v_fma_f32 v88, v74, s18, v84
	v_fma_f32 v89, v75, s18, v84
	s_nop 0
	v_fma_f32 v88, v74, v88, s22
	v_fma_f32 v89, v75, v89, s22
	s_nop 0
	v_fma_f32 v88, v74, v88, s24
	v_fma_f32 v89, v75, v89, s24
	s_nop 0
	v_fma_f32 v88, v74, v88, s26
	v_fma_f32 v89, v75, v89, s26
	s_nop 0
	v_mul_f32_e32 v74, v74, v88
	v_mul_f32_e32 v75, v75, v89
	v_mul_f32_e32 v88, v82, v82
	v_mul_f32_e32 v89, v83, v83
	v_mul_f32_e32 v74, v86, v74
	v_mul_f32_e32 v75, v87, v75
	v_mul_f32_e32 v88, s28, v88
	v_mul_f32_e32 v89, s28, v89
	v_mul_f32_e32 v86, v76, v74
	v_mul_f32_e32 v87, v77, v75
	v_fma_f32 v74, -v76, v74, v76
	v_fma_f32 v75, -v77, v75, v77
	v_exp_f32_e32 v88, v88
	v_cndmask_b32_e32 v76, v74, v86, vcc
	v_cmp_gt_f32_e32 vcc, 0, v77
	v_and_b32_e32 v74, 0x7fffffff, v82
	v_exp_f32_e32 v89, v89
	v_cndmask_b32_e32 v77, v75, v87, vcc
	v_and_b32_e32 v75, 0x7fffffff, v83
	v_fma_f32 v74, v74, s16, 1.0
	v_fma_f32 v75, v75, s16, 1.0
	v_cmp_gt_f32_e32 vcc, 0, v82
	v_rcp_f32_e32 v74, v74
	v_rcp_f32_e32 v75, v75
	s_nop 0
	v_fma_f32 v86, v74, s18, v84
	v_fma_f32 v87, v75, s18, v84
	s_nop 0
	v_fma_f32 v86, v74, v86, s22
	v_fma_f32 v87, v75, v87, s22
	s_nop 0
	v_fma_f32 v86, v74, v86, s24
	v_fma_f32 v87, v75, v87, s24
	s_nop 0
	v_fma_f32 v86, v74, v86, s26
	v_fma_f32 v87, v75, v87, s26
	s_nop 0
	v_mul_f32_e32 v74, v74, v86
	v_mul_f32_e32 v75, v75, v87
	v_mul_f32_e32 v86, v80, v80
	v_mul_f32_e32 v87, v81, v81
	v_mul_f32_e32 v74, v88, v74
	v_mul_f32_e32 v75, v89, v75
	s_nop 0
	v_mul_f32_e32 v88, v82, v74
	v_mul_f32_e32 v89, v83, v75
	v_fma_f32 v74, -v82, v74, v82
	v_fma_f32 v75, -v83, v75, v83
	s_nop 0
	v_cndmask_b32_e32 v82, v74, v88, vcc
	v_cmp_gt_f32_e32 vcc, 0, v83
	v_and_b32_e32 v74, 0x7fffffff, v80
	s_nop 0
	v_cndmask_b32_e32 v83, v75, v89, vcc
	v_and_b32_e32 v75, 0x7fffffff, v81
	v_fma_f32 v74, v74, s16, 1.0
	v_fma_f32 v75, v75, s16, 1.0
	v_cmp_gt_f32_e32 vcc, 0, v80
	v_rcp_f32_e32 v74, v74
	v_rcp_f32_e32 v75, v75
	s_nop 0
	v_fma_f32 v85, v75, s18, v84
	v_fma_f32 v84, v74, s18, v84
	s_nop 0
	v_fma_f32 v84, v74, v84, s22
	v_fma_f32 v85, v75, v85, s22
	s_nop 0
	v_fma_f32 v84, v74, v84, s24
	v_fma_f32 v85, v75, v85, s24
	s_nop 0
	v_fma_f32 v84, v74, v84, s26
	v_fma_f32 v85, v75, v85, s26
	s_nop 0
	v_mul_f32_e32 v74, v74, v84
	v_mul_f32_e32 v75, v75, v85
	v_mul_f32_e32 v84, s28, v86
	v_mul_f32_e32 v85, s28, v87
	s_nop 0
	v_exp_f32_e32 v84, v84
	v_exp_f32_e32 v85, v85
	s_nop 0
	v_mul_f32_e32 v74, v84, v74
	v_mul_f32_e32 v75, v85, v75
	s_nop 0
	v_mul_f32_e32 v84, v80, v74
	v_mul_f32_e32 v85, v81, v75
	v_fma_f32 v74, -v80, v74, v80
	v_fma_f32 v75, -v81, v75, v81
	s_nop 0
	v_cndmask_b32_e32 v80, v74, v84, vcc
	v_cmp_gt_f32_e32 vcc, 0, v81
	s_nop 1
	v_cndmask_b32_e32 v81, v75, v85, vcc
; __device__ __forceinline__ unsigned cvt_pk_bf16(float lo, float hi) { unsigned r; asm volatile("v_cvt_pk_bf16_f32 %0, %1, %2" : "=v"(r) : "v"(lo), "v"(hi)); return r; }
; __device__ __forceinline__ f32x2 gelu_pk(f32x2 v) {
;     const f32x2 av = __builtin_elementwise_abs(v), d = av * 0.2316418882f + 1.0f;
;     f32x2 t; t.x = __builtin_amdgcn_rcpf(d.x); t.y = __builtin_amdgcn_rcpf(d.y);
;     f32x2 q = t * 0.5307027145f + (-0.7265760135f); q = q * t + 0.7107068705f; q = q * t + (-0.142248368f); q = q * t + 0.127414796f; q = q * t;
;     const f32x2 s = (v * v) * (-0.72134752044f);
;     f32x2 e; e.x = __builtin_amdgcn_exp2f(s.x); e.y = __builtin_amdgcn_exp2f(s.y);
;     const f32x2 m = v * (q * e), r = v - m;
;     f32x2 o; o.x = v.x < 0.f ? m.x : r.x; o.y = v.y < 0.f ? m.y : r.y; return o;
;     __device__ __forceinline__ void operator()(const f32x4 (&acc)[2][2][4][2], const Unit& u, int wr, int wc, int fr, int fq) const {
;     ...
;                 for (int bj = 0; bj < 2; ++bj) { const i32x4 a0 = __builtin_bit_cast(i32x4, acc[ai][bj][m][0]), a1 = __builtin_bit_cast(i32x4, acc[ai][bj][m][1]);
;                     f32x4 v0 = (f32x4){(float)a0[0], (float)a0[1], (float)a0[2], (float)a0[3]} * rsc * cv[bj][0], v1 = (f32x4){(float)a1[0], (float)a1[1], (float)a1[2], (float)a1[3]} * rsc * cv[bj][1];
;                     if (act) { f32x2 a = gelu_pk((f32x2){v0[0], v0[1]}), b = gelu_pk((f32x2){v0[2], v0[3]}), c = gelu_pk((f32x2){v1[0], v1[1]}), d = gelu_pk((f32x2){v1[2], v1[3]});
;                         v0 = (f32x4){a.x, a.y, b.x, b.y}; v1 = (f32x4){c.x, c.y, d.x, d.y}; }
;                     u32x4 w; w.x = cvt_pk_bf16(v0[0], v0[1]); w.y = cvt_pk_bf16(v0[2], v0[3]); w.z = cvt_pk_bf16(v1[0], v1[1]); w.w = cvt_pk_bf16(v1[2], v1[3]);
;                     if (nt) __builtin_nontemporal_store(w, (u32x4*)(rowp + bj * HALF)); else *(u32x4*)(rowp + bj * HALF) = w; } }
.LBB0_355:
	v_lshlrev_b64 v[74:75], 15, v[172:173]
	v_lshl_add_u64 v[74:75], s[70:71], 0, v[74:75]
	v_lshl_add_u64 v[74:75], v[170:171], 1, v[74:75]
	s_mov_b32 s2, 0x400000
	v_cvt_f32_i32_e32 v73, v73
	v_cvt_f32_i32_e32 v72, v72
	v_cvt_pk_bf16_f32 v84, v78, v79
	v_cvt_pk_bf16_f32 v85, v76, v77
	v_add_co_u32_e32 v76, vcc, s2, v74
	v_cvt_f32_i32_e32 v71, v71
	v_cvt_f32_i32_e32 v70, v70
	v_cvt_f32_i32_e32 v67, v67
	v_cvt_f32_i32_e32 v79, v69
	v_cvt_f32_i32_e32 v78, v68
	v_cvt_f32_i32_e32 v66, v66
	v_addc_co_u32_e32 v77, vcc, 0, v75, vcc
	v_cvt_pk_bf16_f32 v86, v82, v83
	v_cvt_pk_bf16_f32 v87, v80, v81
	global_store_dwordx4 v[76:77], v[84:87], off
	v_mov_b32_e32 v76, v178
	v_mov_b32_e32 v77, v178
	v_mov_b32_e32 v179, v178
	v_mul_f32_e32 v72, v76, v72
	v_mul_f32_e32 v73, v77, v73
	v_mul_f32_e32 v70, v178, v70
	v_mul_f32_e32 v71, v179, v71
	v_mul_f32_e32 v68, v28, v72
	v_mul_f32_e32 v69, v29, v73
	v_mul_f32_e32 v72, v76, v78
	v_mul_f32_e32 v73, v77, v79
	v_mul_f32_e32 v76, v178, v66
	v_mul_f32_e32 v77, v179, v67
	v_mul_f32_e32 v70, v26, v70
	v_mul_f32_e32 v71, v27, v71
	v_mul_f32_e32 v66, v24, v72
	v_mul_f32_e32 v67, v25, v73
	s_and_b64 vcc, exec, s[4:5]
	v_mul_f32_e32 v72, v22, v76
	v_mul_f32_e32 v73, v23, v77
	s_cbranch_vccnz .LBB0_357
	v_and_b32_e32 v77, 0x7fffffff, v71
	v_and_b32_e32 v76, 0x7fffffff, v70
	v_fma_f32 v76, v76, s16, 1.0
	v_fma_f32 v77, v77, s16, 1.0
	v_mov_b64_e32 v[78:79], s[20:21]
	v_rcp_f32_e32 v76, v76
	v_rcp_f32_e32 v77, v77
	v_mul_f32_e32 v82, v70, v70
	v_mul_f32_e32 v83, v71, v71
	v_cmp_gt_f32_e32 vcc, 0, v70
	v_mul_f32_e32 v82, s28, v82
	v_mul_f32_e32 v83, s28, v83
	v_fma_f32 v80, v76, s18, v78
	v_fma_f32 v81, v77, s18, v78
	v_exp_f32_e32 v82, v82
	v_fma_f32 v80, v76, v80, s22
	v_fma_f32 v81, v77, v81, s22
	v_exp_f32_e32 v83, v83
	v_fma_f32 v80, v76, v80, s24
	v_fma_f32 v81, v77, v81, s24
	s_nop 0
	v_fma_f32 v80, v76, v80, s26
	v_fma_f32 v81, v77, v81, s26
	s_nop 0
	v_mul_f32_e32 v76, v76, v80
	v_mul_f32_e32 v77, v77, v81
	v_mul_f32_e32 v80, v68, v68
	v_mul_f32_e32 v81, v69, v69
	v_mul_f32_e32 v76, v82, v76
	v_mul_f32_e32 v77, v83, v77
	v_mul_f32_e32 v80, s28, v80
	v_mul_f32_e32 v81, s28, v81
	v_mul_f32_e32 v82, v70, v76
	v_mul_f32_e32 v83, v71, v77
	v_fma_f32 v76, -v70, v76, v70
	v_fma_f32 v77, -v71, v77, v71
	v_exp_f32_e32 v80, v80
	v_cndmask_b32_e32 v70, v76, v82, vcc
	v_cmp_gt_f32_e32 vcc, 0, v71
	v_and_b32_e32 v76, 0x7fffffff, v68
	v_exp_f32_e32 v81, v81
	v_cndmask_b32_e32 v71, v77, v83, vcc
	v_and_b32_e32 v77, 0x7fffffff, v69
	v_fma_f32 v76, v76, s16, 1.0
	v_fma_f32 v77, v77, s16, 1.0
	v_cmp_gt_f32_e32 vcc, 0, v68
	v_rcp_f32_e32 v76, v76
	v_rcp_f32_e32 v77, v77
	s_nop 0
	v_fma_f32 v82, v76, s18, v78
	v_fma_f32 v83, v77, s18, v78
	s_nop 0
	v_fma_f32 v82, v76, v82, s22
	v_fma_f32 v83, v77, v83, s22
	s_nop 0
	v_fma_f32 v82, v76, v82, s24
	v_fma_f32 v83, v77, v83, s24
	s_nop 0
	v_fma_f32 v82, v76, v82, s26
	v_fma_f32 v83, v77, v83, s26
	s_nop 0
	v_mul_f32_e32 v76, v76, v82
	v_mul_f32_e32 v77, v77, v83
	v_mul_f32_e32 v82, v72, v72
	v_mul_f32_e32 v83, v73, v73
	v_mul_f32_e32 v76, v80, v76
	v_mul_f32_e32 v77, v81, v77
	v_mul_f32_e32 v82, s28, v82
	v_mul_f32_e32 v83, s28, v83
	v_mul_f32_e32 v80, v68, v76
	v_mul_f32_e32 v81, v69, v77
	v_fma_f32 v76, -v68, v76, v68
	v_fma_f32 v77, -v69, v77, v69
	v_exp_f32_e32 v82, v82
	v_cndmask_b32_e32 v68, v76, v80, vcc
	v_cmp_gt_f32_e32 vcc, 0, v69
	v_and_b32_e32 v76, 0x7fffffff, v72
	v_exp_f32_e32 v83, v83
	v_cndmask_b32_e32 v69, v77, v81, vcc
	v_and_b32_e32 v77, 0x7fffffff, v73
	v_fma_f32 v76, v76, s16, 1.0
	v_fma_f32 v77, v77, s16, 1.0
	v_cmp_gt_f32_e32 vcc, 0, v72
	v_rcp_f32_e32 v76, v76
	v_rcp_f32_e32 v77, v77
	s_nop 0
	v_fma_f32 v80, v76, s18, v78
	v_fma_f32 v81, v77, s18, v78
	s_nop 0
	v_fma_f32 v80, v76, v80, s22
	v_fma_f32 v81, v77, v81, s22
	s_nop 0
	v_fma_f32 v80, v76, v80, s24
	v_fma_f32 v81, v77, v81, s24
	s_nop 0
	v_fma_f32 v80, v76, v80, s26
	v_fma_f32 v81, v77, v81, s26
	s_nop 0
	v_mul_f32_e32 v76, v76, v80
	v_mul_f32_e32 v77, v77, v81
	v_mul_f32_e32 v80, v66, v66
	v_mul_f32_e32 v81, v67, v67
	v_mul_f32_e32 v76, v82, v76
	v_mul_f32_e32 v77, v83, v77
	s_nop 0
	v_mul_f32_e32 v82, v72, v76
	v_mul_f32_e32 v83, v73, v77
	v_fma_f32 v76, -v72, v76, v72
	v_fma_f32 v77, -v73, v77, v73
	s_nop 0
	v_cndmask_b32_e32 v72, v76, v82, vcc
	v_cmp_gt_f32_e32 vcc, 0, v73
	v_and_b32_e32 v76, 0x7fffffff, v66
	s_nop 0
	v_cndmask_b32_e32 v73, v77, v83, vcc
	v_and_b32_e32 v77, 0x7fffffff, v67
	v_fma_f32 v76, v76, s16, 1.0
	v_fma_f32 v77, v77, s16, 1.0
	v_cmp_gt_f32_e32 vcc, 0, v66
	v_rcp_f32_e32 v76, v76
	v_rcp_f32_e32 v77, v77
	s_nop 0
	v_fma_f32 v79, v77, s18, v78
	v_fma_f32 v78, v76, s18, v78
	s_nop 0
	v_fma_f32 v78, v76, v78, s22
	v_fma_f32 v79, v77, v79, s22
	s_nop 0
	v_fma_f32 v78, v76, v78, s24
	v_fma_f32 v79, v77, v79, s24
	s_nop 0
	v_fma_f32 v78, v76, v78, s26
	v_fma_f32 v79, v77, v79, s26
	s_nop 0
	v_mul_f32_e32 v76, v76, v78
	v_mul_f32_e32 v77, v77, v79
	v_mul_f32_e32 v78, s28, v80
	v_mul_f32_e32 v79, s28, v81
	s_nop 0
	v_exp_f32_e32 v78, v78
	v_exp_f32_e32 v79, v79
	s_nop 0
	v_mul_f32_e32 v76, v78, v76
	v_mul_f32_e32 v77, v79, v77
	s_nop 0
	v_mul_f32_e32 v78, v66, v76
	v_mul_f32_e32 v79, v67, v77
	v_fma_f32 v76, -v66, v76, v66
	v_fma_f32 v77, -v67, v77, v67
	s_nop 0
	v_cndmask_b32_e32 v66, v76, v78, vcc
	v_cmp_gt_f32_e32 vcc, 0, v67
	s_nop 1
	v_cndmask_b32_e32 v67, v77, v79, vcc
; __device__ __forceinline__ unsigned cvt_pk_bf16(float lo, float hi) { unsigned r; asm volatile("v_cvt_pk_bf16_f32 %0, %1, %2" : "=v"(r) : "v"(lo), "v"(hi)); return r; }
; __device__ __forceinline__ f32x2 gelu_pk(f32x2 v) {
;     const f32x2 av = __builtin_elementwise_abs(v), d = av * 0.2316418882f + 1.0f;
;     f32x2 t; t.x = __builtin_amdgcn_rcpf(d.x); t.y = __builtin_amdgcn_rcpf(d.y);
;     f32x2 q = t * 0.5307027145f + (-0.7265760135f); q = q * t + 0.7107068705f; q = q * t + (-0.142248368f); q = q * t + 0.127414796f; q = q * t;
;     const f32x2 s = (v * v) * (-0.72134752044f);
;     f32x2 e; e.x = __builtin_amdgcn_exp2f(s.x); e.y = __builtin_amdgcn_exp2f(s.y);
;     const f32x2 m = v * (q * e), r = v - m;
;     f32x2 o; o.x = v.x < 0.f ? m.x : r.x; o.y = v.y < 0.f ? m.y : r.y; return o;
;     __device__ __forceinline__ void operator()(const f32x4 (&acc)[2][2][4][2], const Unit& u, int wr, int wc, int fr, int fq) const {
;     ...
;                 for (int bj = 0; bj < 2; ++bj) { const i32x4 a0 = __builtin_bit_cast(i32x4, acc[ai][bj][m][0]), a1 = __builtin_bit_cast(i32x4, acc[ai][bj][m][1]);
;                     f32x4 v0 = (f32x4){(float)a0[0], (float)a0[1], (float)a0[2], (float)a0[3]} * rsc * cv[bj][0], v1 = (f32x4){(float)a1[0], (float)a1[1], (float)a1[2], (float)a1[3]} * rsc * cv[bj][1];
;                     if (act) { f32x2 a = gelu_pk((f32x2){v0[0], v0[1]}), b = gelu_pk((f32x2){v0[2], v0[3]}), c = gelu_pk((f32x2){v1[0], v1[1]}), d = gelu_pk((f32x2){v1[2], v1[3]});
;                         v0 = (f32x4){a.x, a.y, b.x, b.y}; v1 = (f32x4){c.x, c.y, d.x, d.y}; }
;                     u32x4 w; w.x = cvt_pk_bf16(v0[0], v0[1]); w.y = cvt_pk_bf16(v0[2], v0[3]); w.z = cvt_pk_bf16(v1[0], v1[1]); w.w = cvt_pk_bf16(v1[2], v1[3]);
;                     if (nt) __builtin_nontemporal_store(w, (u32x4*)(rowp + bj * HALF)); else *(u32x4*)(rowp + bj * HALF) = w; } }
.LBB0_357:
	v_cvt_f32_i32_e32 v65, v65
	v_cvt_f32_i32_e32 v64, v64
	v_cvt_pk_bf16_f32 v70, v70, v71
	v_cvt_pk_bf16_f32 v71, v68, v69
	v_cvt_pk_bf16_f32 v72, v72, v73
	v_cvt_f32_i32_e32 v63, v63
	v_cvt_f32_i32_e32 v62, v62
	v_cvt_pk_bf16_f32 v73, v66, v67
	v_cvt_f32_i32_e32 v67, v61
	v_cvt_f32_i32_e32 v59, v59
	v_cvt_f32_i32_e32 v58, v58
	v_cvt_f32_i32_e32 v66, v60
	v_mul_f32_e32 v64, v176, v64
	v_mul_f32_e32 v65, v176, v65
	s_mov_b64 s[40:41], 0x400000
	v_mul_f32_e32 v62, v176, v62
	v_mul_f32_e32 v63, v176, v63
	v_mul_f32_e32 v60, v40, v64
	v_mul_f32_e32 v61, v41, v65
	v_mul_f32_e32 v58, v176, v58
	v_mul_f32_e32 v59, v176, v59
	v_mul_f32_e32 v64, v176, v66
	v_mul_f32_e32 v65, v176, v67
	v_lshl_add_u64 v[74:75], v[74:75], 0, s[40:41]
	v_mul_f32_e32 v62, v38, v62
	v_mul_f32_e32 v63, v39, v63
	v_mul_f32_e32 v64, v36, v64
	v_mul_f32_e32 v65, v37, v65
	s_and_b64 vcc, exec, s[4:5]
	v_mul_f32_e32 v66, v34, v58
	v_mul_f32_e32 v67, v35, v59
	global_store_dwordx4 v[74:75], v[70:73], off offset:256
	s_cbranch_vccnz .LBB0_359
	v_and_b32_e32 v59, 0x7fffffff, v63
	v_and_b32_e32 v58, 0x7fffffff, v62
	v_fma_f32 v58, v58, s16, 1.0
	v_fma_f32 v59, v59, s16, 1.0
	v_mov_b64_e32 v[68:69], s[20:21]
	v_rcp_f32_e32 v58, v58
	v_rcp_f32_e32 v59, v59
	v_mul_f32_e32 v72, v62, v62
	v_mul_f32_e32 v73, v63, v63
	v_cmp_gt_f32_e32 vcc, 0, v62
	v_mul_f32_e32 v72, s28, v72
	v_mul_f32_e32 v73, s28, v73
	v_fma_f32 v70, v58, s18, v68
	v_fma_f32 v71, v59, s18, v68
	v_exp_f32_e32 v72, v72
	v_fma_f32 v70, v58, v70, s22
	v_fma_f32 v71, v59, v71, s22
	v_exp_f32_e32 v73, v73
	v_fma_f32 v70, v58, v70, s24
	v_fma_f32 v71, v59, v71, s24
	s_nop 0
	v_fma_f32 v70, v58, v70, s26
	v_fma_f32 v71, v59, v71, s26
	s_nop 0
	v_mul_f32_e32 v58, v58, v70
	v_mul_f32_e32 v59, v59, v71
	v_mul_f32_e32 v70, v60, v60
	v_mul_f32_e32 v71, v61, v61
	v_mul_f32_e32 v58, v72, v58
	v_mul_f32_e32 v59, v73, v59
	v_mul_f32_e32 v70, s28, v70
	v_mul_f32_e32 v71, s28, v71
	v_mul_f32_e32 v72, v62, v58
	v_mul_f32_e32 v73, v63, v59
	v_fma_f32 v58, -v62, v58, v62
	v_fma_f32 v59, -v63, v59, v63
	v_exp_f32_e32 v70, v70
	v_cndmask_b32_e32 v62, v58, v72, vcc
	v_cmp_gt_f32_e32 vcc, 0, v63
	v_and_b32_e32 v58, 0x7fffffff, v60
	v_exp_f32_e32 v71, v71
	v_cndmask_b32_e32 v63, v59, v73, vcc
	v_and_b32_e32 v59, 0x7fffffff, v61
	v_fma_f32 v58, v58, s16, 1.0
	v_fma_f32 v59, v59, s16, 1.0
	v_cmp_gt_f32_e32 vcc, 0, v60
	v_rcp_f32_e32 v58, v58
	v_rcp_f32_e32 v59, v59
	s_nop 0
	v_fma_f32 v72, v58, s18, v68
	v_fma_f32 v73, v59, s18, v68
	s_nop 0
	v_fma_f32 v72, v58, v72, s22
	v_fma_f32 v73, v59, v73, s22
	s_nop 0
	v_fma_f32 v72, v58, v72, s24
	v_fma_f32 v73, v59, v73, s24
	s_nop 0
	v_fma_f32 v72, v58, v72, s26
	v_fma_f32 v73, v59, v73, s26
	s_nop 0
	v_mul_f32_e32 v58, v58, v72
	v_mul_f32_e32 v59, v59, v73
	v_mul_f32_e32 v72, v66, v66
	v_mul_f32_e32 v73, v67, v67
	v_mul_f32_e32 v58, v70, v58
	v_mul_f32_e32 v59, v71, v59
	v_mul_f32_e32 v72, s28, v72
	v_mul_f32_e32 v73, s28, v73
	v_mul_f32_e32 v70, v60, v58
	v_mul_f32_e32 v71, v61, v59
	v_fma_f32 v58, -v60, v58, v60
	v_fma_f32 v59, -v61, v59, v61
	v_exp_f32_e32 v72, v72
	v_cndmask_b32_e32 v60, v58, v70, vcc
	v_cmp_gt_f32_e32 vcc, 0, v61
	v_and_b32_e32 v58, 0x7fffffff, v66
	v_exp_f32_e32 v73, v73
	v_cndmask_b32_e32 v61, v59, v71, vcc
	v_and_b32_e32 v59, 0x7fffffff, v67
	v_fma_f32 v58, v58, s16, 1.0
	v_fma_f32 v59, v59, s16, 1.0
	v_cmp_gt_f32_e32 vcc, 0, v66
	v_rcp_f32_e32 v58, v58
	v_rcp_f32_e32 v59, v59
	s_nop 0
	v_fma_f32 v70, v58, s18, v68
	v_fma_f32 v71, v59, s18, v68
	s_nop 0
	v_fma_f32 v70, v58, v70, s22
	v_fma_f32 v71, v59, v71, s22
	s_nop 0
	v_fma_f32 v70, v58, v70, s24
	v_fma_f32 v71, v59, v71, s24
	s_nop 0
	v_fma_f32 v70, v58, v70, s26
	v_fma_f32 v71, v59, v71, s26
	s_nop 0
	v_mul_f32_e32 v58, v58, v70
	v_mul_f32_e32 v59, v59, v71
	v_mul_f32_e32 v70, v64, v64
	v_mul_f32_e32 v71, v65, v65
	v_mul_f32_e32 v58, v72, v58
	v_mul_f32_e32 v59, v73, v59
	s_nop 0
	v_mul_f32_e32 v72, v66, v58
	v_mul_f32_e32 v73, v67, v59
	v_fma_f32 v58, -v66, v58, v66
	v_fma_f32 v59, -v67, v59, v67
	s_nop 0
	v_cndmask_b32_e32 v66, v58, v72, vcc
	v_cmp_gt_f32_e32 vcc, 0, v67
	v_and_b32_e32 v58, 0x7fffffff, v64
	s_nop 0
	v_cndmask_b32_e32 v67, v59, v73, vcc
	v_and_b32_e32 v59, 0x7fffffff, v65
	v_fma_f32 v58, v58, s16, 1.0
	v_fma_f32 v59, v59, s16, 1.0
	v_cmp_gt_f32_e32 vcc, 0, v64
	v_rcp_f32_e32 v58, v58
	v_rcp_f32_e32 v59, v59
	s_nop 0
	v_fma_f32 v69, v59, s18, v68
	v_fma_f32 v68, v58, s18, v68
	s_nop 0
	v_fma_f32 v68, v58, v68, s22
	v_fma_f32 v69, v59, v69, s22
	s_nop 0
	v_fma_f32 v68, v58, v68, s24
	v_fma_f32 v69, v59, v69, s24
	s_nop 0
	v_fma_f32 v68, v58, v68, s26
	v_fma_f32 v69, v59, v69, s26
	s_nop 0
	v_mul_f32_e32 v58, v58, v68
	v_mul_f32_e32 v59, v59, v69
	v_mul_f32_e32 v68, s28, v70
	v_mul_f32_e32 v69, s28, v71
	s_nop 0
	v_exp_f32_e32 v68, v68
	v_exp_f32_e32 v69, v69
	s_nop 0
	v_mul_f32_e32 v58, v68, v58
	v_mul_f32_e32 v59, v69, v59
	s_nop 0
	v_mul_f32_e32 v68, v64, v58
	v_mul_f32_e32 v69, v65, v59
	v_fma_f32 v58, -v64, v58, v64
	v_fma_f32 v59, -v65, v59, v65
	s_nop 0
	v_cndmask_b32_e32 v64, v58, v68, vcc
	v_cmp_gt_f32_e32 vcc, 0, v65
	s_nop 1
	v_cndmask_b32_e32 v65, v59, v69, vcc
; __device__ __forceinline__ unsigned cvt_pk_bf16(float lo, float hi) { unsigned r; asm volatile("v_cvt_pk_bf16_f32 %0, %1, %2" : "=v"(r) : "v"(lo), "v"(hi)); return r; }
; __device__ __forceinline__ f32x2 gelu_pk(f32x2 v) {
;     const f32x2 av = __builtin_elementwise_abs(v), d = av * 0.2316418882f + 1.0f;
;     f32x2 t; t.x = __builtin_amdgcn_rcpf(d.x); t.y = __builtin_amdgcn_rcpf(d.y);
;     f32x2 q = t * 0.5307027145f + (-0.7265760135f); q = q * t + 0.7107068705f; q = q * t + (-0.142248368f); q = q * t + 0.127414796f; q = q * t;
;     const f32x2 s = (v * v) * (-0.72134752044f);
;     f32x2 e; e.x = __builtin_amdgcn_exp2f(s.x); e.y = __builtin_amdgcn_exp2f(s.y);
;     const f32x2 m = v * (q * e), r = v - m;
;     f32x2 o; o.x = v.x < 0.f ? m.x : r.x; o.y = v.y < 0.f ? m.y : r.y; return o;
;     __device__ __forceinline__ void operator()(const f32x4 (&acc)[2][2][4][2], const Unit& u, int wr, int wc, int fr, int fq) const {
;     ...
;                 for (int bj = 0; bj < 2; ++bj) { const i32x4 a0 = __builtin_bit_cast(i32x4, acc[ai][bj][m][0]), a1 = __builtin_bit_cast(i32x4, acc[ai][bj][m][1]);
;                     f32x4 v0 = (f32x4){(float)a0[0], (float)a0[1], (float)a0[2], (float)a0[3]} * rsc * cv[bj][0], v1 = (f32x4){(float)a1[0], (float)a1[1], (float)a1[2], (float)a1[3]} * rsc * cv[bj][1];
;                     if (act) { f32x2 a = gelu_pk((f32x2){v0[0], v0[1]}), b = gelu_pk((f32x2){v0[2], v0[3]}), c = gelu_pk((f32x2){v1[0], v1[1]}), d = gelu_pk((f32x2){v1[2], v1[3]});
;                         v0 = (f32x4){a.x, a.y, b.x, b.y}; v1 = (f32x4){c.x, c.y, d.x, d.y}; }
;                     u32x4 w; w.x = cvt_pk_bf16(v0[0], v0[1]); w.y = cvt_pk_bf16(v0[2], v0[3]); w.z = cvt_pk_bf16(v1[0], v1[1]); w.w = cvt_pk_bf16(v1[2], v1[3]);
;                     if (nt) __builtin_nontemporal_store(w, (u32x4*)(rowp + bj * HALF)); else *(u32x4*)(rowp + bj * HALF) = w; } }
.LBB0_359:
	v_lshlrev_b64 v[58:59], 15, v[172:173]
	v_lshl_add_u64 v[58:59], s[70:71], 0, v[58:59]
	v_lshl_add_u64 v[58:59], v[170:171], 1, v[58:59]
	s_mov_b32 s2, 0x480000
	v_cvt_f32_i32_e32 v57, v57
	v_cvt_f32_i32_e32 v56, v56
	v_cvt_pk_bf16_f32 v68, v62, v63
	v_cvt_pk_bf16_f32 v69, v60, v61
	v_add_co_u32_e32 v60, vcc, s2, v58
	v_cvt_f32_i32_e32 v55, v55
	v_cvt_f32_i32_e32 v54, v54
	v_cvt_f32_i32_e32 v51, v51
	v_cvt_f32_i32_e32 v63, v53
	v_cvt_f32_i32_e32 v62, v52
	v_cvt_f32_i32_e32 v50, v50
	v_addc_co_u32_e32 v61, vcc, 0, v59, vcc
	v_cvt_pk_bf16_f32 v70, v66, v67
	v_cvt_pk_bf16_f32 v71, v64, v65
	global_store_dwordx4 v[60:61], v[68:71], off
	v_mov_b32_e32 v60, v176
	v_mov_b32_e32 v61, v176
	v_mov_b32_e32 v177, v176
	v_mul_f32_e32 v56, v60, v56
	v_mul_f32_e32 v57, v61, v57
	v_mul_f32_e32 v54, v176, v54
	v_mul_f32_e32 v55, v177, v55
	v_mul_f32_e32 v52, v28, v56
	v_mul_f32_e32 v53, v29, v57
	v_mul_f32_e32 v56, v60, v62
	v_mul_f32_e32 v57, v61, v63
	v_mul_f32_e32 v60, v176, v50
	v_mul_f32_e32 v61, v177, v51
	v_mul_f32_e32 v54, v26, v54
	v_mul_f32_e32 v55, v27, v55
	v_mul_f32_e32 v50, v24, v56
	v_mul_f32_e32 v51, v25, v57
	s_and_b64 vcc, exec, s[4:5]
	v_mul_f32_e32 v56, v22, v60
	v_mul_f32_e32 v57, v23, v61
	s_cbranch_vccnz .LBB0_361
	v_and_b32_e32 v61, 0x7fffffff, v55
	v_and_b32_e32 v60, 0x7fffffff, v54
	v_fma_f32 v60, v60, s16, 1.0
	v_fma_f32 v61, v61, s16, 1.0
	v_mov_b64_e32 v[62:63], s[20:21]
	v_rcp_f32_e32 v60, v60
	v_rcp_f32_e32 v61, v61
	v_mul_f32_e32 v66, v54, v54
	v_mul_f32_e32 v67, v55, v55
	v_cmp_gt_f32_e32 vcc, 0, v54
	v_mul_f32_e32 v66, s28, v66
	v_mul_f32_e32 v67, s28, v67
	v_fma_f32 v64, v60, s18, v62
	v_fma_f32 v65, v61, s18, v62
	v_exp_f32_e32 v66, v66
	v_fma_f32 v64, v60, v64, s22
	v_fma_f32 v65, v61, v65, s22
	v_exp_f32_e32 v67, v67
	v_fma_f32 v64, v60, v64, s24
	v_fma_f32 v65, v61, v65, s24
	s_nop 0
	v_fma_f32 v64, v60, v64, s26
	v_fma_f32 v65, v61, v65, s26
	s_nop 0
	v_mul_f32_e32 v60, v60, v64
	v_mul_f32_e32 v61, v61, v65
	v_mul_f32_e32 v64, v52, v52
	v_mul_f32_e32 v65, v53, v53
	v_mul_f32_e32 v60, v66, v60
	v_mul_f32_e32 v61, v67, v61
	v_mul_f32_e32 v64, s28, v64
	v_mul_f32_e32 v65, s28, v65
	v_mul_f32_e32 v66, v54, v60
	v_mul_f32_e32 v67, v55, v61
	v_fma_f32 v60, -v54, v60, v54
	v_fma_f32 v61, -v55, v61, v55
	v_exp_f32_e32 v64, v64
	v_cndmask_b32_e32 v54, v60, v66, vcc
	v_cmp_gt_f32_e32 vcc, 0, v55
	v_and_b32_e32 v60, 0x7fffffff, v52
	v_exp_f32_e32 v65, v65
	v_cndmask_b32_e32 v55, v61, v67, vcc
	v_and_b32_e32 v61, 0x7fffffff, v53
	v_fma_f32 v60, v60, s16, 1.0
	v_fma_f32 v61, v61, s16, 1.0
	v_cmp_gt_f32_e32 vcc, 0, v52
	v_rcp_f32_e32 v60, v60
	v_rcp_f32_e32 v61, v61
	s_nop 0
	v_fma_f32 v66, v60, s18, v62
	v_fma_f32 v67, v61, s18, v62
	s_nop 0
	v_fma_f32 v66, v60, v66, s22
	v_fma_f32 v67, v61, v67, s22
	s_nop 0
	v_fma_f32 v66, v60, v66, s24
	v_fma_f32 v67, v61, v67, s24
	s_nop 0
	v_fma_f32 v66, v60, v66, s26
	v_fma_f32 v67, v61, v67, s26
	s_nop 0
	v_mul_f32_e32 v60, v60, v66
	v_mul_f32_e32 v61, v61, v67
	v_mul_f32_e32 v66, v56, v56
	v_mul_f32_e32 v67, v57, v57
	v_mul_f32_e32 v60, v64, v60
	v_mul_f32_e32 v61, v65, v61
	v_mul_f32_e32 v66, s28, v66
	v_mul_f32_e32 v67, s28, v67
	v_mul_f32_e32 v64, v52, v60
	v_mul_f32_e32 v65, v53, v61
	v_fma_f32 v60, -v52, v60, v52
	v_fma_f32 v61, -v53, v61, v53
	v_exp_f32_e32 v66, v66
	v_cndmask_b32_e32 v52, v60, v64, vcc
	v_cmp_gt_f32_e32 vcc, 0, v53
	v_and_b32_e32 v60, 0x7fffffff, v56
	v_exp_f32_e32 v67, v67
	v_cndmask_b32_e32 v53, v61, v65, vcc
	v_and_b32_e32 v61, 0x7fffffff, v57
	v_fma_f32 v60, v60, s16, 1.0
	v_fma_f32 v61, v61, s16, 1.0
	v_cmp_gt_f32_e32 vcc, 0, v56
	v_rcp_f32_e32 v60, v60
	v_rcp_f32_e32 v61, v61
	s_nop 0
	v_fma_f32 v64, v60, s18, v62
	v_fma_f32 v65, v61, s18, v62
	s_nop 0
	v_fma_f32 v64, v60, v64, s22
	v_fma_f32 v65, v61, v65, s22
	s_nop 0
	v_fma_f32 v64, v60, v64, s24
	v_fma_f32 v65, v61, v65, s24
	s_nop 0
	v_fma_f32 v64, v60, v64, s26
	v_fma_f32 v65, v61, v65, s26
	s_nop 0
	v_mul_f32_e32 v60, v60, v64
	v_mul_f32_e32 v61, v61, v65
	v_mul_f32_e32 v64, v50, v50
	v_mul_f32_e32 v65, v51, v51
	v_mul_f32_e32 v60, v66, v60
	v_mul_f32_e32 v61, v67, v61
	s_nop 0
	v_mul_f32_e32 v66, v56, v60
	v_mul_f32_e32 v67, v57, v61
	v_fma_f32 v60, -v56, v60, v56
	v_fma_f32 v61, -v57, v61, v57
	s_nop 0
	v_cndmask_b32_e32 v56, v60, v66, vcc
	v_cmp_gt_f32_e32 vcc, 0, v57
	v_and_b32_e32 v60, 0x7fffffff, v50
	s_nop 0
	v_cndmask_b32_e32 v57, v61, v67, vcc
	v_and_b32_e32 v61, 0x7fffffff, v51
	v_fma_f32 v60, v60, s16, 1.0
	v_fma_f32 v61, v61, s16, 1.0
	v_cmp_gt_f32_e32 vcc, 0, v50
	v_rcp_f32_e32 v60, v60
	v_rcp_f32_e32 v61, v61
	s_nop 0
	v_fma_f32 v63, v61, s18, v62
	v_fma_f32 v62, v60, s18, v62
	s_nop 0
	v_fma_f32 v62, v60, v62, s22
	v_fma_f32 v63, v61, v63, s22
	s_nop 0
	v_fma_f32 v62, v60, v62, s24
	v_fma_f32 v63, v61, v63, s24
	s_nop 0
	v_fma_f32 v62, v60, v62, s26
	v_fma_f32 v63, v61, v63, s26
	s_nop 0
	v_mul_f32_e32 v60, v60, v62
	v_mul_f32_e32 v61, v61, v63
	v_mul_f32_e32 v62, s28, v64
	v_mul_f32_e32 v63, s28, v65
	s_nop 0
	v_exp_f32_e32 v62, v62
	v_exp_f32_e32 v63, v63
	s_nop 0
	v_mul_f32_e32 v60, v62, v60
	v_mul_f32_e32 v61, v63, v61
	s_nop 0
	v_mul_f32_e32 v62, v50, v60
	v_mul_f32_e32 v63, v51, v61
	v_fma_f32 v60, -v50, v60, v50
	v_fma_f32 v61, -v51, v61, v51
	s_nop 0
	v_cndmask_b32_e32 v50, v60, v62, vcc
	v_cmp_gt_f32_e32 vcc, 0, v51
	s_nop 1
	v_cndmask_b32_e32 v51, v61, v63, vcc
; __device__ __forceinline__ unsigned cvt_pk_bf16(float lo, float hi) { unsigned r; asm volatile("v_cvt_pk_bf16_f32 %0, %1, %2" : "=v"(r) : "v"(lo), "v"(hi)); return r; }
; __device__ __forceinline__ f32x2 gelu_pk(f32x2 v) {
;     const f32x2 av = __builtin_elementwise_abs(v), d = av * 0.2316418882f + 1.0f;
;     f32x2 t; t.x = __builtin_amdgcn_rcpf(d.x); t.y = __builtin_amdgcn_rcpf(d.y);
;     f32x2 q = t * 0.5307027145f + (-0.7265760135f); q = q * t + 0.7107068705f; q = q * t + (-0.142248368f); q = q * t + 0.127414796f; q = q * t;
;     const f32x2 s = (v * v) * (-0.72134752044f);
;     f32x2 e; e.x = __builtin_amdgcn_exp2f(s.x); e.y = __builtin_amdgcn_exp2f(s.y);
;     const f32x2 m = v * (q * e), r = v - m;
;     f32x2 o; o.x = v.x < 0.f ? m.x : r.x; o.y = v.y < 0.f ? m.y : r.y; return o;
;     __device__ __forceinline__ void operator()(const f32x4 (&acc)[2][2][4][2], const Unit& u, int wr, int wc, int fr, int fq) const {
;     ...
;                 for (int bj = 0; bj < 2; ++bj) { const i32x4 a0 = __builtin_bit_cast(i32x4, acc[ai][bj][m][0]), a1 = __builtin_bit_cast(i32x4, acc[ai][bj][m][1]);
;                     f32x4 v0 = (f32x4){(float)a0[0], (float)a0[1], (float)a0[2], (float)a0[3]} * rsc * cv[bj][0], v1 = (f32x4){(float)a1[0], (float)a1[1], (float)a1[2], (float)a1[3]} * rsc * cv[bj][1];
;                     if (act) { f32x2 a = gelu_pk((f32x2){v0[0], v0[1]}), b = gelu_pk((f32x2){v0[2], v0[3]}), c = gelu_pk((f32x2){v1[0], v1[1]}), d = gelu_pk((f32x2){v1[2], v1[3]});
;                         v0 = (f32x4){a.x, a.y, b.x, b.y}; v1 = (f32x4){c.x, c.y, d.x, d.y}; }
;                     u32x4 w; w.x = cvt_pk_bf16(v0[0], v0[1]); w.y = cvt_pk_bf16(v0[2], v0[3]); w.z = cvt_pk_bf16(v1[0], v1[1]); w.w = cvt_pk_bf16(v1[2], v1[3]);
;                     if (nt) __builtin_nontemporal_store(w, (u32x4*)(rowp + bj * HALF)); else *(u32x4*)(rowp + bj * HALF) = w; } }
.LBB0_361:
	v_cvt_f32_i32_e32 v49, v49
	v_cvt_f32_i32_e32 v48, v48
	v_cvt_pk_bf16_f32 v54, v54, v55
	v_cvt_pk_bf16_f32 v55, v52, v53
	v_cvt_pk_bf16_f32 v56, v56, v57
	v_cvt_f32_i32_e32 v47, v47
	v_cvt_f32_i32_e32 v46, v46
	v_cvt_pk_bf16_f32 v57, v50, v51
	v_cvt_f32_i32_e32 v51, v45
	v_cvt_f32_i32_e32 v43, v43
	v_cvt_f32_i32_e32 v42, v42
	v_cvt_f32_i32_e32 v50, v44
	v_mul_f32_e32 v48, v174, v48
	v_mul_f32_e32 v49, v174, v49
	s_mov_b64 s[40:41], 0x480000
	v_mul_f32_e32 v46, v174, v46
	v_mul_f32_e32 v47, v174, v47
	v_mul_f32_e32 v44, v40, v48
	v_mul_f32_e32 v45, v41, v49
	v_mul_f32_e32 v42, v174, v42
	v_mul_f32_e32 v43, v174, v43
	v_mul_f32_e32 v48, v174, v50
	v_mul_f32_e32 v49, v174, v51
	v_lshl_add_u64 v[58:59], v[58:59], 0, s[40:41]
	v_mul_f32_e32 v46, v38, v46
	v_mul_f32_e32 v47, v39, v47
	v_mul_f32_e32 v48, v36, v48
	v_mul_f32_e32 v49, v37, v49
	s_and_b64 vcc, exec, s[4:5]
	v_mul_f32_e32 v50, v34, v42
	v_mul_f32_e32 v51, v35, v43
	global_store_dwordx4 v[58:59], v[54:57], off offset:256
	s_cbranch_vccnz .LBB0_363
	v_and_b32_e32 v43, 0x7fffffff, v47
	v_and_b32_e32 v42, 0x7fffffff, v46
	v_fma_f32 v42, v42, s16, 1.0
	v_fma_f32 v43, v43, s16, 1.0
	v_mov_b64_e32 v[52:53], s[20:21]
	v_rcp_f32_e32 v42, v42
	v_rcp_f32_e32 v43, v43
	v_mul_f32_e32 v56, v46, v46
	v_mul_f32_e32 v57, v47, v47
	v_cmp_gt_f32_e32 vcc, 0, v46
	v_mul_f32_e32 v56, s28, v56
	v_mul_f32_e32 v57, s28, v57
	v_fma_f32 v54, v42, s18, v52
	v_fma_f32 v55, v43, s18, v52
	v_exp_f32_e32 v56, v56
	v_fma_f32 v54, v42, v54, s22
	v_fma_f32 v55, v43, v55, s22
	v_exp_f32_e32 v57, v57
	v_fma_f32 v54, v42, v54, s24
	v_fma_f32 v55, v43, v55, s24
	s_nop 0
	v_fma_f32 v54, v42, v54, s26
	v_fma_f32 v55, v43, v55, s26
	s_nop 0
	v_mul_f32_e32 v42, v42, v54
	v_mul_f32_e32 v43, v43, v55
	v_mul_f32_e32 v54, v44, v44
	v_mul_f32_e32 v55, v45, v45
	v_mul_f32_e32 v42, v56, v42
	v_mul_f32_e32 v43, v57, v43
	v_mul_f32_e32 v54, s28, v54
	v_mul_f32_e32 v55, s28, v55
	v_mul_f32_e32 v56, v46, v42
	v_mul_f32_e32 v57, v47, v43
	v_fma_f32 v42, -v46, v42, v46
	v_fma_f32 v43, -v47, v43, v47
	v_exp_f32_e32 v54, v54
	v_cndmask_b32_e32 v46, v42, v56, vcc
	v_cmp_gt_f32_e32 vcc, 0, v47
	v_and_b32_e32 v42, 0x7fffffff, v44
	v_exp_f32_e32 v55, v55
	v_cndmask_b32_e32 v47, v43, v57, vcc
	v_and_b32_e32 v43, 0x7fffffff, v45
	v_fma_f32 v42, v42, s16, 1.0
	v_fma_f32 v43, v43, s16, 1.0
	v_cmp_gt_f32_e32 vcc, 0, v44
	v_rcp_f32_e32 v42, v42
	v_rcp_f32_e32 v43, v43
	s_nop 0
	v_fma_f32 v56, v42, s18, v52
	v_fma_f32 v57, v43, s18, v52
	s_nop 0
	v_fma_f32 v56, v42, v56, s22
	v_fma_f32 v57, v43, v57, s22
	s_nop 0
	v_fma_f32 v56, v42, v56, s24
	v_fma_f32 v57, v43, v57, s24
	s_nop 0
	v_fma_f32 v56, v42, v56, s26
	v_fma_f32 v57, v43, v57, s26
	s_nop 0
	v_mul_f32_e32 v42, v42, v56
	v_mul_f32_e32 v43, v43, v57
	v_mul_f32_e32 v56, v50, v50
	v_mul_f32_e32 v57, v51, v51
	v_mul_f32_e32 v42, v54, v42
	v_mul_f32_e32 v43, v55, v43
	v_mul_f32_e32 v56, s28, v56
	v_mul_f32_e32 v57, s28, v57
	v_mul_f32_e32 v54, v44, v42
	v_mul_f32_e32 v55, v45, v43
	v_fma_f32 v42, -v44, v42, v44
	v_fma_f32 v43, -v45, v43, v45
	v_exp_f32_e32 v56, v56
	v_cndmask_b32_e32 v44, v42, v54, vcc
	v_cmp_gt_f32_e32 vcc, 0, v45
	v_and_b32_e32 v42, 0x7fffffff, v50
	v_exp_f32_e32 v57, v57
	v_cndmask_b32_e32 v45, v43, v55, vcc
	v_and_b32_e32 v43, 0x7fffffff, v51
	v_fma_f32 v42, v42, s16, 1.0
	v_fma_f32 v43, v43, s16, 1.0
	v_cmp_gt_f32_e32 vcc, 0, v50
	v_rcp_f32_e32 v42, v42
	v_rcp_f32_e32 v43, v43
	s_nop 0
	v_fma_f32 v54, v42, s18, v52
	v_fma_f32 v55, v43, s18, v52
	s_nop 0
	v_fma_f32 v54, v42, v54, s22
	v_fma_f32 v55, v43, v55, s22
	s_nop 0
	v_fma_f32 v54, v42, v54, s24
	v_fma_f32 v55, v43, v55, s24
	s_nop 0
	v_fma_f32 v54, v42, v54, s26
	v_fma_f32 v55, v43, v55, s26
	s_nop 0
	v_mul_f32_e32 v42, v42, v54
	v_mul_f32_e32 v43, v43, v55
	v_mul_f32_e32 v54, v48, v48
	v_mul_f32_e32 v55, v49, v49
	v_mul_f32_e32 v42, v56, v42
	v_mul_f32_e32 v43, v57, v43
	s_nop 0
	v_mul_f32_e32 v56, v50, v42
	v_mul_f32_e32 v57, v51, v43
	v_fma_f32 v42, -v50, v42, v50
	v_fma_f32 v43, -v51, v43, v51
	s_nop 0
	v_cndmask_b32_e32 v50, v42, v56, vcc
	v_cmp_gt_f32_e32 vcc, 0, v51
	v_and_b32_e32 v42, 0x7fffffff, v48
	s_nop 0
	v_cndmask_b32_e32 v51, v43, v57, vcc
	v_and_b32_e32 v43, 0x7fffffff, v49
	v_fma_f32 v42, v42, s16, 1.0
	v_fma_f32 v43, v43, s16, 1.0
	v_cmp_gt_f32_e32 vcc, 0, v48
	v_rcp_f32_e32 v42, v42
	v_rcp_f32_e32 v43, v43
	s_nop 0
	v_fma_f32 v53, v43, s18, v52
	v_fma_f32 v52, v42, s18, v52
	s_nop 0
	v_fma_f32 v52, v42, v52, s22
	v_fma_f32 v53, v43, v53, s22
	s_nop 0
	v_fma_f32 v52, v42, v52, s24
	v_fma_f32 v53, v43, v53, s24
	s_nop 0
	v_fma_f32 v52, v42, v52, s26
	v_fma_f32 v53, v43, v53, s26
	s_nop 0
	v_mul_f32_e32 v42, v42, v52
	v_mul_f32_e32 v43, v43, v53
	v_mul_f32_e32 v52, s28, v54
	v_mul_f32_e32 v53, s28, v55
	s_nop 0
	v_exp_f32_e32 v52, v52
	v_exp_f32_e32 v53, v53
	s_nop 0
	v_mul_f32_e32 v42, v52, v42
	v_mul_f32_e32 v43, v53, v43
	s_nop 0
	v_mul_f32_e32 v52, v48, v42
	v_mul_f32_e32 v53, v49, v43
	v_fma_f32 v42, -v48, v42, v48
	v_fma_f32 v43, -v49, v43, v49
	s_nop 0
	v_cndmask_b32_e32 v48, v42, v52, vcc
	v_cmp_gt_f32_e32 vcc, 0, v49
	s_nop 1
	v_cndmask_b32_e32 v49, v43, v53, vcc
; __device__ __forceinline__ unsigned cvt_pk_bf16(float lo, float hi) { unsigned r; asm volatile("v_cvt_pk_bf16_f32 %0, %1, %2" : "=v"(r) : "v"(lo), "v"(hi)); return r; }
; __device__ __forceinline__ f32x2 gelu_pk(f32x2 v) {
;     const f32x2 av = __builtin_elementwise_abs(v), d = av * 0.2316418882f + 1.0f;
;     f32x2 t; t.x = __builtin_amdgcn_rcpf(d.x); t.y = __builtin_amdgcn_rcpf(d.y);
;     f32x2 q = t * 0.5307027145f + (-0.7265760135f); q = q * t + 0.7107068705f; q = q * t + (-0.142248368f); q = q * t + 0.127414796f; q = q * t;
;     const f32x2 s = (v * v) * (-0.72134752044f);
;     f32x2 e; e.x = __builtin_amdgcn_exp2f(s.x); e.y = __builtin_amdgcn_exp2f(s.y);
;     const f32x2 m = v * (q * e), r = v - m;
;     f32x2 o; o.x = v.x < 0.f ? m.x : r.x; o.y = v.y < 0.f ? m.y : r.y; return o;
;     __device__ __forceinline__ void operator()(const f32x4 (&acc)[2][2][4][2], const Unit& u, int wr, int wc, int fr, int fq) const {
;     ...
;                 for (int bj = 0; bj < 2; ++bj) { const i32x4 a0 = __builtin_bit_cast(i32x4, acc[ai][bj][m][0]), a1 = __builtin_bit_cast(i32x4, acc[ai][bj][m][1]);
;                     f32x4 v0 = (f32x4){(float)a0[0], (float)a0[1], (float)a0[2], (float)a0[3]} * rsc * cv[bj][0], v1 = (f32x4){(float)a1[0], (float)a1[1], (float)a1[2], (float)a1[3]} * rsc * cv[bj][1];
;                     if (act) { f32x2 a = gelu_pk((f32x2){v0[0], v0[1]}), b = gelu_pk((f32x2){v0[2], v0[3]}), c = gelu_pk((f32x2){v1[0], v1[1]}), d = gelu_pk((f32x2){v1[2], v1[3]});
;                         v0 = (f32x4){a.x, a.y, b.x, b.y}; v1 = (f32x4){c.x, c.y, d.x, d.y}; }
;                     u32x4 w; w.x = cvt_pk_bf16(v0[0], v0[1]); w.y = cvt_pk_bf16(v0[2], v0[3]); w.z = cvt_pk_bf16(v1[0], v1[1]); w.w = cvt_pk_bf16(v1[2], v1[3]);
;                     if (nt) __builtin_nontemporal_store(w, (u32x4*)(rowp + bj * HALF)); else *(u32x4*)(rowp + bj * HALF) = w; } }
.LBB0_363:
	v_lshlrev_b64 v[42:43], 15, v[172:173]
	v_lshl_add_u64 v[42:43], s[70:71], 0, v[42:43]
	v_lshl_add_u64 v[42:43], v[170:171], 1, v[42:43]
	s_mov_b32 s2, 0x500000
	v_cvt_f32_i32_e32 v33, v33
	v_cvt_f32_i32_e32 v32, v32
	v_cvt_pk_bf16_f32 v52, v46, v47
	v_cvt_pk_bf16_f32 v53, v44, v45
	v_add_co_u32_e32 v44, vcc, s2, v42
	v_cvt_f32_i32_e32 v31, v31
	v_cvt_f32_i32_e32 v30, v30
	v_cvt_f32_i32_e32 v19, v19
	v_cvt_f32_i32_e32 v47, v21
	v_cvt_f32_i32_e32 v46, v20
	v_cvt_f32_i32_e32 v18, v18
	v_addc_co_u32_e32 v45, vcc, 0, v43, vcc
	v_cvt_pk_bf16_f32 v54, v50, v51
	v_cvt_pk_bf16_f32 v55, v48, v49
	global_store_dwordx4 v[44:45], v[52:55], off
	v_mov_b32_e32 v44, v174
	v_mov_b32_e32 v45, v174
	v_mov_b32_e32 v175, v174
	v_mul_f32_e32 v32, v44, v32
	v_mul_f32_e32 v33, v45, v33
	v_mul_f32_e32 v30, v174, v30
	v_mul_f32_e32 v31, v175, v31
	v_mul_f32_e32 v20, v28, v32
	v_mul_f32_e32 v21, v29, v33
	v_mul_f32_e32 v32, v44, v46
	v_mul_f32_e32 v33, v45, v47
	v_mul_f32_e32 v44, v174, v18
	v_mul_f32_e32 v45, v175, v19
	v_mul_f32_e32 v30, v26, v30
	v_mul_f32_e32 v31, v27, v31
	v_mul_f32_e32 v18, v24, v32
	v_mul_f32_e32 v19, v25, v33
	s_and_b64 vcc, exec, s[4:5]
	v_mul_f32_e32 v32, v22, v44
	v_mul_f32_e32 v33, v23, v45
	s_cbranch_vccnz .LBB0_365
	v_and_b32_e32 v45, 0x7fffffff, v31
	v_and_b32_e32 v44, 0x7fffffff, v30
	v_fma_f32 v44, v44, s16, 1.0
	v_fma_f32 v45, v45, s16, 1.0
	v_mov_b64_e32 v[46:47], s[20:21]
	v_rcp_f32_e32 v44, v44
	v_rcp_f32_e32 v45, v45
	v_mul_f32_e32 v50, v30, v30
	v_mul_f32_e32 v51, v31, v31
	v_cmp_gt_f32_e32 vcc, 0, v30
	v_mul_f32_e32 v50, s28, v50
	v_mul_f32_e32 v51, s28, v51
	v_fma_f32 v48, v44, s18, v46
	v_fma_f32 v49, v45, s18, v46
	v_exp_f32_e32 v50, v50
	v_fma_f32 v48, v44, v48, s22
	v_fma_f32 v49, v45, v49, s22
	v_exp_f32_e32 v51, v51
	v_fma_f32 v48, v44, v48, s24
	v_fma_f32 v49, v45, v49, s24
	s_nop 0
	v_fma_f32 v48, v44, v48, s26
	v_fma_f32 v49, v45, v49, s26
	s_nop 0
	v_mul_f32_e32 v44, v44, v48
	v_mul_f32_e32 v45, v45, v49
	v_mul_f32_e32 v48, v20, v20
	v_mul_f32_e32 v49, v21, v21
	v_mul_f32_e32 v44, v50, v44
	v_mul_f32_e32 v45, v51, v45
	v_mul_f32_e32 v48, s28, v48
	v_mul_f32_e32 v49, s28, v49
	v_mul_f32_e32 v50, v30, v44
	v_mul_f32_e32 v51, v31, v45
	v_fma_f32 v44, -v30, v44, v30
	v_fma_f32 v45, -v31, v45, v31
	v_exp_f32_e32 v48, v48
	v_cndmask_b32_e32 v30, v44, v50, vcc
	v_cmp_gt_f32_e32 vcc, 0, v31
	v_and_b32_e32 v44, 0x7fffffff, v20
	v_exp_f32_e32 v49, v49
	v_cndmask_b32_e32 v31, v45, v51, vcc
	v_and_b32_e32 v45, 0x7fffffff, v21
	v_fma_f32 v44, v44, s16, 1.0
	v_fma_f32 v45, v45, s16, 1.0
	v_cmp_gt_f32_e32 vcc, 0, v20
	v_rcp_f32_e32 v44, v44
	v_rcp_f32_e32 v45, v45
	s_nop 0
	v_fma_f32 v50, v44, s18, v46
	v_fma_f32 v51, v45, s18, v46
	s_nop 0
	v_fma_f32 v50, v44, v50, s22
	v_fma_f32 v51, v45, v51, s22
	s_nop 0
	v_fma_f32 v50, v44, v50, s24
	v_fma_f32 v51, v45, v51, s24
	s_nop 0
	v_fma_f32 v50, v44, v50, s26
	v_fma_f32 v51, v45, v51, s26
	s_nop 0
	v_mul_f32_e32 v44, v44, v50
	v_mul_f32_e32 v45, v45, v51
	v_mul_f32_e32 v50, v32, v32
	v_mul_f32_e32 v51, v33, v33
	v_mul_f32_e32 v44, v48, v44
	v_mul_f32_e32 v45, v49, v45
	v_mul_f32_e32 v50, s28, v50
	v_mul_f32_e32 v51, s28, v51
	v_mul_f32_e32 v48, v20, v44
	v_mul_f32_e32 v49, v21, v45
	v_fma_f32 v44, -v20, v44, v20
	v_fma_f32 v45, -v21, v45, v21
	v_exp_f32_e32 v50, v50
	v_cndmask_b32_e32 v20, v44, v48, vcc
	v_cmp_gt_f32_e32 vcc, 0, v21
	v_and_b32_e32 v44, 0x7fffffff, v32
	v_exp_f32_e32 v51, v51
	v_cndmask_b32_e32 v21, v45, v49, vcc
	v_and_b32_e32 v45, 0x7fffffff, v33
	v_fma_f32 v44, v44, s16, 1.0
	v_fma_f32 v45, v45, s16, 1.0
	v_cmp_gt_f32_e32 vcc, 0, v32
	v_rcp_f32_e32 v44, v44
	v_rcp_f32_e32 v45, v45
	s_nop 0
	v_fma_f32 v48, v44, s18, v46
	v_fma_f32 v49, v45, s18, v46
	s_nop 0
	v_fma_f32 v48, v44, v48, s22
	v_fma_f32 v49, v45, v49, s22
	s_nop 0
	v_fma_f32 v48, v44, v48, s24
	v_fma_f32 v49, v45, v49, s24
	s_nop 0
	v_fma_f32 v48, v44, v48, s26
	v_fma_f32 v49, v45, v49, s26
	s_nop 0
	v_mul_f32_e32 v44, v44, v48
	v_mul_f32_e32 v45, v45, v49
	v_mul_f32_e32 v48, v18, v18
	v_mul_f32_e32 v49, v19, v19
	v_mul_f32_e32 v44, v50, v44
	v_mul_f32_e32 v45, v51, v45
	s_nop 0
	v_mul_f32_e32 v50, v32, v44
	v_mul_f32_e32 v51, v33, v45
	v_fma_f32 v44, -v32, v44, v32
	v_fma_f32 v45, -v33, v45, v33
	s_nop 0
	v_cndmask_b32_e32 v32, v44, v50, vcc
	v_cmp_gt_f32_e32 vcc, 0, v33
	v_and_b32_e32 v44, 0x7fffffff, v18
	s_nop 0
	v_cndmask_b32_e32 v33, v45, v51, vcc
	v_and_b32_e32 v45, 0x7fffffff, v19
	v_fma_f32 v44, v44, s16, 1.0
	v_fma_f32 v45, v45, s16, 1.0
	v_cmp_gt_f32_e32 vcc, 0, v18
	v_rcp_f32_e32 v44, v44
	v_rcp_f32_e32 v45, v45
	s_nop 0
	v_fma_f32 v47, v45, s18, v46
	v_fma_f32 v46, v44, s18, v46
	s_nop 0
	v_fma_f32 v46, v44, v46, s22
	v_fma_f32 v47, v45, v47, s22
	s_nop 0
	v_fma_f32 v46, v44, v46, s24
	v_fma_f32 v47, v45, v47, s24
	s_nop 0
	v_fma_f32 v46, v44, v46, s26
	v_fma_f32 v47, v45, v47, s26
	s_nop 0
	v_mul_f32_e32 v44, v44, v46
	v_mul_f32_e32 v45, v45, v47
	v_mul_f32_e32 v46, s28, v48
	v_mul_f32_e32 v47, s28, v49
	s_nop 0
	v_exp_f32_e32 v46, v46
	v_exp_f32_e32 v47, v47
	s_nop 0
	v_mul_f32_e32 v44, v46, v44
	v_mul_f32_e32 v45, v47, v45
	s_nop 0
	v_mul_f32_e32 v46, v18, v44
	v_mul_f32_e32 v47, v19, v45
	v_fma_f32 v44, -v18, v44, v18
	v_fma_f32 v45, -v19, v45, v19
	s_nop 0
	v_cndmask_b32_e32 v18, v44, v46, vcc
	v_cmp_gt_f32_e32 vcc, 0, v19
	s_nop 1
	v_cndmask_b32_e32 v19, v45, v47, vcc
; __device__ __forceinline__ unsigned cvt_pk_bf16(float lo, float hi) { unsigned r; asm volatile("v_cvt_pk_bf16_f32 %0, %1, %2" : "=v"(r) : "v"(lo), "v"(hi)); return r; }
; __device__ __forceinline__ f32x2 gelu_pk(f32x2 v) {
;     const f32x2 av = __builtin_elementwise_abs(v), d = av * 0.2316418882f + 1.0f;
;     f32x2 t; t.x = __builtin_amdgcn_rcpf(d.x); t.y = __builtin_amdgcn_rcpf(d.y);
;     f32x2 q = t * 0.5307027145f + (-0.7265760135f); q = q * t + 0.7107068705f; q = q * t + (-0.142248368f); q = q * t + 0.127414796f; q = q * t;
;     const f32x2 s = (v * v) * (-0.72134752044f);
;     f32x2 e; e.x = __builtin_amdgcn_exp2f(s.x); e.y = __builtin_amdgcn_exp2f(s.y);
;     const f32x2 m = v * (q * e), r = v - m;
;     f32x2 o; o.x = v.x < 0.f ? m.x : r.x; o.y = v.y < 0.f ? m.y : r.y; return o;
;     __device__ __forceinline__ void operator()(const f32x4 (&acc)[2][2][4][2], const Unit& u, int wr, int wc, int fr, int fq) const {
;     ...
;             for (int m = 0; m < 4; ++m) { const int row = row0 + ai * HALF + m * 16; const float rsc = rsv[ai][m]; bf16_t* rowp = O + (size_t)row * ldc + col0;
; #pragma unroll
;                 for (int bj = 0; bj < 2; ++bj) { const i32x4 a0 = __builtin_bit_cast(i32x4, acc[ai][bj][m][0]), a1 = __builtin_bit_cast(i32x4, acc[ai][bj][m][1]);
;                     f32x4 v0 = (f32x4){(float)a0[0], (float)a0[1], (float)a0[2], (float)a0[3]} * rsc * cv[bj][0], v1 = (f32x4){(float)a1[0], (float)a1[1], (float)a1[2], (float)a1[3]} * rsc * cv[bj][1];
;                     if (act) { f32x2 a = gelu_pk((f32x2){v0[0], v0[1]}), b = gelu_pk((f32x2){v0[2], v0[3]}), c = gelu_pk((f32x2){v1[0], v1[1]}), d = gelu_pk((f32x2){v1[2], v1[3]});
;                         v0 = (f32x4){a.x, a.y, b.x, b.y}; v1 = (f32x4){c.x, c.y, d.x, d.y}; }
;                     u32x4 w; w.x = cvt_pk_bf16(v0[0], v0[1]); w.y = cvt_pk_bf16(v0[2], v0[3]); w.z = cvt_pk_bf16(v1[0], v1[1]); w.w = cvt_pk_bf16(v1[2], v1[3]);
.LBB0_365:
	v_cvt_f32_i32_e32 v17, v17
	v_cvt_f32_i32_e32 v16, v16
	v_cvt_pk_bf16_f32 v30, v30, v31
	v_cvt_pk_bf16_f32 v31, v20, v21
	v_cvt_pk_bf16_f32 v32, v32, v33
	v_cvt_f32_i32_e32 v15, v15
	v_cvt_f32_i32_e32 v14, v14
	v_cvt_pk_bf16_f32 v33, v18, v19
	v_cvt_f32_i32_e32 v19, v13
	v_cvt_f32_i32_e32 v11, v11
	v_cvt_f32_i32_e32 v10, v10
	v_cvt_f32_i32_e32 v18, v12
	v_mul_f32_e32 v16, v168, v16
	v_mul_f32_e32 v17, v168, v17
	s_mov_b64 s[40:41], 0x500000
	v_mul_f32_e32 v14, v168, v14
	v_mul_f32_e32 v15, v168, v15
	v_mul_f32_e32 v12, v40, v16
	v_mul_f32_e32 v13, v41, v17
	v_mul_f32_e32 v10, v168, v10
	v_mul_f32_e32 v11, v168, v11
	v_mul_f32_e32 v16, v168, v18
	v_mul_f32_e32 v17, v168, v19
	v_lshl_add_u64 v[42:43], v[42:43], 0, s[40:41]
	v_mul_f32_e32 v14, v38, v14
	v_mul_f32_e32 v15, v39, v15
	v_mul_f32_e32 v16, v36, v16
	v_mul_f32_e32 v17, v37, v17
	s_and_b64 vcc, exec, s[4:5]
	v_mul_f32_e32 v18, v34, v10
	v_mul_f32_e32 v19, v35, v11
	global_store_dwordx4 v[42:43], v[30:33], off offset:256
	s_cbranch_vccnz .LBB0_367
	v_and_b32_e32 v11, 0x7fffffff, v15
	v_and_b32_e32 v10, 0x7fffffff, v14
	v_fma_f32 v10, v10, s16, 1.0
	v_fma_f32 v11, v11, s16, 1.0
	v_mov_b64_e32 v[20:21], s[20:21]
	v_rcp_f32_e32 v10, v10
	v_rcp_f32_e32 v11, v11
	v_mul_f32_e32 v32, v14, v14
	v_mul_f32_e32 v33, v15, v15
	v_cmp_gt_f32_e32 vcc, 0, v14
	v_mul_f32_e32 v32, s28, v32
	v_mul_f32_e32 v33, s28, v33
	v_fma_f32 v30, v10, s18, v20
	v_fma_f32 v31, v11, s18, v20
	v_exp_f32_e32 v32, v32
	v_fma_f32 v30, v10, v30, s22
	v_fma_f32 v31, v11, v31, s22
	v_exp_f32_e32 v33, v33
	v_fma_f32 v30, v10, v30, s24
	v_fma_f32 v31, v11, v31, s24
	s_nop 0
	v_fma_f32 v30, v10, v30, s26
	v_fma_f32 v31, v11, v31, s26
	s_nop 0
	v_mul_f32_e32 v10, v10, v30
	v_mul_f32_e32 v11, v11, v31
	v_mul_f32_e32 v30, v12, v12
	v_mul_f32_e32 v31, v13, v13
	v_mul_f32_e32 v10, v32, v10
	v_mul_f32_e32 v11, v33, v11
	v_mul_f32_e32 v30, s28, v30
	v_mul_f32_e32 v31, s28, v31
	v_mul_f32_e32 v32, v14, v10
	v_mul_f32_e32 v33, v15, v11
	v_fma_f32 v10, -v14, v10, v14
	v_fma_f32 v11, -v15, v11, v15
	v_exp_f32_e32 v30, v30
	v_cndmask_b32_e32 v14, v10, v32, vcc
	v_cmp_gt_f32_e32 vcc, 0, v15
	v_and_b32_e32 v10, 0x7fffffff, v12
	v_exp_f32_e32 v31, v31
	v_cndmask_b32_e32 v15, v11, v33, vcc
	v_and_b32_e32 v11, 0x7fffffff, v13
	v_fma_f32 v10, v10, s16, 1.0
	v_fma_f32 v11, v11, s16, 1.0
	v_cmp_gt_f32_e32 vcc, 0, v12
	v_rcp_f32_e32 v10, v10
	v_rcp_f32_e32 v11, v11
	s_nop 0
	v_fma_f32 v32, v10, s18, v20
	v_fma_f32 v33, v11, s18, v20
	s_nop 0
	v_fma_f32 v32, v10, v32, s22
	v_fma_f32 v33, v11, v33, s22
	s_nop 0
	v_fma_f32 v32, v10, v32, s24
	v_fma_f32 v33, v11, v33, s24
	s_nop 0
	v_fma_f32 v32, v10, v32, s26
	v_fma_f32 v33, v11, v33, s26
	s_nop 0
	v_mul_f32_e32 v10, v10, v32
	v_mul_f32_e32 v11, v11, v33
	v_mul_f32_e32 v32, v18, v18
	v_mul_f32_e32 v33, v19, v19
	v_mul_f32_e32 v10, v30, v10
	v_mul_f32_e32 v11, v31, v11
	v_mul_f32_e32 v32, s28, v32
	v_mul_f32_e32 v33, s28, v33
	v_mul_f32_e32 v30, v12, v10
	v_mul_f32_e32 v31, v13, v11
	v_fma_f32 v10, -v12, v10, v12
	v_fma_f32 v11, -v13, v11, v13
	v_exp_f32_e32 v32, v32
	v_cndmask_b32_e32 v12, v10, v30, vcc
	v_cmp_gt_f32_e32 vcc, 0, v13
	v_and_b32_e32 v10, 0x7fffffff, v18
	v_exp_f32_e32 v33, v33
	v_cndmask_b32_e32 v13, v11, v31, vcc
	v_and_b32_e32 v11, 0x7fffffff, v19
	v_fma_f32 v10, v10, s16, 1.0
	v_fma_f32 v11, v11, s16, 1.0
	v_cmp_gt_f32_e32 vcc, 0, v18
	v_rcp_f32_e32 v10, v10
	v_rcp_f32_e32 v11, v11
	s_nop 0
	v_fma_f32 v30, v10, s18, v20
	v_fma_f32 v31, v11, s18, v20
	s_nop 0
	v_fma_f32 v30, v10, v30, s22
	v_fma_f32 v31, v11, v31, s22
	s_nop 0
	v_fma_f32 v30, v10, v30, s24
	v_fma_f32 v31, v11, v31, s24
	s_nop 0
	v_fma_f32 v30, v10, v30, s26
	v_fma_f32 v31, v11, v31, s26
	s_nop 0
	v_mul_f32_e32 v10, v10, v30
	v_mul_f32_e32 v11, v11, v31
	v_mul_f32_e32 v30, v16, v16
	v_mul_f32_e32 v31, v17, v17
	v_mul_f32_e32 v10, v32, v10
	v_mul_f32_e32 v11, v33, v11
	s_nop 0
	v_mul_f32_e32 v32, v18, v10
	v_mul_f32_e32 v33, v19, v11
	v_fma_f32 v10, -v18, v10, v18
	v_fma_f32 v11, -v19, v11, v19
	s_nop 0
	v_cndmask_b32_e32 v18, v10, v32, vcc
	v_cmp_gt_f32_e32 vcc, 0, v19
	v_and_b32_e32 v10, 0x7fffffff, v16
	s_nop 0
	v_cndmask_b32_e32 v19, v11, v33, vcc
	v_and_b32_e32 v11, 0x7fffffff, v17
	v_fma_f32 v10, v10, s16, 1.0
	v_fma_f32 v11, v11, s16, 1.0
	v_cmp_gt_f32_e32 vcc, 0, v16
	v_rcp_f32_e32 v10, v10
	v_rcp_f32_e32 v11, v11
	s_nop 0
	v_fma_f32 v21, v11, s18, v20
	v_fma_f32 v20, v10, s18, v20
	s_nop 0
	v_fma_f32 v20, v10, v20, s22
	v_fma_f32 v21, v11, v21, s22
	s_nop 0
	v_fma_f32 v20, v10, v20, s24
	v_fma_f32 v21, v11, v21, s24
	s_nop 0
	v_fma_f32 v20, v10, v20, s26
	v_fma_f32 v21, v11, v21, s26
	s_nop 0
	v_mul_f32_e32 v10, v10, v20
	v_mul_f32_e32 v11, v11, v21
	v_mul_f32_e32 v20, s28, v30
	v_mul_f32_e32 v21, s28, v31
	s_nop 0
	v_exp_f32_e32 v20, v20
	v_exp_f32_e32 v21, v21
	s_nop 0
	v_mul_f32_e32 v10, v20, v10
	v_mul_f32_e32 v11, v21, v11
	s_nop 0
	v_mul_f32_e32 v20, v16, v10
	v_mul_f32_e32 v21, v17, v11
	v_fma_f32 v10, -v16, v10, v16
	v_fma_f32 v11, -v17, v11, v17
	s_nop 0
	v_cndmask_b32_e32 v16, v10, v20, vcc
	v_cmp_gt_f32_e32 vcc, 0, v17
	s_nop 1
	v_cndmask_b32_e32 v17, v11, v21, vcc
; __device__ __forceinline__ unsigned cvt_pk_bf16(float lo, float hi) { unsigned r; asm volatile("v_cvt_pk_bf16_f32 %0, %1, %2" : "=v"(r) : "v"(lo), "v"(hi)); return r; }
; __device__ __forceinline__ f32x2 gelu_pk(f32x2 v) {
;     const f32x2 av = __builtin_elementwise_abs(v), d = av * 0.2316418882f + 1.0f;
;     f32x2 t; t.x = __builtin_amdgcn_rcpf(d.x); t.y = __builtin_amdgcn_rcpf(d.y);
;     f32x2 q = t * 0.5307027145f + (-0.7265760135f); q = q * t + 0.7107068705f; q = q * t + (-0.142248368f); q = q * t + 0.127414796f; q = q * t;
;     const f32x2 s = (v * v) * (-0.72134752044f);
;     f32x2 e; e.x = __builtin_amdgcn_exp2f(s.x); e.y = __builtin_amdgcn_exp2f(s.y);
;     const f32x2 m = v * (q * e), r = v - m;
;     f32x2 o; o.x = v.x < 0.f ? m.x : r.x; o.y = v.y < 0.f ? m.y : r.y; return o;
;     __device__ __forceinline__ void operator()(const f32x4 (&acc)[2][2][4][2], const Unit& u, int wr, int wc, int fr, int fq) const {
;     ...
;             for (int m = 0; m < 4; ++m) { const int row = row0 + ai * HALF + m * 16; const float rsc = rsv[ai][m]; bf16_t* rowp = O + (size_t)row * ldc + col0;
; #pragma unroll
;                 for (int bj = 0; bj < 2; ++bj) { const i32x4 a0 = __builtin_bit_cast(i32x4, acc[ai][bj][m][0]), a1 = __builtin_bit_cast(i32x4, acc[ai][bj][m][1]);
;                     f32x4 v0 = (f32x4){(float)a0[0], (float)a0[1], (float)a0[2], (float)a0[3]} * rsc * cv[bj][0], v1 = (f32x4){(float)a1[0], (float)a1[1], (float)a1[2], (float)a1[3]} * rsc * cv[bj][1];
;                     if (act) { f32x2 a = gelu_pk((f32x2){v0[0], v0[1]}), b = gelu_pk((f32x2){v0[2], v0[3]}), c = gelu_pk((f32x2){v1[0], v1[1]}), d = gelu_pk((f32x2){v1[2], v1[3]});
;                         v0 = (f32x4){a.x, a.y, b.x, b.y}; v1 = (f32x4){c.x, c.y, d.x, d.y}; }
;                     u32x4 w; w.x = cvt_pk_bf16(v0[0], v0[1]); w.y = cvt_pk_bf16(v0[2], v0[3]); w.z = cvt_pk_bf16(v1[0], v1[1]); w.w = cvt_pk_bf16(v1[2], v1[3]);
.LBB0_367:
	v_lshlrev_b64 v[10:11], 15, v[172:173]
	v_lshl_add_u64 v[10:11], s[70:71], 0, v[10:11]
	v_lshl_add_u64 v[10:11], v[170:171], 1, v[10:11]
	s_mov_b32 s2, 0x580000
	v_cvt_f32_i32_e32 v7, v7
	v_cvt_f32_i32_e32 v9, v9
	v_cvt_f32_i32_e32 v8, v8
	v_cvt_f32_i32_e32 v6, v6
	v_cvt_pk_bf16_f32 v30, v14, v15
	v_cvt_pk_bf16_f32 v31, v12, v13
	v_cvt_pk_bf16_f32 v32, v18, v19
	v_cvt_pk_bf16_f32 v33, v16, v17
	v_add_co_u32_e32 v12, vcc, s2, v10
	v_cvt_f32_i32_e32 v15, v3
	v_cvt_f32_i32_e32 v17, v5
	v_cvt_f32_i32_e32 v16, v4
	v_cvt_f32_i32_e32 v14, v2
	v_addc_co_u32_e32 v13, vcc, 0, v11, vcc
	v_mov_b32_e32 v169, v168
	global_store_dwordx4 v[12:13], v[30:33], off
	v_mov_b32_e32 v12, v168
	v_mov_b32_e32 v13, v168
	v_mul_f32_e32 v8, v12, v8
	v_mul_f32_e32 v9, v13, v9
	v_mul_f32_e32 v6, v168, v6
	v_mul_f32_e32 v7, v169, v7
	v_mul_f32_e32 v2, v28, v8
	v_mul_f32_e32 v3, v29, v9
	v_mul_f32_e32 v4, v26, v6
	v_mul_f32_e32 v5, v27, v7
	v_mul_f32_e32 v6, v12, v16
	v_mul_f32_e32 v7, v13, v17
	v_mul_f32_e32 v8, v168, v14
	v_mul_f32_e32 v9, v169, v15
	v_mul_f32_e32 v6, v24, v6
	v_mul_f32_e32 v7, v25, v7
	s_and_b64 vcc, exec, s[4:5]
	v_mul_f32_e32 v8, v22, v8
	v_mul_f32_e32 v9, v23, v9
	s_cbranch_vccnz .LBB0_369
	v_and_b32_e32 v13, 0x7fffffff, v5
	v_and_b32_e32 v12, 0x7fffffff, v4
	v_fma_f32 v12, v12, s16, 1.0
	v_fma_f32 v13, v13, s16, 1.0
	v_mov_b64_e32 v[14:15], s[20:21]
	v_rcp_f32_e32 v12, v12
	v_rcp_f32_e32 v13, v13
	v_mul_f32_e32 v18, v4, v4
	v_mul_f32_e32 v19, v5, v5
	v_cmp_gt_f32_e32 vcc, 0, v4
	v_mul_f32_e32 v18, s28, v18
	v_mul_f32_e32 v19, s28, v19
	v_fma_f32 v16, v12, s18, v14
	v_fma_f32 v17, v13, s18, v14
	v_exp_f32_e32 v18, v18
	v_fma_f32 v16, v12, v16, s22
	v_fma_f32 v17, v13, v17, s22
	v_exp_f32_e32 v19, v19
	v_fma_f32 v16, v12, v16, s24
	v_fma_f32 v17, v13, v17, s24
	s_nop 0
	v_fma_f32 v16, v12, v16, s26
	v_fma_f32 v17, v13, v17, s26
	s_nop 0
	v_mul_f32_e32 v12, v12, v16
	v_mul_f32_e32 v13, v13, v17
	v_mul_f32_e32 v16, v2, v2
	v_mul_f32_e32 v17, v3, v3
	v_mul_f32_e32 v12, v18, v12
	v_mul_f32_e32 v13, v19, v13
	v_mul_f32_e32 v16, s28, v16
	v_mul_f32_e32 v17, s28, v17
	v_mul_f32_e32 v18, v4, v12
	v_mul_f32_e32 v19, v5, v13
	v_fma_f32 v12, -v4, v12, v4
	v_fma_f32 v13, -v5, v13, v5
	v_exp_f32_e32 v16, v16
	v_cndmask_b32_e32 v4, v12, v18, vcc
	v_cmp_gt_f32_e32 vcc, 0, v5
	v_and_b32_e32 v12, 0x7fffffff, v2
	v_exp_f32_e32 v17, v17
	v_cndmask_b32_e32 v5, v13, v19, vcc
	v_and_b32_e32 v13, 0x7fffffff, v3
	v_fma_f32 v12, v12, s16, 1.0
	v_fma_f32 v13, v13, s16, 1.0
	v_cmp_gt_f32_e32 vcc, 0, v2
	v_rcp_f32_e32 v12, v12
	v_rcp_f32_e32 v13, v13
	s_nop 0
	v_fma_f32 v18, v12, s18, v14
	v_fma_f32 v19, v13, s18, v14
	s_nop 0
	v_fma_f32 v18, v12, v18, s22
	v_fma_f32 v19, v13, v19, s22
	s_nop 0
	v_fma_f32 v18, v12, v18, s24
	v_fma_f32 v19, v13, v19, s24
	s_nop 0
	v_fma_f32 v18, v12, v18, s26
	v_fma_f32 v19, v13, v19, s26
	s_nop 0
	v_mul_f32_e32 v12, v12, v18
	v_mul_f32_e32 v13, v13, v19
	v_mul_f32_e32 v18, v8, v8
	v_mul_f32_e32 v19, v9, v9
	v_mul_f32_e32 v12, v16, v12
	v_mul_f32_e32 v13, v17, v13
	v_mul_f32_e32 v18, s28, v18
	v_mul_f32_e32 v19, s28, v19
	v_mul_f32_e32 v16, v2, v12
	v_mul_f32_e32 v17, v3, v13
	v_fma_f32 v12, -v2, v12, v2
	v_fma_f32 v13, -v3, v13, v3
	v_exp_f32_e32 v18, v18
	v_cndmask_b32_e32 v2, v12, v16, vcc
	v_cmp_gt_f32_e32 vcc, 0, v3
	v_and_b32_e32 v12, 0x7fffffff, v8
	v_exp_f32_e32 v19, v19
	v_cndmask_b32_e32 v3, v13, v17, vcc
	v_and_b32_e32 v13, 0x7fffffff, v9
	v_fma_f32 v12, v12, s16, 1.0
	v_fma_f32 v13, v13, s16, 1.0
	v_cmp_gt_f32_e32 vcc, 0, v8
	v_rcp_f32_e32 v12, v12
	v_rcp_f32_e32 v13, v13
	s_nop 0
	v_fma_f32 v16, v12, s18, v14
	v_fma_f32 v17, v13, s18, v14
	s_nop 0
	v_fma_f32 v16, v12, v16, s22
	v_fma_f32 v17, v13, v17, s22
	s_nop 0
	v_fma_f32 v16, v12, v16, s24
	v_fma_f32 v17, v13, v17, s24
	s_nop 0
	v_fma_f32 v16, v12, v16, s26
	v_fma_f32 v17, v13, v17, s26
	s_nop 0
	v_mul_f32_e32 v12, v12, v16
	v_mul_f32_e32 v13, v13, v17
	v_mul_f32_e32 v16, v6, v6
	v_mul_f32_e32 v17, v7, v7
	v_mul_f32_e32 v12, v18, v12
	v_mul_f32_e32 v13, v19, v13
	s_nop 0
	v_mul_f32_e32 v18, v8, v12
	v_mul_f32_e32 v19, v9, v13
	v_fma_f32 v12, -v8, v12, v8
	v_fma_f32 v13, -v9, v13, v9
	s_nop 0
	v_cndmask_b32_e32 v8, v12, v18, vcc
	v_cmp_gt_f32_e32 vcc, 0, v9
	v_and_b32_e32 v12, 0x7fffffff, v6
	s_nop 0
	v_cndmask_b32_e32 v9, v13, v19, vcc
	v_and_b32_e32 v13, 0x7fffffff, v7
	v_fma_f32 v12, v12, s16, 1.0
	v_fma_f32 v13, v13, s16, 1.0
	v_cmp_gt_f32_e32 vcc, 0, v6
	v_rcp_f32_e32 v12, v12
	v_rcp_f32_e32 v13, v13
	s_nop 0
	v_fma_f32 v15, v13, s18, v14
	v_fma_f32 v14, v12, s18, v14
	s_nop 0
	v_fma_f32 v14, v12, v14, s22
	v_fma_f32 v15, v13, v15, s22
	s_nop 0
	v_fma_f32 v14, v12, v14, s24
	v_fma_f32 v15, v13, v15, s24
	s_nop 0
	v_fma_f32 v14, v12, v14, s26
	v_fma_f32 v15, v13, v15, s26
	s_nop 0
	v_mul_f32_e32 v12, v12, v14
	v_mul_f32_e32 v13, v13, v15
	v_mul_f32_e32 v14, s28, v16
	v_mul_f32_e32 v15, s28, v17
	s_nop 0
	v_exp_f32_e32 v14, v14
	v_exp_f32_e32 v15, v15
	s_nop 0
	v_mul_f32_e32 v12, v14, v12
	v_mul_f32_e32 v13, v15, v13
	s_nop 0
	v_mul_f32_e32 v14, v6, v12
	v_mul_f32_e32 v15, v7, v13
	v_fma_f32 v12, -v6, v12, v6
	v_fma_f32 v13, -v7, v13, v7
	s_nop 0
	v_cndmask_b32_e32 v6, v12, v14, vcc
	v_cmp_gt_f32_e32 vcc, 0, v7
	s_nop 1
	v_cndmask_b32_e32 v7, v13, v15, vcc
